# prologue Wc-fold items: 64 weight-row loads in flight per wave (two batches) instead of 2 per loop trip with a full drain
# speedup vs baseline: 1.0081x; 1.0081x over previous
; #define GAS __attribute__((address_space(1)))
; #define LDS_WAIT() asm volatile("s_waitcnt lgkmcnt(0)" ::: "memory")
; __device__ __forceinline__ void p0_prologue(Frame& F) {
;     ...
;         if (r < NI_BD) {
;             const int nb = r & 15, cb = (r >> 4) & 15, part = (r >> 8) & 1, g = r >> 9; const int n = nb * 64 + F.lane, c0 = cb * 8;
;             const GAS float* wsrc = (const GAS float*)inp(F, I_WOUT) + (size_t)(512 + 128 * g) * 1024 + n;
;             { float s0, c0_, s1, c1_; sincospif((float)F.lane * (1.f / 64.f), &s0, &c0_); sincospif((float)(F.lane + 64) * (1.f / 64.f), &s1, &c1_);
;               scr[F.lane] = part ? s0 : c0_; scr[F.lane + 64] = part ? s1 : c1_; LDS_WAIT(); asm volatile("" ::: "memory"); }
;             float acc8[8];
; #pragma unroll
;             for (int j = 0; j < 8; ++j) acc8[j] = 0.f;
; #pragma unroll 2
;             for (int m = 0; m < 128; ++m) { const float wv = wsrc[(size_t)m * 1024];
; #pragma unroll
;                 for (int j = 0; j < 8; ++j) acc8[j] += scr[(m * (c0 + j)) & 127] * wv; }
;             LDS_WAIT(); asm volatile("" ::: "memory");
.Lbd_pipe:
	s_mov_b64 s[0:1], 0x2000
	global_load_dword v120, v[4:5], off offset:-4096
	global_load_dword v122, v[4:5], off
	v_lshl_add_u64 v[4:5], v[4:5], 0, s[0:1]
	global_load_dword v124, v[4:5], off offset:-4096
	global_load_dword v126, v[4:5], off
	v_lshl_add_u64 v[4:5], v[4:5], 0, s[0:1]
	global_load_dword v128, v[4:5], off offset:-4096
	global_load_dword v130, v[4:5], off
	v_lshl_add_u64 v[4:5], v[4:5], 0, s[0:1]
	global_load_dword v132, v[4:5], off offset:-4096
	global_load_dword v134, v[4:5], off
	v_lshl_add_u64 v[4:5], v[4:5], 0, s[0:1]
	global_load_dword v136, v[4:5], off offset:-4096
	global_load_dword v138, v[4:5], off
	v_lshl_add_u64 v[4:5], v[4:5], 0, s[0:1]
	global_load_dword v140, v[4:5], off offset:-4096
	global_load_dword v142, v[4:5], off
	v_lshl_add_u64 v[4:5], v[4:5], 0, s[0:1]
	global_load_dword v144, v[4:5], off offset:-4096
	global_load_dword v146, v[4:5], off
	v_lshl_add_u64 v[4:5], v[4:5], 0, s[0:1]
	global_load_dword v148, v[4:5], off offset:-4096
	global_load_dword v150, v[4:5], off
	v_lshl_add_u64 v[4:5], v[4:5], 0, s[0:1]
	global_load_dword v152, v[4:5], off offset:-4096
	global_load_dword v154, v[4:5], off
	v_lshl_add_u64 v[4:5], v[4:5], 0, s[0:1]
	global_load_dword v156, v[4:5], off offset:-4096
	global_load_dword v158, v[4:5], off
	v_lshl_add_u64 v[4:5], v[4:5], 0, s[0:1]
	global_load_dword v160, v[4:5], off offset:-4096
	global_load_dword v162, v[4:5], off
	v_lshl_add_u64 v[4:5], v[4:5], 0, s[0:1]
	global_load_dword v164, v[4:5], off offset:-4096
	global_load_dword v166, v[4:5], off
	v_lshl_add_u64 v[4:5], v[4:5], 0, s[0:1]
	global_load_dword v168, v[4:5], off offset:-4096
	global_load_dword v170, v[4:5], off
	v_lshl_add_u64 v[4:5], v[4:5], 0, s[0:1]
	global_load_dword v172, v[4:5], off offset:-4096
	global_load_dword v174, v[4:5], off
	v_lshl_add_u64 v[4:5], v[4:5], 0, s[0:1]
	global_load_dword v176, v[4:5], off offset:-4096
	global_load_dword v178, v[4:5], off
	v_lshl_add_u64 v[4:5], v[4:5], 0, s[0:1]
	global_load_dword v180, v[4:5], off offset:-4096
	global_load_dword v182, v[4:5], off
	v_lshl_add_u64 v[4:5], v[4:5], 0, s[0:1]
	global_load_dword v184, v[4:5], off offset:-4096
	global_load_dword v186, v[4:5], off
	v_lshl_add_u64 v[4:5], v[4:5], 0, s[0:1]
	global_load_dword v188, v[4:5], off offset:-4096
	global_load_dword v190, v[4:5], off
	v_lshl_add_u64 v[4:5], v[4:5], 0, s[0:1]
	global_load_dword v192, v[4:5], off offset:-4096
	global_load_dword v194, v[4:5], off
	v_lshl_add_u64 v[4:5], v[4:5], 0, s[0:1]
	global_load_dword v196, v[4:5], off offset:-4096
	global_load_dword v198, v[4:5], off
	v_lshl_add_u64 v[4:5], v[4:5], 0, s[0:1]
	global_load_dword v200, v[4:5], off offset:-4096
	global_load_dword v202, v[4:5], off
	v_lshl_add_u64 v[4:5], v[4:5], 0, s[0:1]
	global_load_dword v204, v[4:5], off offset:-4096
	global_load_dword v206, v[4:5], off
	v_lshl_add_u64 v[4:5], v[4:5], 0, s[0:1]
	global_load_dword v208, v[4:5], off offset:-4096
	global_load_dword v210, v[4:5], off
	v_lshl_add_u64 v[4:5], v[4:5], 0, s[0:1]
	global_load_dword v212, v[4:5], off offset:-4096
	global_load_dword v214, v[4:5], off
	v_lshl_add_u64 v[4:5], v[4:5], 0, s[0:1]
	global_load_dword v216, v[4:5], off offset:-4096
	global_load_dword v218, v[4:5], off
	v_lshl_add_u64 v[4:5], v[4:5], 0, s[0:1]
	global_load_dword v220, v[4:5], off offset:-4096
	global_load_dword v222, v[4:5], off
	v_lshl_add_u64 v[4:5], v[4:5], 0, s[0:1]
	global_load_dword v224, v[4:5], off offset:-4096
	global_load_dword v226, v[4:5], off
	v_lshl_add_u64 v[4:5], v[4:5], 0, s[0:1]
	global_load_dword v228, v[4:5], off offset:-4096
	global_load_dword v230, v[4:5], off
	v_lshl_add_u64 v[4:5], v[4:5], 0, s[0:1]
	global_load_dword v232, v[4:5], off offset:-4096
	global_load_dword v234, v[4:5], off
	v_lshl_add_u64 v[4:5], v[4:5], 0, s[0:1]
	global_load_dword v236, v[4:5], off offset:-4096
	global_load_dword v238, v[4:5], off
	v_lshl_add_u64 v[4:5], v[4:5], 0, s[0:1]
	global_load_dword v240, v[4:5], off offset:-4096
	global_load_dword v242, v[4:5], off
	v_lshl_add_u64 v[4:5], v[4:5], 0, s[0:1]
	global_load_dword v244, v[4:5], off offset:-4096
	global_load_dword v246, v[4:5], off
	v_lshl_add_u64 v[4:5], v[4:5], 0, s[0:1]
	s_and_b32 s20, s42, 0x70
	s_add_i32 s30, s21, -1
	s_add_i32 s31, s10, -2
	s_add_i32 s97, s18, -3
	s_add_i32 s3, s4, -4
	s_add_i32 s63, s91, -5
	s_add_i32 s79, s13, -6
	s_and_b32 s81, vcc_lo, 0x7e
	s_add_i32 s70, s44, s42
	s_add_i32 s76, s44, s21
	s_add_i32 s19, s44, s10
	s_add_i32 s69, s44, s18
	s_add_i32 s53, s44, s4
	s_add_i32 s94, s44, s91
	s_add_i32 s88, s44, s13
	s_add_i32 s45, s65, vcc_lo
	s_lshl_b32 s0, s20, 2
	s_and_b32 s1, s30, 0x7e
	s_and_b32 s20, s31, 0x7c
	s_and_b32 s30, s97, 0x7e
	s_and_b32 s3, s3, 0x78
	s_and_b32 s31, s63, 0x7e
	s_and_b32 s63, s79, 0x7c
	s_lshl_b32 s79, s81, 2
	s_and_b32 s70, s70, 0x78
	s_and_b32 s76, s76, 0x7f
	s_and_b32 s19, s19, 0x7e
	s_and_b32 s69, s69, 0x7f
	s_and_b32 s53, s53, 0x7c
	s_and_b32 s81, s94, 0x7f
	s_and_b32 s88, s88, 0x7e
	s_and_b32 s45, s45, 0x7f
	s_add_i32 s0, s49, s0
	s_lshl_b32 s1, s1, 2
	s_lshl_b32 s20, s20, 2
	s_lshl_b32 s30, s30, 2
	s_lshl_b32 s3, s3, 2
	s_lshl_b32 s31, s31, 2
	s_lshl_b32 s63, s63, 2
	s_add_i32 s79, s49, s79
	s_lshl_b32 s70, s70, 2
	s_lshl_b32 s76, s76, 2
	s_lshl_b32 s19, s19, 2
	s_lshl_b32 s69, s69, 2
	s_lshl_b32 s53, s53, 2
	s_lshl_b32 s81, s81, 2
	s_lshl_b32 s88, s88, 2
	s_lshl_b32 s45, s45, 2
	v_mov_b32_e32 v13, s0
	s_add_i32 s0, s49, s1
	s_add_i32 s1, s49, s20
	s_add_i32 s20, s49, s30
	s_add_i32 s3, s49, s3
	s_add_i32 s30, s49, s31
	s_add_i32 s31, s49, s63
	v_mov_b32_e32 v15, s79
	s_add_i32 s63, s49, s70
	s_add_i32 s70, s49, s76
	s_add_i32 s19, s49, s19
	s_add_i32 s69, s49, s69
	s_add_i32 s53, s49, s53
	s_add_i32 s76, s49, s81
	s_add_i32 s79, s49, s88
	s_add_i32 s45, s49, s45
	v_mov_b32_e32 v19, s1
	v_mov_b32_e32 v20, s20
	v_mov_b32_e32 v24, s3
	v_mov_b32_e32 v25, s30
	v_mov_b32_e32 v26, s31
	v_mov_b32_e32 v27, s63
	v_mov_b32_e32 v28, s70
	v_mov_b32_e32 v29, s19
	v_mov_b32_e32 v30, s69
	v_mov_b32_e32 v31, s53
	v_mov_b32_e32 v32, s76
	v_mov_b32_e32 v33, s79
	v_mov_b32_e32 v17, s0
	v_mov_b32_e32 v40, s45
	ds_read_b32 v18, v13
	ds_read_b32 v21, v15
	ds_read_b32 v22, v17
	ds_read_b32 v19, v19
	ds_read_b32 v23, v20
	ds_read_b32 v24, v24
	ds_read_b32 v20, v25
	ds_read_b32 v25, v26
	ds_read_b32 v26, v27
	ds_read_b32 v28, v28
	ds_read_b32 v27, v29
	ds_read_b32 v29, v30
	ds_read_b32 v30, v31
	ds_read_b32 v32, v32
	ds_read_b32 v31, v33
	ds_read_b32 v33, v40
	s_add_i32 vcc_hi, vcc_hi, 2
	s_add_i32 s21, s21, s11
	s_add_i32 s10, s10, s12
	s_add_i32 s18, s18, s14
	s_add_i32 s4, s4, s15
	s_add_i32 s91, s91, s16
	s_add_i32 s13, s13, s17
	s_add_i32 vcc_lo, vcc_lo, s90
	s_add_i32 s42, s42, s5
	s_waitcnt vmcnt(62) lgkmcnt(0)
; __device__ __forceinline__ void p0_prologue(Frame& F) {
;     ...
; #pragma unroll 2
;             for (int m = 0; m < 128; ++m) { const float wv = wsrc[(size_t)m * 1024];
; #pragma unroll
;                 for (int j = 0; j < 8; ++j) acc8[j] += scr[(m * (c0 + j)) & 127] * wv; }
	v_pk_fma_f32 v[8:9], v[120:121], v[18:19], v[8:9] op_sel_hi:[0,1,1]
	v_pk_fma_f32 v[2:3], v[120:121], v[22:23], v[2:3] op_sel_hi:[0,1,1]
	v_pk_fma_f32 v[10:11], v[120:121], v[24:25], v[10:11] op_sel_hi:[0,1,1]
	v_pk_fma_f32 v[6:7], v[120:121], v[20:21], v[6:7] op_sel_hi:[0,1,1]
	v_pk_fma_f32 v[8:9], v[122:123], v[26:27], v[8:9] op_sel_hi:[0,1,1]
	v_pk_fma_f32 v[2:3], v[122:123], v[28:29], v[2:3] op_sel_hi:[0,1,1]
	v_pk_fma_f32 v[10:11], v[122:123], v[30:31], v[10:11] op_sel_hi:[0,1,1]
	v_pk_fma_f32 v[6:7], v[122:123], v[32:33], v[6:7] op_sel_hi:[0,1,1]
	s_and_b32 s20, s42, 0x70
	s_add_i32 s30, s21, -1
	s_add_i32 s31, s10, -2
	s_add_i32 s97, s18, -3
	s_add_i32 s3, s4, -4
	s_add_i32 s63, s91, -5
	s_add_i32 s79, s13, -6
	s_and_b32 s81, vcc_lo, 0x7e
	s_add_i32 s70, s44, s42
	s_add_i32 s76, s44, s21
	s_add_i32 s19, s44, s10
	s_add_i32 s69, s44, s18
	s_add_i32 s53, s44, s4
	s_add_i32 s94, s44, s91
	s_add_i32 s88, s44, s13
	s_add_i32 s45, s65, vcc_lo
	s_lshl_b32 s0, s20, 2
	s_and_b32 s1, s30, 0x7e
	s_and_b32 s20, s31, 0x7c
	s_and_b32 s30, s97, 0x7e
	s_and_b32 s3, s3, 0x78
	s_and_b32 s31, s63, 0x7e
	s_and_b32 s63, s79, 0x7c
	s_lshl_b32 s79, s81, 2
	s_and_b32 s70, s70, 0x78
	s_and_b32 s76, s76, 0x7f
	s_and_b32 s19, s19, 0x7e
	s_and_b32 s69, s69, 0x7f
	s_and_b32 s53, s53, 0x7c
	s_and_b32 s81, s94, 0x7f
	s_and_b32 s88, s88, 0x7e
	s_and_b32 s45, s45, 0x7f
	s_add_i32 s0, s49, s0
	s_lshl_b32 s1, s1, 2
	s_lshl_b32 s20, s20, 2
	s_lshl_b32 s30, s30, 2
	s_lshl_b32 s3, s3, 2
	s_lshl_b32 s31, s31, 2
	s_lshl_b32 s63, s63, 2
	s_add_i32 s79, s49, s79
	s_lshl_b32 s70, s70, 2
	s_lshl_b32 s76, s76, 2
	s_lshl_b32 s19, s19, 2
	s_lshl_b32 s69, s69, 2
	s_lshl_b32 s53, s53, 2
	s_lshl_b32 s81, s81, 2
	s_lshl_b32 s88, s88, 2
	s_lshl_b32 s45, s45, 2
	v_mov_b32_e32 v13, s0
	s_add_i32 s0, s49, s1
	s_add_i32 s1, s49, s20
	s_add_i32 s20, s49, s30
	s_add_i32 s3, s49, s3
	s_add_i32 s30, s49, s31
	s_add_i32 s31, s49, s63
	v_mov_b32_e32 v15, s79
	s_add_i32 s63, s49, s70
	s_add_i32 s70, s49, s76
	s_add_i32 s19, s49, s19
	s_add_i32 s69, s49, s69
	s_add_i32 s53, s49, s53
	s_add_i32 s76, s49, s81
	s_add_i32 s79, s49, s88
	s_add_i32 s45, s49, s45
	v_mov_b32_e32 v19, s1
	v_mov_b32_e32 v20, s20
	v_mov_b32_e32 v24, s3
	v_mov_b32_e32 v25, s30
	v_mov_b32_e32 v26, s31
	v_mov_b32_e32 v27, s63
	v_mov_b32_e32 v28, s70
	v_mov_b32_e32 v29, s19
	v_mov_b32_e32 v30, s69
	v_mov_b32_e32 v31, s53
	v_mov_b32_e32 v32, s76
	v_mov_b32_e32 v33, s79
	v_mov_b32_e32 v17, s0
	v_mov_b32_e32 v40, s45
	ds_read_b32 v18, v13
	ds_read_b32 v21, v15
	ds_read_b32 v22, v17
	ds_read_b32 v19, v19
	ds_read_b32 v23, v20
	ds_read_b32 v24, v24
	ds_read_b32 v20, v25
	ds_read_b32 v25, v26
	ds_read_b32 v26, v27
	ds_read_b32 v28, v28
	ds_read_b32 v27, v29
	ds_read_b32 v29, v30
	ds_read_b32 v30, v31
	ds_read_b32 v32, v32
	ds_read_b32 v31, v33
	ds_read_b32 v33, v40
	s_add_i32 vcc_hi, vcc_hi, 2
	s_add_i32 s21, s21, s11
	s_add_i32 s10, s10, s12
	s_add_i32 s18, s18, s14
	s_add_i32 s4, s4, s15
	s_add_i32 s91, s91, s16
	s_add_i32 s13, s13, s17
	s_add_i32 vcc_lo, vcc_lo, s90
	s_add_i32 s42, s42, s5
	s_waitcnt vmcnt(60) lgkmcnt(0)
	v_pk_fma_f32 v[8:9], v[124:125], v[18:19], v[8:9] op_sel_hi:[0,1,1]
	v_pk_fma_f32 v[2:3], v[124:125], v[22:23], v[2:3] op_sel_hi:[0,1,1]
	v_pk_fma_f32 v[10:11], v[124:125], v[24:25], v[10:11] op_sel_hi:[0,1,1]
	v_pk_fma_f32 v[6:7], v[124:125], v[20:21], v[6:7] op_sel_hi:[0,1,1]
	v_pk_fma_f32 v[8:9], v[126:127], v[26:27], v[8:9] op_sel_hi:[0,1,1]
	v_pk_fma_f32 v[2:3], v[126:127], v[28:29], v[2:3] op_sel_hi:[0,1,1]
	v_pk_fma_f32 v[10:11], v[126:127], v[30:31], v[10:11] op_sel_hi:[0,1,1]
	v_pk_fma_f32 v[6:7], v[126:127], v[32:33], v[6:7] op_sel_hi:[0,1,1]
	s_and_b32 s20, s42, 0x70
	s_add_i32 s30, s21, -1
	s_add_i32 s31, s10, -2
	s_add_i32 s97, s18, -3
	s_add_i32 s3, s4, -4
	s_add_i32 s63, s91, -5
	s_add_i32 s79, s13, -6
	s_and_b32 s81, vcc_lo, 0x7e
	s_add_i32 s70, s44, s42
	s_add_i32 s76, s44, s21
	s_add_i32 s19, s44, s10
	s_add_i32 s69, s44, s18
	s_add_i32 s53, s44, s4
	s_add_i32 s94, s44, s91
	s_add_i32 s88, s44, s13
	s_add_i32 s45, s65, vcc_lo
	s_lshl_b32 s0, s20, 2
	s_and_b32 s1, s30, 0x7e
	s_and_b32 s20, s31, 0x7c
	s_and_b32 s30, s97, 0x7e
	s_and_b32 s3, s3, 0x78
	s_and_b32 s31, s63, 0x7e
	s_and_b32 s63, s79, 0x7c
	s_lshl_b32 s79, s81, 2
	s_and_b32 s70, s70, 0x78
	s_and_b32 s76, s76, 0x7f
	s_and_b32 s19, s19, 0x7e
	s_and_b32 s69, s69, 0x7f
	s_and_b32 s53, s53, 0x7c
	s_and_b32 s81, s94, 0x7f
	s_and_b32 s88, s88, 0x7e
	s_and_b32 s45, s45, 0x7f
	s_add_i32 s0, s49, s0
	s_lshl_b32 s1, s1, 2
	s_lshl_b32 s20, s20, 2
	s_lshl_b32 s30, s30, 2
	s_lshl_b32 s3, s3, 2
	s_lshl_b32 s31, s31, 2
	s_lshl_b32 s63, s63, 2
	s_add_i32 s79, s49, s79
	s_lshl_b32 s70, s70, 2
	s_lshl_b32 s76, s76, 2
	s_lshl_b32 s19, s19, 2
	s_lshl_b32 s69, s69, 2
	s_lshl_b32 s53, s53, 2
	s_lshl_b32 s81, s81, 2
	s_lshl_b32 s88, s88, 2
	s_lshl_b32 s45, s45, 2
	v_mov_b32_e32 v13, s0
	s_add_i32 s0, s49, s1
	s_add_i32 s1, s49, s20
	s_add_i32 s20, s49, s30
	s_add_i32 s3, s49, s3
	s_add_i32 s30, s49, s31
	s_add_i32 s31, s49, s63
	v_mov_b32_e32 v15, s79
	s_add_i32 s63, s49, s70
	s_add_i32 s70, s49, s76
	s_add_i32 s19, s49, s19
	s_add_i32 s69, s49, s69
	s_add_i32 s53, s49, s53
	s_add_i32 s76, s49, s81
	s_add_i32 s79, s49, s88
	s_add_i32 s45, s49, s45
	v_mov_b32_e32 v19, s1
	v_mov_b32_e32 v20, s20
	v_mov_b32_e32 v24, s3
	v_mov_b32_e32 v25, s30
	v_mov_b32_e32 v26, s31
	v_mov_b32_e32 v27, s63
	v_mov_b32_e32 v28, s70
	v_mov_b32_e32 v29, s19
	v_mov_b32_e32 v30, s69
	v_mov_b32_e32 v31, s53
	v_mov_b32_e32 v32, s76
	v_mov_b32_e32 v33, s79
	v_mov_b32_e32 v17, s0
	v_mov_b32_e32 v40, s45
	ds_read_b32 v18, v13
	ds_read_b32 v21, v15
	ds_read_b32 v22, v17
	ds_read_b32 v19, v19
	ds_read_b32 v23, v20
	ds_read_b32 v24, v24
	ds_read_b32 v20, v25
	ds_read_b32 v25, v26
	ds_read_b32 v26, v27
	ds_read_b32 v28, v28
	ds_read_b32 v27, v29
	ds_read_b32 v29, v30
	ds_read_b32 v30, v31
	ds_read_b32 v32, v32
	ds_read_b32 v31, v33
	ds_read_b32 v33, v40
	s_add_i32 vcc_hi, vcc_hi, 2
	s_add_i32 s21, s21, s11
	s_add_i32 s10, s10, s12
	s_add_i32 s18, s18, s14
	s_add_i32 s4, s4, s15
	s_add_i32 s91, s91, s16
	s_add_i32 s13, s13, s17
	s_add_i32 vcc_lo, vcc_lo, s90
	s_add_i32 s42, s42, s5
	s_waitcnt vmcnt(58) lgkmcnt(0)
; __device__ __forceinline__ void p0_prologue(Frame& F) {
;     ...
; #pragma unroll 2
;             for (int m = 0; m < 128; ++m) { const float wv = wsrc[(size_t)m * 1024];
; #pragma unroll
;                 for (int j = 0; j < 8; ++j) acc8[j] += scr[(m * (c0 + j)) & 127] * wv; }
	v_pk_fma_f32 v[8:9], v[128:129], v[18:19], v[8:9] op_sel_hi:[0,1,1]
	v_pk_fma_f32 v[2:3], v[128:129], v[22:23], v[2:3] op_sel_hi:[0,1,1]
	v_pk_fma_f32 v[10:11], v[128:129], v[24:25], v[10:11] op_sel_hi:[0,1,1]
	v_pk_fma_f32 v[6:7], v[128:129], v[20:21], v[6:7] op_sel_hi:[0,1,1]
	v_pk_fma_f32 v[8:9], v[130:131], v[26:27], v[8:9] op_sel_hi:[0,1,1]
	v_pk_fma_f32 v[2:3], v[130:131], v[28:29], v[2:3] op_sel_hi:[0,1,1]
	v_pk_fma_f32 v[10:11], v[130:131], v[30:31], v[10:11] op_sel_hi:[0,1,1]
	v_pk_fma_f32 v[6:7], v[130:131], v[32:33], v[6:7] op_sel_hi:[0,1,1]
	s_and_b32 s20, s42, 0x70
	s_add_i32 s30, s21, -1
	s_add_i32 s31, s10, -2
	s_add_i32 s97, s18, -3
	s_add_i32 s3, s4, -4
	s_add_i32 s63, s91, -5
	s_add_i32 s79, s13, -6
	s_and_b32 s81, vcc_lo, 0x7e
	s_add_i32 s70, s44, s42
	s_add_i32 s76, s44, s21
	s_add_i32 s19, s44, s10
	s_add_i32 s69, s44, s18
	s_add_i32 s53, s44, s4
	s_add_i32 s94, s44, s91
	s_add_i32 s88, s44, s13
	s_add_i32 s45, s65, vcc_lo
	s_lshl_b32 s0, s20, 2
	s_and_b32 s1, s30, 0x7e
	s_and_b32 s20, s31, 0x7c
	s_and_b32 s30, s97, 0x7e
	s_and_b32 s3, s3, 0x78
	s_and_b32 s31, s63, 0x7e
	s_and_b32 s63, s79, 0x7c
	s_lshl_b32 s79, s81, 2
	s_and_b32 s70, s70, 0x78
	s_and_b32 s76, s76, 0x7f
	s_and_b32 s19, s19, 0x7e
	s_and_b32 s69, s69, 0x7f
	s_and_b32 s53, s53, 0x7c
	s_and_b32 s81, s94, 0x7f
	s_and_b32 s88, s88, 0x7e
	s_and_b32 s45, s45, 0x7f
	s_add_i32 s0, s49, s0
	s_lshl_b32 s1, s1, 2
	s_lshl_b32 s20, s20, 2
	s_lshl_b32 s30, s30, 2
	s_lshl_b32 s3, s3, 2
	s_lshl_b32 s31, s31, 2
	s_lshl_b32 s63, s63, 2
	s_add_i32 s79, s49, s79
	s_lshl_b32 s70, s70, 2
	s_lshl_b32 s76, s76, 2
	s_lshl_b32 s19, s19, 2
	s_lshl_b32 s69, s69, 2
	s_lshl_b32 s53, s53, 2
	s_lshl_b32 s81, s81, 2
	s_lshl_b32 s88, s88, 2
	s_lshl_b32 s45, s45, 2
	v_mov_b32_e32 v13, s0
	s_add_i32 s0, s49, s1
	s_add_i32 s1, s49, s20
	s_add_i32 s20, s49, s30
	s_add_i32 s3, s49, s3
	s_add_i32 s30, s49, s31
	s_add_i32 s31, s49, s63
	v_mov_b32_e32 v15, s79
	s_add_i32 s63, s49, s70
	s_add_i32 s70, s49, s76
	s_add_i32 s19, s49, s19
	s_add_i32 s69, s49, s69
	s_add_i32 s53, s49, s53
	s_add_i32 s76, s49, s81
	s_add_i32 s79, s49, s88
	s_add_i32 s45, s49, s45
	v_mov_b32_e32 v19, s1
	v_mov_b32_e32 v20, s20
	v_mov_b32_e32 v24, s3
	v_mov_b32_e32 v25, s30
	v_mov_b32_e32 v26, s31
	v_mov_b32_e32 v27, s63
	v_mov_b32_e32 v28, s70
	v_mov_b32_e32 v29, s19
	v_mov_b32_e32 v30, s69
	v_mov_b32_e32 v31, s53
	v_mov_b32_e32 v32, s76
	v_mov_b32_e32 v33, s79
	v_mov_b32_e32 v17, s0
	v_mov_b32_e32 v40, s45
	ds_read_b32 v18, v13
	ds_read_b32 v21, v15
	ds_read_b32 v22, v17
	ds_read_b32 v19, v19
	ds_read_b32 v23, v20
	ds_read_b32 v24, v24
	ds_read_b32 v20, v25
	ds_read_b32 v25, v26
	ds_read_b32 v26, v27
	ds_read_b32 v28, v28
	ds_read_b32 v27, v29
	ds_read_b32 v29, v30
	ds_read_b32 v30, v31
	ds_read_b32 v32, v32
	ds_read_b32 v31, v33
	ds_read_b32 v33, v40
	s_add_i32 vcc_hi, vcc_hi, 2
	s_add_i32 s21, s21, s11
	s_add_i32 s10, s10, s12
	s_add_i32 s18, s18, s14
	s_add_i32 s4, s4, s15
	s_add_i32 s91, s91, s16
	s_add_i32 s13, s13, s17
	s_add_i32 vcc_lo, vcc_lo, s90
	s_add_i32 s42, s42, s5
	s_waitcnt vmcnt(56) lgkmcnt(0)
	v_pk_fma_f32 v[8:9], v[132:133], v[18:19], v[8:9] op_sel_hi:[0,1,1]
	v_pk_fma_f32 v[2:3], v[132:133], v[22:23], v[2:3] op_sel_hi:[0,1,1]
	v_pk_fma_f32 v[10:11], v[132:133], v[24:25], v[10:11] op_sel_hi:[0,1,1]
	v_pk_fma_f32 v[6:7], v[132:133], v[20:21], v[6:7] op_sel_hi:[0,1,1]
	v_pk_fma_f32 v[8:9], v[134:135], v[26:27], v[8:9] op_sel_hi:[0,1,1]
	v_pk_fma_f32 v[2:3], v[134:135], v[28:29], v[2:3] op_sel_hi:[0,1,1]
	v_pk_fma_f32 v[10:11], v[134:135], v[30:31], v[10:11] op_sel_hi:[0,1,1]
	v_pk_fma_f32 v[6:7], v[134:135], v[32:33], v[6:7] op_sel_hi:[0,1,1]
	s_and_b32 s20, s42, 0x70
	s_add_i32 s30, s21, -1
	s_add_i32 s31, s10, -2
	s_add_i32 s97, s18, -3
	s_add_i32 s3, s4, -4
	s_add_i32 s63, s91, -5
	s_add_i32 s79, s13, -6
	s_and_b32 s81, vcc_lo, 0x7e
	s_add_i32 s70, s44, s42
	s_add_i32 s76, s44, s21
	s_add_i32 s19, s44, s10
	s_add_i32 s69, s44, s18
	s_add_i32 s53, s44, s4
	s_add_i32 s94, s44, s91
	s_add_i32 s88, s44, s13
	s_add_i32 s45, s65, vcc_lo
	s_lshl_b32 s0, s20, 2
	s_and_b32 s1, s30, 0x7e
	s_and_b32 s20, s31, 0x7c
	s_and_b32 s30, s97, 0x7e
	s_and_b32 s3, s3, 0x78
	s_and_b32 s31, s63, 0x7e
	s_and_b32 s63, s79, 0x7c
	s_lshl_b32 s79, s81, 2
	s_and_b32 s70, s70, 0x78
	s_and_b32 s76, s76, 0x7f
	s_and_b32 s19, s19, 0x7e
	s_and_b32 s69, s69, 0x7f
	s_and_b32 s53, s53, 0x7c
	s_and_b32 s81, s94, 0x7f
	s_and_b32 s88, s88, 0x7e
	s_and_b32 s45, s45, 0x7f
	s_add_i32 s0, s49, s0
	s_lshl_b32 s1, s1, 2
	s_lshl_b32 s20, s20, 2
	s_lshl_b32 s30, s30, 2
	s_lshl_b32 s3, s3, 2
	s_lshl_b32 s31, s31, 2
	s_lshl_b32 s63, s63, 2
	s_add_i32 s79, s49, s79
	s_lshl_b32 s70, s70, 2
	s_lshl_b32 s76, s76, 2
	s_lshl_b32 s19, s19, 2
	s_lshl_b32 s69, s69, 2
	s_lshl_b32 s53, s53, 2
	s_lshl_b32 s81, s81, 2
	s_lshl_b32 s88, s88, 2
	s_lshl_b32 s45, s45, 2
	v_mov_b32_e32 v13, s0
	s_add_i32 s0, s49, s1
	s_add_i32 s1, s49, s20
	s_add_i32 s20, s49, s30
	s_add_i32 s3, s49, s3
	s_add_i32 s30, s49, s31
	s_add_i32 s31, s49, s63
	v_mov_b32_e32 v15, s79
	s_add_i32 s63, s49, s70
	s_add_i32 s70, s49, s76
	s_add_i32 s19, s49, s19
	s_add_i32 s69, s49, s69
	s_add_i32 s53, s49, s53
	s_add_i32 s76, s49, s81
	s_add_i32 s79, s49, s88
	s_add_i32 s45, s49, s45
	v_mov_b32_e32 v19, s1
	v_mov_b32_e32 v20, s20
	v_mov_b32_e32 v24, s3
	v_mov_b32_e32 v25, s30
	v_mov_b32_e32 v26, s31
	v_mov_b32_e32 v27, s63
	v_mov_b32_e32 v28, s70
	v_mov_b32_e32 v29, s19
	v_mov_b32_e32 v30, s69
	v_mov_b32_e32 v31, s53
	v_mov_b32_e32 v32, s76
	v_mov_b32_e32 v33, s79
	v_mov_b32_e32 v17, s0
	v_mov_b32_e32 v40, s45
	ds_read_b32 v18, v13
	ds_read_b32 v21, v15
	ds_read_b32 v22, v17
	ds_read_b32 v19, v19
	ds_read_b32 v23, v20
	ds_read_b32 v24, v24
	ds_read_b32 v20, v25
	ds_read_b32 v25, v26
	ds_read_b32 v26, v27
	ds_read_b32 v28, v28
	ds_read_b32 v27, v29
	ds_read_b32 v29, v30
	ds_read_b32 v30, v31
	ds_read_b32 v32, v32
	ds_read_b32 v31, v33
	ds_read_b32 v33, v40
	s_add_i32 vcc_hi, vcc_hi, 2
	s_add_i32 s21, s21, s11
	s_add_i32 s10, s10, s12
	s_add_i32 s18, s18, s14
	s_add_i32 s4, s4, s15
	s_add_i32 s91, s91, s16
	s_add_i32 s13, s13, s17
	s_add_i32 vcc_lo, vcc_lo, s90
	s_add_i32 s42, s42, s5
	s_waitcnt vmcnt(54) lgkmcnt(0)
; __device__ __forceinline__ void p0_prologue(Frame& F) {
;     ...
; #pragma unroll 2
;             for (int m = 0; m < 128; ++m) { const float wv = wsrc[(size_t)m * 1024];
; #pragma unroll
;                 for (int j = 0; j < 8; ++j) acc8[j] += scr[(m * (c0 + j)) & 127] * wv; }
	v_pk_fma_f32 v[8:9], v[136:137], v[18:19], v[8:9] op_sel_hi:[0,1,1]
	v_pk_fma_f32 v[2:3], v[136:137], v[22:23], v[2:3] op_sel_hi:[0,1,1]
	v_pk_fma_f32 v[10:11], v[136:137], v[24:25], v[10:11] op_sel_hi:[0,1,1]
	v_pk_fma_f32 v[6:7], v[136:137], v[20:21], v[6:7] op_sel_hi:[0,1,1]
	v_pk_fma_f32 v[8:9], v[138:139], v[26:27], v[8:9] op_sel_hi:[0,1,1]
	v_pk_fma_f32 v[2:3], v[138:139], v[28:29], v[2:3] op_sel_hi:[0,1,1]
	v_pk_fma_f32 v[10:11], v[138:139], v[30:31], v[10:11] op_sel_hi:[0,1,1]
	v_pk_fma_f32 v[6:7], v[138:139], v[32:33], v[6:7] op_sel_hi:[0,1,1]
	s_and_b32 s20, s42, 0x70
	s_add_i32 s30, s21, -1
	s_add_i32 s31, s10, -2
	s_add_i32 s97, s18, -3
	s_add_i32 s3, s4, -4
	s_add_i32 s63, s91, -5
	s_add_i32 s79, s13, -6
	s_and_b32 s81, vcc_lo, 0x7e
	s_add_i32 s70, s44, s42
	s_add_i32 s76, s44, s21
	s_add_i32 s19, s44, s10
	s_add_i32 s69, s44, s18
	s_add_i32 s53, s44, s4
	s_add_i32 s94, s44, s91
	s_add_i32 s88, s44, s13
	s_add_i32 s45, s65, vcc_lo
	s_lshl_b32 s0, s20, 2
	s_and_b32 s1, s30, 0x7e
	s_and_b32 s20, s31, 0x7c
	s_and_b32 s30, s97, 0x7e
	s_and_b32 s3, s3, 0x78
	s_and_b32 s31, s63, 0x7e
	s_and_b32 s63, s79, 0x7c
	s_lshl_b32 s79, s81, 2
	s_and_b32 s70, s70, 0x78
	s_and_b32 s76, s76, 0x7f
	s_and_b32 s19, s19, 0x7e
	s_and_b32 s69, s69, 0x7f
	s_and_b32 s53, s53, 0x7c
	s_and_b32 s81, s94, 0x7f
	s_and_b32 s88, s88, 0x7e
	s_and_b32 s45, s45, 0x7f
	s_add_i32 s0, s49, s0
	s_lshl_b32 s1, s1, 2
	s_lshl_b32 s20, s20, 2
	s_lshl_b32 s30, s30, 2
	s_lshl_b32 s3, s3, 2
	s_lshl_b32 s31, s31, 2
	s_lshl_b32 s63, s63, 2
	s_add_i32 s79, s49, s79
	s_lshl_b32 s70, s70, 2
	s_lshl_b32 s76, s76, 2
	s_lshl_b32 s19, s19, 2
	s_lshl_b32 s69, s69, 2
	s_lshl_b32 s53, s53, 2
	s_lshl_b32 s81, s81, 2
	s_lshl_b32 s88, s88, 2
	s_lshl_b32 s45, s45, 2
	v_mov_b32_e32 v13, s0
	s_add_i32 s0, s49, s1
	s_add_i32 s1, s49, s20
	s_add_i32 s20, s49, s30
	s_add_i32 s3, s49, s3
	s_add_i32 s30, s49, s31
	s_add_i32 s31, s49, s63
	v_mov_b32_e32 v15, s79
	s_add_i32 s63, s49, s70
	s_add_i32 s70, s49, s76
	s_add_i32 s19, s49, s19
	s_add_i32 s69, s49, s69
	s_add_i32 s53, s49, s53
	s_add_i32 s76, s49, s81
	s_add_i32 s79, s49, s88
	s_add_i32 s45, s49, s45
	v_mov_b32_e32 v19, s1
	v_mov_b32_e32 v20, s20
	v_mov_b32_e32 v24, s3
	v_mov_b32_e32 v25, s30
	v_mov_b32_e32 v26, s31
	v_mov_b32_e32 v27, s63
	v_mov_b32_e32 v28, s70
	v_mov_b32_e32 v29, s19
	v_mov_b32_e32 v30, s69
	v_mov_b32_e32 v31, s53
	v_mov_b32_e32 v32, s76
	v_mov_b32_e32 v33, s79
	v_mov_b32_e32 v17, s0
	v_mov_b32_e32 v40, s45
	ds_read_b32 v18, v13
	ds_read_b32 v21, v15
	ds_read_b32 v22, v17
	ds_read_b32 v19, v19
	ds_read_b32 v23, v20
	ds_read_b32 v24, v24
	ds_read_b32 v20, v25
	ds_read_b32 v25, v26
	ds_read_b32 v26, v27
	ds_read_b32 v28, v28
	ds_read_b32 v27, v29
	ds_read_b32 v29, v30
	ds_read_b32 v30, v31
	ds_read_b32 v32, v32
	ds_read_b32 v31, v33
	ds_read_b32 v33, v40
	s_add_i32 vcc_hi, vcc_hi, 2
	s_add_i32 s21, s21, s11
	s_add_i32 s10, s10, s12
	s_add_i32 s18, s18, s14
	s_add_i32 s4, s4, s15
	s_add_i32 s91, s91, s16
	s_add_i32 s13, s13, s17
	s_add_i32 vcc_lo, vcc_lo, s90
	s_add_i32 s42, s42, s5
	s_waitcnt vmcnt(52) lgkmcnt(0)
	v_pk_fma_f32 v[8:9], v[140:141], v[18:19], v[8:9] op_sel_hi:[0,1,1]
	v_pk_fma_f32 v[2:3], v[140:141], v[22:23], v[2:3] op_sel_hi:[0,1,1]
	v_pk_fma_f32 v[10:11], v[140:141], v[24:25], v[10:11] op_sel_hi:[0,1,1]
	v_pk_fma_f32 v[6:7], v[140:141], v[20:21], v[6:7] op_sel_hi:[0,1,1]
	v_pk_fma_f32 v[8:9], v[142:143], v[26:27], v[8:9] op_sel_hi:[0,1,1]
	v_pk_fma_f32 v[2:3], v[142:143], v[28:29], v[2:3] op_sel_hi:[0,1,1]
	v_pk_fma_f32 v[10:11], v[142:143], v[30:31], v[10:11] op_sel_hi:[0,1,1]
	v_pk_fma_f32 v[6:7], v[142:143], v[32:33], v[6:7] op_sel_hi:[0,1,1]
	s_and_b32 s20, s42, 0x70
	s_add_i32 s30, s21, -1
	s_add_i32 s31, s10, -2
	s_add_i32 s97, s18, -3
	s_add_i32 s3, s4, -4
	s_add_i32 s63, s91, -5
	s_add_i32 s79, s13, -6
	s_and_b32 s81, vcc_lo, 0x7e
	s_add_i32 s70, s44, s42
	s_add_i32 s76, s44, s21
	s_add_i32 s19, s44, s10
	s_add_i32 s69, s44, s18
	s_add_i32 s53, s44, s4
	s_add_i32 s94, s44, s91
	s_add_i32 s88, s44, s13
	s_add_i32 s45, s65, vcc_lo
	s_lshl_b32 s0, s20, 2
	s_and_b32 s1, s30, 0x7e
	s_and_b32 s20, s31, 0x7c
	s_and_b32 s30, s97, 0x7e
	s_and_b32 s3, s3, 0x78
	s_and_b32 s31, s63, 0x7e
	s_and_b32 s63, s79, 0x7c
	s_lshl_b32 s79, s81, 2
	s_and_b32 s70, s70, 0x78
	s_and_b32 s76, s76, 0x7f
	s_and_b32 s19, s19, 0x7e
	s_and_b32 s69, s69, 0x7f
	s_and_b32 s53, s53, 0x7c
	s_and_b32 s81, s94, 0x7f
	s_and_b32 s88, s88, 0x7e
	s_and_b32 s45, s45, 0x7f
	s_add_i32 s0, s49, s0
	s_lshl_b32 s1, s1, 2
	s_lshl_b32 s20, s20, 2
	s_lshl_b32 s30, s30, 2
	s_lshl_b32 s3, s3, 2
	s_lshl_b32 s31, s31, 2
	s_lshl_b32 s63, s63, 2
	s_add_i32 s79, s49, s79
	s_lshl_b32 s70, s70, 2
	s_lshl_b32 s76, s76, 2
	s_lshl_b32 s19, s19, 2
	s_lshl_b32 s69, s69, 2
	s_lshl_b32 s53, s53, 2
	s_lshl_b32 s81, s81, 2
	s_lshl_b32 s88, s88, 2
	s_lshl_b32 s45, s45, 2
	v_mov_b32_e32 v13, s0
	s_add_i32 s0, s49, s1
	s_add_i32 s1, s49, s20
	s_add_i32 s20, s49, s30
	s_add_i32 s3, s49, s3
	s_add_i32 s30, s49, s31
	s_add_i32 s31, s49, s63
	v_mov_b32_e32 v15, s79
	s_add_i32 s63, s49, s70
	s_add_i32 s70, s49, s76
	s_add_i32 s19, s49, s19
	s_add_i32 s69, s49, s69
	s_add_i32 s53, s49, s53
	s_add_i32 s76, s49, s81
	s_add_i32 s79, s49, s88
	s_add_i32 s45, s49, s45
	v_mov_b32_e32 v19, s1
	v_mov_b32_e32 v20, s20
	v_mov_b32_e32 v24, s3
	v_mov_b32_e32 v25, s30
	v_mov_b32_e32 v26, s31
	v_mov_b32_e32 v27, s63
	v_mov_b32_e32 v28, s70
	v_mov_b32_e32 v29, s19
	v_mov_b32_e32 v30, s69
	v_mov_b32_e32 v31, s53
	v_mov_b32_e32 v32, s76
	v_mov_b32_e32 v33, s79
	v_mov_b32_e32 v17, s0
	v_mov_b32_e32 v40, s45
	ds_read_b32 v18, v13
	ds_read_b32 v21, v15
	ds_read_b32 v22, v17
	ds_read_b32 v19, v19
	ds_read_b32 v23, v20
	ds_read_b32 v24, v24
	ds_read_b32 v20, v25
	ds_read_b32 v25, v26
	ds_read_b32 v26, v27
	ds_read_b32 v28, v28
	ds_read_b32 v27, v29
	ds_read_b32 v29, v30
	ds_read_b32 v30, v31
	ds_read_b32 v32, v32
	ds_read_b32 v31, v33
	ds_read_b32 v33, v40
	s_add_i32 vcc_hi, vcc_hi, 2
	s_add_i32 s21, s21, s11
	s_add_i32 s10, s10, s12
	s_add_i32 s18, s18, s14
	s_add_i32 s4, s4, s15
	s_add_i32 s91, s91, s16
	s_add_i32 s13, s13, s17
	s_add_i32 vcc_lo, vcc_lo, s90
	s_add_i32 s42, s42, s5
	s_waitcnt vmcnt(50) lgkmcnt(0)
; __device__ __forceinline__ void p0_prologue(Frame& F) {
;     ...
; #pragma unroll 2
;             for (int m = 0; m < 128; ++m) { const float wv = wsrc[(size_t)m * 1024];
; #pragma unroll
;                 for (int j = 0; j < 8; ++j) acc8[j] += scr[(m * (c0 + j)) & 127] * wv; }
	v_pk_fma_f32 v[8:9], v[144:145], v[18:19], v[8:9] op_sel_hi:[0,1,1]
	v_pk_fma_f32 v[2:3], v[144:145], v[22:23], v[2:3] op_sel_hi:[0,1,1]
	v_pk_fma_f32 v[10:11], v[144:145], v[24:25], v[10:11] op_sel_hi:[0,1,1]
	v_pk_fma_f32 v[6:7], v[144:145], v[20:21], v[6:7] op_sel_hi:[0,1,1]
	v_pk_fma_f32 v[8:9], v[146:147], v[26:27], v[8:9] op_sel_hi:[0,1,1]
	v_pk_fma_f32 v[2:3], v[146:147], v[28:29], v[2:3] op_sel_hi:[0,1,1]
	v_pk_fma_f32 v[10:11], v[146:147], v[30:31], v[10:11] op_sel_hi:[0,1,1]
	v_pk_fma_f32 v[6:7], v[146:147], v[32:33], v[6:7] op_sel_hi:[0,1,1]
	s_and_b32 s20, s42, 0x70
	s_add_i32 s30, s21, -1
	s_add_i32 s31, s10, -2
	s_add_i32 s97, s18, -3
	s_add_i32 s3, s4, -4
	s_add_i32 s63, s91, -5
	s_add_i32 s79, s13, -6
	s_and_b32 s81, vcc_lo, 0x7e
	s_add_i32 s70, s44, s42
	s_add_i32 s76, s44, s21
	s_add_i32 s19, s44, s10
	s_add_i32 s69, s44, s18
	s_add_i32 s53, s44, s4
	s_add_i32 s94, s44, s91
	s_add_i32 s88, s44, s13
	s_add_i32 s45, s65, vcc_lo
	s_lshl_b32 s0, s20, 2
	s_and_b32 s1, s30, 0x7e
	s_and_b32 s20, s31, 0x7c
	s_and_b32 s30, s97, 0x7e
	s_and_b32 s3, s3, 0x78
	s_and_b32 s31, s63, 0x7e
	s_and_b32 s63, s79, 0x7c
	s_lshl_b32 s79, s81, 2
	s_and_b32 s70, s70, 0x78
	s_and_b32 s76, s76, 0x7f
	s_and_b32 s19, s19, 0x7e
	s_and_b32 s69, s69, 0x7f
	s_and_b32 s53, s53, 0x7c
	s_and_b32 s81, s94, 0x7f
	s_and_b32 s88, s88, 0x7e
	s_and_b32 s45, s45, 0x7f
	s_add_i32 s0, s49, s0
	s_lshl_b32 s1, s1, 2
	s_lshl_b32 s20, s20, 2
	s_lshl_b32 s30, s30, 2
	s_lshl_b32 s3, s3, 2
	s_lshl_b32 s31, s31, 2
	s_lshl_b32 s63, s63, 2
	s_add_i32 s79, s49, s79
	s_lshl_b32 s70, s70, 2
	s_lshl_b32 s76, s76, 2
	s_lshl_b32 s19, s19, 2
	s_lshl_b32 s69, s69, 2
	s_lshl_b32 s53, s53, 2
	s_lshl_b32 s81, s81, 2
	s_lshl_b32 s88, s88, 2
	s_lshl_b32 s45, s45, 2
	v_mov_b32_e32 v13, s0
	s_add_i32 s0, s49, s1
	s_add_i32 s1, s49, s20
	s_add_i32 s20, s49, s30
	s_add_i32 s3, s49, s3
	s_add_i32 s30, s49, s31
	s_add_i32 s31, s49, s63
	v_mov_b32_e32 v15, s79
	s_add_i32 s63, s49, s70
	s_add_i32 s70, s49, s76
	s_add_i32 s19, s49, s19
	s_add_i32 s69, s49, s69
	s_add_i32 s53, s49, s53
	s_add_i32 s76, s49, s81
	s_add_i32 s79, s49, s88
	s_add_i32 s45, s49, s45
	v_mov_b32_e32 v19, s1
	v_mov_b32_e32 v20, s20
	v_mov_b32_e32 v24, s3
	v_mov_b32_e32 v25, s30
	v_mov_b32_e32 v26, s31
	v_mov_b32_e32 v27, s63
	v_mov_b32_e32 v28, s70
	v_mov_b32_e32 v29, s19
	v_mov_b32_e32 v30, s69
	v_mov_b32_e32 v31, s53
	v_mov_b32_e32 v32, s76
	v_mov_b32_e32 v33, s79
	v_mov_b32_e32 v17, s0
	v_mov_b32_e32 v40, s45
	ds_read_b32 v18, v13
	ds_read_b32 v21, v15
	ds_read_b32 v22, v17
	ds_read_b32 v19, v19
	ds_read_b32 v23, v20
	ds_read_b32 v24, v24
	ds_read_b32 v20, v25
	ds_read_b32 v25, v26
	ds_read_b32 v26, v27
	ds_read_b32 v28, v28
	ds_read_b32 v27, v29
	ds_read_b32 v29, v30
	ds_read_b32 v30, v31
	ds_read_b32 v32, v32
	ds_read_b32 v31, v33
	ds_read_b32 v33, v40
	s_add_i32 vcc_hi, vcc_hi, 2
	s_add_i32 s21, s21, s11
	s_add_i32 s10, s10, s12
	s_add_i32 s18, s18, s14
	s_add_i32 s4, s4, s15
	s_add_i32 s91, s91, s16
	s_add_i32 s13, s13, s17
	s_add_i32 vcc_lo, vcc_lo, s90
	s_add_i32 s42, s42, s5
	s_waitcnt vmcnt(48) lgkmcnt(0)
	v_pk_fma_f32 v[8:9], v[148:149], v[18:19], v[8:9] op_sel_hi:[0,1,1]
	v_pk_fma_f32 v[2:3], v[148:149], v[22:23], v[2:3] op_sel_hi:[0,1,1]
	v_pk_fma_f32 v[10:11], v[148:149], v[24:25], v[10:11] op_sel_hi:[0,1,1]
	v_pk_fma_f32 v[6:7], v[148:149], v[20:21], v[6:7] op_sel_hi:[0,1,1]
	v_pk_fma_f32 v[8:9], v[150:151], v[26:27], v[8:9] op_sel_hi:[0,1,1]
	v_pk_fma_f32 v[2:3], v[150:151], v[28:29], v[2:3] op_sel_hi:[0,1,1]
	v_pk_fma_f32 v[10:11], v[150:151], v[30:31], v[10:11] op_sel_hi:[0,1,1]
	v_pk_fma_f32 v[6:7], v[150:151], v[32:33], v[6:7] op_sel_hi:[0,1,1]
	s_and_b32 s20, s42, 0x70
	s_add_i32 s30, s21, -1
	s_add_i32 s31, s10, -2
	s_add_i32 s97, s18, -3
	s_add_i32 s3, s4, -4
	s_add_i32 s63, s91, -5
	s_add_i32 s79, s13, -6
	s_and_b32 s81, vcc_lo, 0x7e
	s_add_i32 s70, s44, s42
	s_add_i32 s76, s44, s21
	s_add_i32 s19, s44, s10
	s_add_i32 s69, s44, s18
	s_add_i32 s53, s44, s4
	s_add_i32 s94, s44, s91
	s_add_i32 s88, s44, s13
	s_add_i32 s45, s65, vcc_lo
	s_lshl_b32 s0, s20, 2
	s_and_b32 s1, s30, 0x7e
	s_and_b32 s20, s31, 0x7c
	s_and_b32 s30, s97, 0x7e
	s_and_b32 s3, s3, 0x78
	s_and_b32 s31, s63, 0x7e
	s_and_b32 s63, s79, 0x7c
	s_lshl_b32 s79, s81, 2
	s_and_b32 s70, s70, 0x78
	s_and_b32 s76, s76, 0x7f
	s_and_b32 s19, s19, 0x7e
	s_and_b32 s69, s69, 0x7f
	s_and_b32 s53, s53, 0x7c
	s_and_b32 s81, s94, 0x7f
	s_and_b32 s88, s88, 0x7e
	s_and_b32 s45, s45, 0x7f
	s_add_i32 s0, s49, s0
	s_lshl_b32 s1, s1, 2
	s_lshl_b32 s20, s20, 2
	s_lshl_b32 s30, s30, 2
	s_lshl_b32 s3, s3, 2
	s_lshl_b32 s31, s31, 2
	s_lshl_b32 s63, s63, 2
	s_add_i32 s79, s49, s79
	s_lshl_b32 s70, s70, 2
	s_lshl_b32 s76, s76, 2
	s_lshl_b32 s19, s19, 2
	s_lshl_b32 s69, s69, 2
	s_lshl_b32 s53, s53, 2
	s_lshl_b32 s81, s81, 2
	s_lshl_b32 s88, s88, 2
	s_lshl_b32 s45, s45, 2
	v_mov_b32_e32 v13, s0
	s_add_i32 s0, s49, s1
	s_add_i32 s1, s49, s20
	s_add_i32 s20, s49, s30
	s_add_i32 s3, s49, s3
	s_add_i32 s30, s49, s31
	s_add_i32 s31, s49, s63
	v_mov_b32_e32 v15, s79
	s_add_i32 s63, s49, s70
	s_add_i32 s70, s49, s76
	s_add_i32 s19, s49, s19
	s_add_i32 s69, s49, s69
	s_add_i32 s53, s49, s53
	s_add_i32 s76, s49, s81
	s_add_i32 s79, s49, s88
	s_add_i32 s45, s49, s45
	v_mov_b32_e32 v19, s1
	v_mov_b32_e32 v20, s20
	v_mov_b32_e32 v24, s3
	v_mov_b32_e32 v25, s30
	v_mov_b32_e32 v26, s31
	v_mov_b32_e32 v27, s63
	v_mov_b32_e32 v28, s70
	v_mov_b32_e32 v29, s19
	v_mov_b32_e32 v30, s69
	v_mov_b32_e32 v31, s53
	v_mov_b32_e32 v32, s76
	v_mov_b32_e32 v33, s79
	v_mov_b32_e32 v17, s0
	v_mov_b32_e32 v40, s45
	ds_read_b32 v18, v13
	ds_read_b32 v21, v15
	ds_read_b32 v22, v17
	ds_read_b32 v19, v19
	ds_read_b32 v23, v20
	ds_read_b32 v24, v24
	ds_read_b32 v20, v25
	ds_read_b32 v25, v26
	ds_read_b32 v26, v27
	ds_read_b32 v28, v28
	ds_read_b32 v27, v29
	ds_read_b32 v29, v30
	ds_read_b32 v30, v31
	ds_read_b32 v32, v32
	ds_read_b32 v31, v33
	ds_read_b32 v33, v40
	s_add_i32 vcc_hi, vcc_hi, 2
	s_add_i32 s21, s21, s11
	s_add_i32 s10, s10, s12
	s_add_i32 s18, s18, s14
	s_add_i32 s4, s4, s15
	s_add_i32 s91, s91, s16
	s_add_i32 s13, s13, s17
	s_add_i32 vcc_lo, vcc_lo, s90
	s_add_i32 s42, s42, s5
	s_waitcnt vmcnt(46) lgkmcnt(0)
; __device__ __forceinline__ void p0_prologue(Frame& F) {
;     ...
; #pragma unroll 2
;             for (int m = 0; m < 128; ++m) { const float wv = wsrc[(size_t)m * 1024];
; #pragma unroll
;                 for (int j = 0; j < 8; ++j) acc8[j] += scr[(m * (c0 + j)) & 127] * wv; }
	v_pk_fma_f32 v[8:9], v[152:153], v[18:19], v[8:9] op_sel_hi:[0,1,1]
	v_pk_fma_f32 v[2:3], v[152:153], v[22:23], v[2:3] op_sel_hi:[0,1,1]
	v_pk_fma_f32 v[10:11], v[152:153], v[24:25], v[10:11] op_sel_hi:[0,1,1]
	v_pk_fma_f32 v[6:7], v[152:153], v[20:21], v[6:7] op_sel_hi:[0,1,1]
	v_pk_fma_f32 v[8:9], v[154:155], v[26:27], v[8:9] op_sel_hi:[0,1,1]
	v_pk_fma_f32 v[2:3], v[154:155], v[28:29], v[2:3] op_sel_hi:[0,1,1]
	v_pk_fma_f32 v[10:11], v[154:155], v[30:31], v[10:11] op_sel_hi:[0,1,1]
	v_pk_fma_f32 v[6:7], v[154:155], v[32:33], v[6:7] op_sel_hi:[0,1,1]
	s_and_b32 s20, s42, 0x70
	s_add_i32 s30, s21, -1
	s_add_i32 s31, s10, -2
	s_add_i32 s97, s18, -3
	s_add_i32 s3, s4, -4
	s_add_i32 s63, s91, -5
	s_add_i32 s79, s13, -6
	s_and_b32 s81, vcc_lo, 0x7e
	s_add_i32 s70, s44, s42
	s_add_i32 s76, s44, s21
	s_add_i32 s19, s44, s10
	s_add_i32 s69, s44, s18
	s_add_i32 s53, s44, s4
	s_add_i32 s94, s44, s91
	s_add_i32 s88, s44, s13
	s_add_i32 s45, s65, vcc_lo
	s_lshl_b32 s0, s20, 2
	s_and_b32 s1, s30, 0x7e
	s_and_b32 s20, s31, 0x7c
	s_and_b32 s30, s97, 0x7e
	s_and_b32 s3, s3, 0x78
	s_and_b32 s31, s63, 0x7e
	s_and_b32 s63, s79, 0x7c
	s_lshl_b32 s79, s81, 2
	s_and_b32 s70, s70, 0x78
	s_and_b32 s76, s76, 0x7f
	s_and_b32 s19, s19, 0x7e
	s_and_b32 s69, s69, 0x7f
	s_and_b32 s53, s53, 0x7c
	s_and_b32 s81, s94, 0x7f
	s_and_b32 s88, s88, 0x7e
	s_and_b32 s45, s45, 0x7f
	s_add_i32 s0, s49, s0
	s_lshl_b32 s1, s1, 2
	s_lshl_b32 s20, s20, 2
	s_lshl_b32 s30, s30, 2
	s_lshl_b32 s3, s3, 2
	s_lshl_b32 s31, s31, 2
	s_lshl_b32 s63, s63, 2
	s_add_i32 s79, s49, s79
	s_lshl_b32 s70, s70, 2
	s_lshl_b32 s76, s76, 2
	s_lshl_b32 s19, s19, 2
	s_lshl_b32 s69, s69, 2
	s_lshl_b32 s53, s53, 2
	s_lshl_b32 s81, s81, 2
	s_lshl_b32 s88, s88, 2
	s_lshl_b32 s45, s45, 2
	v_mov_b32_e32 v13, s0
	s_add_i32 s0, s49, s1
	s_add_i32 s1, s49, s20
	s_add_i32 s20, s49, s30
	s_add_i32 s3, s49, s3
	s_add_i32 s30, s49, s31
	s_add_i32 s31, s49, s63
	v_mov_b32_e32 v15, s79
	s_add_i32 s63, s49, s70
	s_add_i32 s70, s49, s76
	s_add_i32 s19, s49, s19
	s_add_i32 s69, s49, s69
	s_add_i32 s53, s49, s53
	s_add_i32 s76, s49, s81
	s_add_i32 s79, s49, s88
	s_add_i32 s45, s49, s45
	v_mov_b32_e32 v19, s1
	v_mov_b32_e32 v20, s20
	v_mov_b32_e32 v24, s3
	v_mov_b32_e32 v25, s30
	v_mov_b32_e32 v26, s31
	v_mov_b32_e32 v27, s63
	v_mov_b32_e32 v28, s70
	v_mov_b32_e32 v29, s19
	v_mov_b32_e32 v30, s69
	v_mov_b32_e32 v31, s53
	v_mov_b32_e32 v32, s76
	v_mov_b32_e32 v33, s79
	v_mov_b32_e32 v17, s0
	v_mov_b32_e32 v40, s45
	ds_read_b32 v18, v13
	ds_read_b32 v21, v15
	ds_read_b32 v22, v17
	ds_read_b32 v19, v19
	ds_read_b32 v23, v20
	ds_read_b32 v24, v24
	ds_read_b32 v20, v25
	ds_read_b32 v25, v26
	ds_read_b32 v26, v27
	ds_read_b32 v28, v28
	ds_read_b32 v27, v29
	ds_read_b32 v29, v30
	ds_read_b32 v30, v31
	ds_read_b32 v32, v32
	ds_read_b32 v31, v33
	ds_read_b32 v33, v40
	s_add_i32 vcc_hi, vcc_hi, 2
	s_add_i32 s21, s21, s11
	s_add_i32 s10, s10, s12
	s_add_i32 s18, s18, s14
	s_add_i32 s4, s4, s15
	s_add_i32 s91, s91, s16
	s_add_i32 s13, s13, s17
	s_add_i32 vcc_lo, vcc_lo, s90
	s_add_i32 s42, s42, s5
	s_waitcnt vmcnt(44) lgkmcnt(0)
	v_pk_fma_f32 v[8:9], v[156:157], v[18:19], v[8:9] op_sel_hi:[0,1,1]
	v_pk_fma_f32 v[2:3], v[156:157], v[22:23], v[2:3] op_sel_hi:[0,1,1]
	v_pk_fma_f32 v[10:11], v[156:157], v[24:25], v[10:11] op_sel_hi:[0,1,1]
	v_pk_fma_f32 v[6:7], v[156:157], v[20:21], v[6:7] op_sel_hi:[0,1,1]
	v_pk_fma_f32 v[8:9], v[158:159], v[26:27], v[8:9] op_sel_hi:[0,1,1]
	v_pk_fma_f32 v[2:3], v[158:159], v[28:29], v[2:3] op_sel_hi:[0,1,1]
	v_pk_fma_f32 v[10:11], v[158:159], v[30:31], v[10:11] op_sel_hi:[0,1,1]
	v_pk_fma_f32 v[6:7], v[158:159], v[32:33], v[6:7] op_sel_hi:[0,1,1]
	s_and_b32 s20, s42, 0x70
	s_add_i32 s30, s21, -1
	s_add_i32 s31, s10, -2
	s_add_i32 s97, s18, -3
	s_add_i32 s3, s4, -4
	s_add_i32 s63, s91, -5
	s_add_i32 s79, s13, -6
	s_and_b32 s81, vcc_lo, 0x7e
	s_add_i32 s70, s44, s42
	s_add_i32 s76, s44, s21
	s_add_i32 s19, s44, s10
	s_add_i32 s69, s44, s18
	s_add_i32 s53, s44, s4
	s_add_i32 s94, s44, s91
	s_add_i32 s88, s44, s13
	s_add_i32 s45, s65, vcc_lo
	s_lshl_b32 s0, s20, 2
	s_and_b32 s1, s30, 0x7e
	s_and_b32 s20, s31, 0x7c
	s_and_b32 s30, s97, 0x7e
	s_and_b32 s3, s3, 0x78
	s_and_b32 s31, s63, 0x7e
	s_and_b32 s63, s79, 0x7c
	s_lshl_b32 s79, s81, 2
	s_and_b32 s70, s70, 0x78
	s_and_b32 s76, s76, 0x7f
	s_and_b32 s19, s19, 0x7e
	s_and_b32 s69, s69, 0x7f
	s_and_b32 s53, s53, 0x7c
	s_and_b32 s81, s94, 0x7f
	s_and_b32 s88, s88, 0x7e
	s_and_b32 s45, s45, 0x7f
	s_add_i32 s0, s49, s0
	s_lshl_b32 s1, s1, 2
	s_lshl_b32 s20, s20, 2
	s_lshl_b32 s30, s30, 2
	s_lshl_b32 s3, s3, 2
	s_lshl_b32 s31, s31, 2
	s_lshl_b32 s63, s63, 2
	s_add_i32 s79, s49, s79
	s_lshl_b32 s70, s70, 2
	s_lshl_b32 s76, s76, 2
	s_lshl_b32 s19, s19, 2
	s_lshl_b32 s69, s69, 2
	s_lshl_b32 s53, s53, 2
	s_lshl_b32 s81, s81, 2
	s_lshl_b32 s88, s88, 2
	s_lshl_b32 s45, s45, 2
	v_mov_b32_e32 v13, s0
	s_add_i32 s0, s49, s1
	s_add_i32 s1, s49, s20
	s_add_i32 s20, s49, s30
	s_add_i32 s3, s49, s3
	s_add_i32 s30, s49, s31
	s_add_i32 s31, s49, s63
	v_mov_b32_e32 v15, s79
	s_add_i32 s63, s49, s70
	s_add_i32 s70, s49, s76
	s_add_i32 s19, s49, s19
	s_add_i32 s69, s49, s69
	s_add_i32 s53, s49, s53
	s_add_i32 s76, s49, s81
	s_add_i32 s79, s49, s88
	s_add_i32 s45, s49, s45
	v_mov_b32_e32 v19, s1
	v_mov_b32_e32 v20, s20
	v_mov_b32_e32 v24, s3
	v_mov_b32_e32 v25, s30
	v_mov_b32_e32 v26, s31
	v_mov_b32_e32 v27, s63
	v_mov_b32_e32 v28, s70
	v_mov_b32_e32 v29, s19
	v_mov_b32_e32 v30, s69
	v_mov_b32_e32 v31, s53
	v_mov_b32_e32 v32, s76
	v_mov_b32_e32 v33, s79
	v_mov_b32_e32 v17, s0
	v_mov_b32_e32 v40, s45
	ds_read_b32 v18, v13
	ds_read_b32 v21, v15
	ds_read_b32 v22, v17
	ds_read_b32 v19, v19
	ds_read_b32 v23, v20
	ds_read_b32 v24, v24
	ds_read_b32 v20, v25
	ds_read_b32 v25, v26
	ds_read_b32 v26, v27
	ds_read_b32 v28, v28
	ds_read_b32 v27, v29
	ds_read_b32 v29, v30
	ds_read_b32 v30, v31
	ds_read_b32 v32, v32
	ds_read_b32 v31, v33
	ds_read_b32 v33, v40
	s_add_i32 vcc_hi, vcc_hi, 2
	s_add_i32 s21, s21, s11
	s_add_i32 s10, s10, s12
	s_add_i32 s18, s18, s14
	s_add_i32 s4, s4, s15
	s_add_i32 s91, s91, s16
	s_add_i32 s13, s13, s17
	s_add_i32 vcc_lo, vcc_lo, s90
	s_add_i32 s42, s42, s5
	s_waitcnt vmcnt(42) lgkmcnt(0)
; __device__ __forceinline__ void p0_prologue(Frame& F) {
;     ...
; #pragma unroll 2
;             for (int m = 0; m < 128; ++m) { const float wv = wsrc[(size_t)m * 1024];
; #pragma unroll
;                 for (int j = 0; j < 8; ++j) acc8[j] += scr[(m * (c0 + j)) & 127] * wv; }
	v_pk_fma_f32 v[8:9], v[160:161], v[18:19], v[8:9] op_sel_hi:[0,1,1]
	v_pk_fma_f32 v[2:3], v[160:161], v[22:23], v[2:3] op_sel_hi:[0,1,1]
	v_pk_fma_f32 v[10:11], v[160:161], v[24:25], v[10:11] op_sel_hi:[0,1,1]
	v_pk_fma_f32 v[6:7], v[160:161], v[20:21], v[6:7] op_sel_hi:[0,1,1]
	v_pk_fma_f32 v[8:9], v[162:163], v[26:27], v[8:9] op_sel_hi:[0,1,1]
	v_pk_fma_f32 v[2:3], v[162:163], v[28:29], v[2:3] op_sel_hi:[0,1,1]
	v_pk_fma_f32 v[10:11], v[162:163], v[30:31], v[10:11] op_sel_hi:[0,1,1]
	v_pk_fma_f32 v[6:7], v[162:163], v[32:33], v[6:7] op_sel_hi:[0,1,1]
	s_and_b32 s20, s42, 0x70
	s_add_i32 s30, s21, -1
	s_add_i32 s31, s10, -2
	s_add_i32 s97, s18, -3
	s_add_i32 s3, s4, -4
	s_add_i32 s63, s91, -5
	s_add_i32 s79, s13, -6
	s_and_b32 s81, vcc_lo, 0x7e
	s_add_i32 s70, s44, s42
	s_add_i32 s76, s44, s21
	s_add_i32 s19, s44, s10
	s_add_i32 s69, s44, s18
	s_add_i32 s53, s44, s4
	s_add_i32 s94, s44, s91
	s_add_i32 s88, s44, s13
	s_add_i32 s45, s65, vcc_lo
	s_lshl_b32 s0, s20, 2
	s_and_b32 s1, s30, 0x7e
	s_and_b32 s20, s31, 0x7c
	s_and_b32 s30, s97, 0x7e
	s_and_b32 s3, s3, 0x78
	s_and_b32 s31, s63, 0x7e
	s_and_b32 s63, s79, 0x7c
	s_lshl_b32 s79, s81, 2
	s_and_b32 s70, s70, 0x78
	s_and_b32 s76, s76, 0x7f
	s_and_b32 s19, s19, 0x7e
	s_and_b32 s69, s69, 0x7f
	s_and_b32 s53, s53, 0x7c
	s_and_b32 s81, s94, 0x7f
	s_and_b32 s88, s88, 0x7e
	s_and_b32 s45, s45, 0x7f
	s_add_i32 s0, s49, s0
	s_lshl_b32 s1, s1, 2
	s_lshl_b32 s20, s20, 2
	s_lshl_b32 s30, s30, 2
	s_lshl_b32 s3, s3, 2
	s_lshl_b32 s31, s31, 2
	s_lshl_b32 s63, s63, 2
	s_add_i32 s79, s49, s79
	s_lshl_b32 s70, s70, 2
	s_lshl_b32 s76, s76, 2
	s_lshl_b32 s19, s19, 2
	s_lshl_b32 s69, s69, 2
	s_lshl_b32 s53, s53, 2
	s_lshl_b32 s81, s81, 2
	s_lshl_b32 s88, s88, 2
	s_lshl_b32 s45, s45, 2
	v_mov_b32_e32 v13, s0
	s_add_i32 s0, s49, s1
	s_add_i32 s1, s49, s20
	s_add_i32 s20, s49, s30
	s_add_i32 s3, s49, s3
	s_add_i32 s30, s49, s31
	s_add_i32 s31, s49, s63
	v_mov_b32_e32 v15, s79
	s_add_i32 s63, s49, s70
	s_add_i32 s70, s49, s76
	s_add_i32 s19, s49, s19
	s_add_i32 s69, s49, s69
	s_add_i32 s53, s49, s53
	s_add_i32 s76, s49, s81
	s_add_i32 s79, s49, s88
	s_add_i32 s45, s49, s45
	v_mov_b32_e32 v19, s1
	v_mov_b32_e32 v20, s20
	v_mov_b32_e32 v24, s3
	v_mov_b32_e32 v25, s30
	v_mov_b32_e32 v26, s31
	v_mov_b32_e32 v27, s63
	v_mov_b32_e32 v28, s70
	v_mov_b32_e32 v29, s19
	v_mov_b32_e32 v30, s69
	v_mov_b32_e32 v31, s53
	v_mov_b32_e32 v32, s76
	v_mov_b32_e32 v33, s79
	v_mov_b32_e32 v17, s0
	v_mov_b32_e32 v40, s45
	ds_read_b32 v18, v13
	ds_read_b32 v21, v15
	ds_read_b32 v22, v17
	ds_read_b32 v19, v19
	ds_read_b32 v23, v20
	ds_read_b32 v24, v24
	ds_read_b32 v20, v25
	ds_read_b32 v25, v26
	ds_read_b32 v26, v27
	ds_read_b32 v28, v28
	ds_read_b32 v27, v29
	ds_read_b32 v29, v30
	ds_read_b32 v30, v31
	ds_read_b32 v32, v32
	ds_read_b32 v31, v33
	ds_read_b32 v33, v40
	s_add_i32 vcc_hi, vcc_hi, 2
	s_add_i32 s21, s21, s11
	s_add_i32 s10, s10, s12
	s_add_i32 s18, s18, s14
	s_add_i32 s4, s4, s15
	s_add_i32 s91, s91, s16
	s_add_i32 s13, s13, s17
	s_add_i32 vcc_lo, vcc_lo, s90
	s_add_i32 s42, s42, s5
	s_waitcnt vmcnt(40) lgkmcnt(0)
	v_pk_fma_f32 v[8:9], v[164:165], v[18:19], v[8:9] op_sel_hi:[0,1,1]
	v_pk_fma_f32 v[2:3], v[164:165], v[22:23], v[2:3] op_sel_hi:[0,1,1]
	v_pk_fma_f32 v[10:11], v[164:165], v[24:25], v[10:11] op_sel_hi:[0,1,1]
	v_pk_fma_f32 v[6:7], v[164:165], v[20:21], v[6:7] op_sel_hi:[0,1,1]
	v_pk_fma_f32 v[8:9], v[166:167], v[26:27], v[8:9] op_sel_hi:[0,1,1]
	v_pk_fma_f32 v[2:3], v[166:167], v[28:29], v[2:3] op_sel_hi:[0,1,1]
	v_pk_fma_f32 v[10:11], v[166:167], v[30:31], v[10:11] op_sel_hi:[0,1,1]
	v_pk_fma_f32 v[6:7], v[166:167], v[32:33], v[6:7] op_sel_hi:[0,1,1]
	s_and_b32 s20, s42, 0x70
	s_add_i32 s30, s21, -1
	s_add_i32 s31, s10, -2
	s_add_i32 s97, s18, -3
	s_add_i32 s3, s4, -4
	s_add_i32 s63, s91, -5
	s_add_i32 s79, s13, -6
	s_and_b32 s81, vcc_lo, 0x7e
	s_add_i32 s70, s44, s42
	s_add_i32 s76, s44, s21
	s_add_i32 s19, s44, s10
	s_add_i32 s69, s44, s18
	s_add_i32 s53, s44, s4
	s_add_i32 s94, s44, s91
	s_add_i32 s88, s44, s13
	s_add_i32 s45, s65, vcc_lo
	s_lshl_b32 s0, s20, 2
	s_and_b32 s1, s30, 0x7e
	s_and_b32 s20, s31, 0x7c
	s_and_b32 s30, s97, 0x7e
	s_and_b32 s3, s3, 0x78
	s_and_b32 s31, s63, 0x7e
	s_and_b32 s63, s79, 0x7c
	s_lshl_b32 s79, s81, 2
	s_and_b32 s70, s70, 0x78
	s_and_b32 s76, s76, 0x7f
	s_and_b32 s19, s19, 0x7e
	s_and_b32 s69, s69, 0x7f
	s_and_b32 s53, s53, 0x7c
	s_and_b32 s81, s94, 0x7f
	s_and_b32 s88, s88, 0x7e
	s_and_b32 s45, s45, 0x7f
	s_add_i32 s0, s49, s0
	s_lshl_b32 s1, s1, 2
	s_lshl_b32 s20, s20, 2
	s_lshl_b32 s30, s30, 2
	s_lshl_b32 s3, s3, 2
	s_lshl_b32 s31, s31, 2
	s_lshl_b32 s63, s63, 2
	s_add_i32 s79, s49, s79
	s_lshl_b32 s70, s70, 2
	s_lshl_b32 s76, s76, 2
	s_lshl_b32 s19, s19, 2
	s_lshl_b32 s69, s69, 2
	s_lshl_b32 s53, s53, 2
	s_lshl_b32 s81, s81, 2
	s_lshl_b32 s88, s88, 2
	s_lshl_b32 s45, s45, 2
	v_mov_b32_e32 v13, s0
	s_add_i32 s0, s49, s1
	s_add_i32 s1, s49, s20
	s_add_i32 s20, s49, s30
	s_add_i32 s3, s49, s3
	s_add_i32 s30, s49, s31
	s_add_i32 s31, s49, s63
	v_mov_b32_e32 v15, s79
	s_add_i32 s63, s49, s70
	s_add_i32 s70, s49, s76
	s_add_i32 s19, s49, s19
	s_add_i32 s69, s49, s69
	s_add_i32 s53, s49, s53
	s_add_i32 s76, s49, s81
	s_add_i32 s79, s49, s88
	s_add_i32 s45, s49, s45
	v_mov_b32_e32 v19, s1
	v_mov_b32_e32 v20, s20
	v_mov_b32_e32 v24, s3
	v_mov_b32_e32 v25, s30
	v_mov_b32_e32 v26, s31
	v_mov_b32_e32 v27, s63
	v_mov_b32_e32 v28, s70
	v_mov_b32_e32 v29, s19
	v_mov_b32_e32 v30, s69
	v_mov_b32_e32 v31, s53
	v_mov_b32_e32 v32, s76
	v_mov_b32_e32 v33, s79
	v_mov_b32_e32 v17, s0
	v_mov_b32_e32 v40, s45
	ds_read_b32 v18, v13
	ds_read_b32 v21, v15
	ds_read_b32 v22, v17
	ds_read_b32 v19, v19
	ds_read_b32 v23, v20
	ds_read_b32 v24, v24
	ds_read_b32 v20, v25
	ds_read_b32 v25, v26
	ds_read_b32 v26, v27
	ds_read_b32 v28, v28
	ds_read_b32 v27, v29
	ds_read_b32 v29, v30
	ds_read_b32 v30, v31
	ds_read_b32 v32, v32
	ds_read_b32 v31, v33
	ds_read_b32 v33, v40
	s_add_i32 vcc_hi, vcc_hi, 2
	s_add_i32 s21, s21, s11
	s_add_i32 s10, s10, s12
	s_add_i32 s18, s18, s14
	s_add_i32 s4, s4, s15
	s_add_i32 s91, s91, s16
	s_add_i32 s13, s13, s17
	s_add_i32 vcc_lo, vcc_lo, s90
	s_add_i32 s42, s42, s5
	s_waitcnt vmcnt(38) lgkmcnt(0)
; __device__ __forceinline__ void p0_prologue(Frame& F) {
;     ...
; #pragma unroll 2
;             for (int m = 0; m < 128; ++m) { const float wv = wsrc[(size_t)m * 1024];
; #pragma unroll
;                 for (int j = 0; j < 8; ++j) acc8[j] += scr[(m * (c0 + j)) & 127] * wv; }
	v_pk_fma_f32 v[8:9], v[168:169], v[18:19], v[8:9] op_sel_hi:[0,1,1]
	v_pk_fma_f32 v[2:3], v[168:169], v[22:23], v[2:3] op_sel_hi:[0,1,1]
	v_pk_fma_f32 v[10:11], v[168:169], v[24:25], v[10:11] op_sel_hi:[0,1,1]
	v_pk_fma_f32 v[6:7], v[168:169], v[20:21], v[6:7] op_sel_hi:[0,1,1]
	v_pk_fma_f32 v[8:9], v[170:171], v[26:27], v[8:9] op_sel_hi:[0,1,1]
	v_pk_fma_f32 v[2:3], v[170:171], v[28:29], v[2:3] op_sel_hi:[0,1,1]
	v_pk_fma_f32 v[10:11], v[170:171], v[30:31], v[10:11] op_sel_hi:[0,1,1]
	v_pk_fma_f32 v[6:7], v[170:171], v[32:33], v[6:7] op_sel_hi:[0,1,1]
	s_and_b32 s20, s42, 0x70
	s_add_i32 s30, s21, -1
	s_add_i32 s31, s10, -2
	s_add_i32 s97, s18, -3
	s_add_i32 s3, s4, -4
	s_add_i32 s63, s91, -5
	s_add_i32 s79, s13, -6
	s_and_b32 s81, vcc_lo, 0x7e
	s_add_i32 s70, s44, s42
	s_add_i32 s76, s44, s21
	s_add_i32 s19, s44, s10
	s_add_i32 s69, s44, s18
	s_add_i32 s53, s44, s4
	s_add_i32 s94, s44, s91
	s_add_i32 s88, s44, s13
	s_add_i32 s45, s65, vcc_lo
	s_lshl_b32 s0, s20, 2
	s_and_b32 s1, s30, 0x7e
	s_and_b32 s20, s31, 0x7c
	s_and_b32 s30, s97, 0x7e
	s_and_b32 s3, s3, 0x78
	s_and_b32 s31, s63, 0x7e
	s_and_b32 s63, s79, 0x7c
	s_lshl_b32 s79, s81, 2
	s_and_b32 s70, s70, 0x78
	s_and_b32 s76, s76, 0x7f
	s_and_b32 s19, s19, 0x7e
	s_and_b32 s69, s69, 0x7f
	s_and_b32 s53, s53, 0x7c
	s_and_b32 s81, s94, 0x7f
	s_and_b32 s88, s88, 0x7e
	s_and_b32 s45, s45, 0x7f
	s_add_i32 s0, s49, s0
	s_lshl_b32 s1, s1, 2
	s_lshl_b32 s20, s20, 2
	s_lshl_b32 s30, s30, 2
	s_lshl_b32 s3, s3, 2
	s_lshl_b32 s31, s31, 2
	s_lshl_b32 s63, s63, 2
	s_add_i32 s79, s49, s79
	s_lshl_b32 s70, s70, 2
	s_lshl_b32 s76, s76, 2
	s_lshl_b32 s19, s19, 2
	s_lshl_b32 s69, s69, 2
	s_lshl_b32 s53, s53, 2
	s_lshl_b32 s81, s81, 2
	s_lshl_b32 s88, s88, 2
	s_lshl_b32 s45, s45, 2
	v_mov_b32_e32 v13, s0
	s_add_i32 s0, s49, s1
	s_add_i32 s1, s49, s20
	s_add_i32 s20, s49, s30
	s_add_i32 s3, s49, s3
	s_add_i32 s30, s49, s31
	s_add_i32 s31, s49, s63
	v_mov_b32_e32 v15, s79
	s_add_i32 s63, s49, s70
	s_add_i32 s70, s49, s76
	s_add_i32 s19, s49, s19
	s_add_i32 s69, s49, s69
	s_add_i32 s53, s49, s53
	s_add_i32 s76, s49, s81
	s_add_i32 s79, s49, s88
	s_add_i32 s45, s49, s45
	v_mov_b32_e32 v19, s1
	v_mov_b32_e32 v20, s20
	v_mov_b32_e32 v24, s3
	v_mov_b32_e32 v25, s30
	v_mov_b32_e32 v26, s31
	v_mov_b32_e32 v27, s63
	v_mov_b32_e32 v28, s70
	v_mov_b32_e32 v29, s19
	v_mov_b32_e32 v30, s69
	v_mov_b32_e32 v31, s53
	v_mov_b32_e32 v32, s76
	v_mov_b32_e32 v33, s79
	v_mov_b32_e32 v17, s0
	v_mov_b32_e32 v40, s45
	ds_read_b32 v18, v13
	ds_read_b32 v21, v15
	ds_read_b32 v22, v17
	ds_read_b32 v19, v19
	ds_read_b32 v23, v20
	ds_read_b32 v24, v24
	ds_read_b32 v20, v25
	ds_read_b32 v25, v26
	ds_read_b32 v26, v27
	ds_read_b32 v28, v28
	ds_read_b32 v27, v29
	ds_read_b32 v29, v30
	ds_read_b32 v30, v31
	ds_read_b32 v32, v32
	ds_read_b32 v31, v33
	ds_read_b32 v33, v40
	s_add_i32 vcc_hi, vcc_hi, 2
	s_add_i32 s21, s21, s11
	s_add_i32 s10, s10, s12
	s_add_i32 s18, s18, s14
	s_add_i32 s4, s4, s15
	s_add_i32 s91, s91, s16
	s_add_i32 s13, s13, s17
	s_add_i32 vcc_lo, vcc_lo, s90
	s_add_i32 s42, s42, s5
	s_waitcnt vmcnt(36) lgkmcnt(0)
	v_pk_fma_f32 v[8:9], v[172:173], v[18:19], v[8:9] op_sel_hi:[0,1,1]
	v_pk_fma_f32 v[2:3], v[172:173], v[22:23], v[2:3] op_sel_hi:[0,1,1]
	v_pk_fma_f32 v[10:11], v[172:173], v[24:25], v[10:11] op_sel_hi:[0,1,1]
	v_pk_fma_f32 v[6:7], v[172:173], v[20:21], v[6:7] op_sel_hi:[0,1,1]
	v_pk_fma_f32 v[8:9], v[174:175], v[26:27], v[8:9] op_sel_hi:[0,1,1]
	v_pk_fma_f32 v[2:3], v[174:175], v[28:29], v[2:3] op_sel_hi:[0,1,1]
	v_pk_fma_f32 v[10:11], v[174:175], v[30:31], v[10:11] op_sel_hi:[0,1,1]
	v_pk_fma_f32 v[6:7], v[174:175], v[32:33], v[6:7] op_sel_hi:[0,1,1]
	s_and_b32 s20, s42, 0x70
	s_add_i32 s30, s21, -1
	s_add_i32 s31, s10, -2
	s_add_i32 s97, s18, -3
	s_add_i32 s3, s4, -4
	s_add_i32 s63, s91, -5
	s_add_i32 s79, s13, -6
	s_and_b32 s81, vcc_lo, 0x7e
	s_add_i32 s70, s44, s42
	s_add_i32 s76, s44, s21
	s_add_i32 s19, s44, s10
	s_add_i32 s69, s44, s18
	s_add_i32 s53, s44, s4
	s_add_i32 s94, s44, s91
	s_add_i32 s88, s44, s13
	s_add_i32 s45, s65, vcc_lo
	s_lshl_b32 s0, s20, 2
	s_and_b32 s1, s30, 0x7e
	s_and_b32 s20, s31, 0x7c
	s_and_b32 s30, s97, 0x7e
	s_and_b32 s3, s3, 0x78
	s_and_b32 s31, s63, 0x7e
	s_and_b32 s63, s79, 0x7c
	s_lshl_b32 s79, s81, 2
	s_and_b32 s70, s70, 0x78
	s_and_b32 s76, s76, 0x7f
	s_and_b32 s19, s19, 0x7e
	s_and_b32 s69, s69, 0x7f
	s_and_b32 s53, s53, 0x7c
	s_and_b32 s81, s94, 0x7f
	s_and_b32 s88, s88, 0x7e
	s_and_b32 s45, s45, 0x7f
	s_add_i32 s0, s49, s0
	s_lshl_b32 s1, s1, 2
	s_lshl_b32 s20, s20, 2
	s_lshl_b32 s30, s30, 2
	s_lshl_b32 s3, s3, 2
	s_lshl_b32 s31, s31, 2
	s_lshl_b32 s63, s63, 2
	s_add_i32 s79, s49, s79
	s_lshl_b32 s70, s70, 2
	s_lshl_b32 s76, s76, 2
	s_lshl_b32 s19, s19, 2
	s_lshl_b32 s69, s69, 2
	s_lshl_b32 s53, s53, 2
	s_lshl_b32 s81, s81, 2
	s_lshl_b32 s88, s88, 2
	s_lshl_b32 s45, s45, 2
	v_mov_b32_e32 v13, s0
	s_add_i32 s0, s49, s1
	s_add_i32 s1, s49, s20
	s_add_i32 s20, s49, s30
	s_add_i32 s3, s49, s3
	s_add_i32 s30, s49, s31
	s_add_i32 s31, s49, s63
	v_mov_b32_e32 v15, s79
	s_add_i32 s63, s49, s70
	s_add_i32 s70, s49, s76
	s_add_i32 s19, s49, s19
	s_add_i32 s69, s49, s69
	s_add_i32 s53, s49, s53
	s_add_i32 s76, s49, s81
	s_add_i32 s79, s49, s88
	s_add_i32 s45, s49, s45
	v_mov_b32_e32 v19, s1
	v_mov_b32_e32 v20, s20
	v_mov_b32_e32 v24, s3
	v_mov_b32_e32 v25, s30
	v_mov_b32_e32 v26, s31
	v_mov_b32_e32 v27, s63
	v_mov_b32_e32 v28, s70
	v_mov_b32_e32 v29, s19
	v_mov_b32_e32 v30, s69
	v_mov_b32_e32 v31, s53
	v_mov_b32_e32 v32, s76
	v_mov_b32_e32 v33, s79
	v_mov_b32_e32 v17, s0
	v_mov_b32_e32 v40, s45
	ds_read_b32 v18, v13
	ds_read_b32 v21, v15
	ds_read_b32 v22, v17
	ds_read_b32 v19, v19
	ds_read_b32 v23, v20
	ds_read_b32 v24, v24
	ds_read_b32 v20, v25
	ds_read_b32 v25, v26
	ds_read_b32 v26, v27
	ds_read_b32 v28, v28
	ds_read_b32 v27, v29
	ds_read_b32 v29, v30
	ds_read_b32 v30, v31
	ds_read_b32 v32, v32
	ds_read_b32 v31, v33
	ds_read_b32 v33, v40
	s_add_i32 vcc_hi, vcc_hi, 2
	s_add_i32 s21, s21, s11
	s_add_i32 s10, s10, s12
	s_add_i32 s18, s18, s14
	s_add_i32 s4, s4, s15
	s_add_i32 s91, s91, s16
	s_add_i32 s13, s13, s17
	s_add_i32 vcc_lo, vcc_lo, s90
	s_add_i32 s42, s42, s5
	s_waitcnt vmcnt(34) lgkmcnt(0)
; __device__ __forceinline__ void p0_prologue(Frame& F) {
;     ...
; #pragma unroll 2
;             for (int m = 0; m < 128; ++m) { const float wv = wsrc[(size_t)m * 1024];
; #pragma unroll
;                 for (int j = 0; j < 8; ++j) acc8[j] += scr[(m * (c0 + j)) & 127] * wv; }
	v_pk_fma_f32 v[8:9], v[176:177], v[18:19], v[8:9] op_sel_hi:[0,1,1]
	v_pk_fma_f32 v[2:3], v[176:177], v[22:23], v[2:3] op_sel_hi:[0,1,1]
	v_pk_fma_f32 v[10:11], v[176:177], v[24:25], v[10:11] op_sel_hi:[0,1,1]
	v_pk_fma_f32 v[6:7], v[176:177], v[20:21], v[6:7] op_sel_hi:[0,1,1]
	v_pk_fma_f32 v[8:9], v[178:179], v[26:27], v[8:9] op_sel_hi:[0,1,1]
	v_pk_fma_f32 v[2:3], v[178:179], v[28:29], v[2:3] op_sel_hi:[0,1,1]
	v_pk_fma_f32 v[10:11], v[178:179], v[30:31], v[10:11] op_sel_hi:[0,1,1]
	v_pk_fma_f32 v[6:7], v[178:179], v[32:33], v[6:7] op_sel_hi:[0,1,1]
	s_and_b32 s20, s42, 0x70
	s_add_i32 s30, s21, -1
	s_add_i32 s31, s10, -2
	s_add_i32 s97, s18, -3
	s_add_i32 s3, s4, -4
	s_add_i32 s63, s91, -5
	s_add_i32 s79, s13, -6
	s_and_b32 s81, vcc_lo, 0x7e
	s_add_i32 s70, s44, s42
	s_add_i32 s76, s44, s21
	s_add_i32 s19, s44, s10
	s_add_i32 s69, s44, s18
	s_add_i32 s53, s44, s4
	s_add_i32 s94, s44, s91
	s_add_i32 s88, s44, s13
	s_add_i32 s45, s65, vcc_lo
	s_lshl_b32 s0, s20, 2
	s_and_b32 s1, s30, 0x7e
	s_and_b32 s20, s31, 0x7c
	s_and_b32 s30, s97, 0x7e
	s_and_b32 s3, s3, 0x78
	s_and_b32 s31, s63, 0x7e
	s_and_b32 s63, s79, 0x7c
	s_lshl_b32 s79, s81, 2
	s_and_b32 s70, s70, 0x78
	s_and_b32 s76, s76, 0x7f
	s_and_b32 s19, s19, 0x7e
	s_and_b32 s69, s69, 0x7f
	s_and_b32 s53, s53, 0x7c
	s_and_b32 s81, s94, 0x7f
	s_and_b32 s88, s88, 0x7e
	s_and_b32 s45, s45, 0x7f
	s_add_i32 s0, s49, s0
	s_lshl_b32 s1, s1, 2
	s_lshl_b32 s20, s20, 2
	s_lshl_b32 s30, s30, 2
	s_lshl_b32 s3, s3, 2
	s_lshl_b32 s31, s31, 2
	s_lshl_b32 s63, s63, 2
	s_add_i32 s79, s49, s79
	s_lshl_b32 s70, s70, 2
	s_lshl_b32 s76, s76, 2
	s_lshl_b32 s19, s19, 2
	s_lshl_b32 s69, s69, 2
	s_lshl_b32 s53, s53, 2
	s_lshl_b32 s81, s81, 2
	s_lshl_b32 s88, s88, 2
	s_lshl_b32 s45, s45, 2
	v_mov_b32_e32 v13, s0
	s_add_i32 s0, s49, s1
	s_add_i32 s1, s49, s20
	s_add_i32 s20, s49, s30
	s_add_i32 s3, s49, s3
	s_add_i32 s30, s49, s31
	s_add_i32 s31, s49, s63
	v_mov_b32_e32 v15, s79
	s_add_i32 s63, s49, s70
	s_add_i32 s70, s49, s76
	s_add_i32 s19, s49, s19
	s_add_i32 s69, s49, s69
	s_add_i32 s53, s49, s53
	s_add_i32 s76, s49, s81
	s_add_i32 s79, s49, s88
	s_add_i32 s45, s49, s45
	v_mov_b32_e32 v19, s1
	v_mov_b32_e32 v20, s20
	v_mov_b32_e32 v24, s3
	v_mov_b32_e32 v25, s30
	v_mov_b32_e32 v26, s31
	v_mov_b32_e32 v27, s63
	v_mov_b32_e32 v28, s70
	v_mov_b32_e32 v29, s19
	v_mov_b32_e32 v30, s69
	v_mov_b32_e32 v31, s53
	v_mov_b32_e32 v32, s76
	v_mov_b32_e32 v33, s79
	v_mov_b32_e32 v17, s0
	v_mov_b32_e32 v40, s45
	ds_read_b32 v18, v13
	ds_read_b32 v21, v15
	ds_read_b32 v22, v17
	ds_read_b32 v19, v19
	ds_read_b32 v23, v20
	ds_read_b32 v24, v24
	ds_read_b32 v20, v25
	ds_read_b32 v25, v26
	ds_read_b32 v26, v27
	ds_read_b32 v28, v28
	ds_read_b32 v27, v29
	ds_read_b32 v29, v30
	ds_read_b32 v30, v31
	ds_read_b32 v32, v32
	ds_read_b32 v31, v33
	ds_read_b32 v33, v40
	s_add_i32 vcc_hi, vcc_hi, 2
	s_add_i32 s21, s21, s11
	s_add_i32 s10, s10, s12
	s_add_i32 s18, s18, s14
	s_add_i32 s4, s4, s15
	s_add_i32 s91, s91, s16
	s_add_i32 s13, s13, s17
	s_add_i32 vcc_lo, vcc_lo, s90
	s_add_i32 s42, s42, s5
	s_waitcnt vmcnt(32) lgkmcnt(0)
	v_pk_fma_f32 v[8:9], v[180:181], v[18:19], v[8:9] op_sel_hi:[0,1,1]
	v_pk_fma_f32 v[2:3], v[180:181], v[22:23], v[2:3] op_sel_hi:[0,1,1]
	v_pk_fma_f32 v[10:11], v[180:181], v[24:25], v[10:11] op_sel_hi:[0,1,1]
	v_pk_fma_f32 v[6:7], v[180:181], v[20:21], v[6:7] op_sel_hi:[0,1,1]
	v_pk_fma_f32 v[8:9], v[182:183], v[26:27], v[8:9] op_sel_hi:[0,1,1]
	v_pk_fma_f32 v[2:3], v[182:183], v[28:29], v[2:3] op_sel_hi:[0,1,1]
	v_pk_fma_f32 v[10:11], v[182:183], v[30:31], v[10:11] op_sel_hi:[0,1,1]
	v_pk_fma_f32 v[6:7], v[182:183], v[32:33], v[6:7] op_sel_hi:[0,1,1]
	s_and_b32 s20, s42, 0x70
	s_add_i32 s30, s21, -1
	s_add_i32 s31, s10, -2
	s_add_i32 s97, s18, -3
	s_add_i32 s3, s4, -4
	s_add_i32 s63, s91, -5
	s_add_i32 s79, s13, -6
	s_and_b32 s81, vcc_lo, 0x7e
	s_add_i32 s70, s44, s42
	s_add_i32 s76, s44, s21
	s_add_i32 s19, s44, s10
	s_add_i32 s69, s44, s18
	s_add_i32 s53, s44, s4
	s_add_i32 s94, s44, s91
	s_add_i32 s88, s44, s13
	s_add_i32 s45, s65, vcc_lo
	s_lshl_b32 s0, s20, 2
	s_and_b32 s1, s30, 0x7e
	s_and_b32 s20, s31, 0x7c
	s_and_b32 s30, s97, 0x7e
	s_and_b32 s3, s3, 0x78
	s_and_b32 s31, s63, 0x7e
	s_and_b32 s63, s79, 0x7c
	s_lshl_b32 s79, s81, 2
	s_and_b32 s70, s70, 0x78
	s_and_b32 s76, s76, 0x7f
	s_and_b32 s19, s19, 0x7e
	s_and_b32 s69, s69, 0x7f
	s_and_b32 s53, s53, 0x7c
	s_and_b32 s81, s94, 0x7f
	s_and_b32 s88, s88, 0x7e
	s_and_b32 s45, s45, 0x7f
	s_add_i32 s0, s49, s0
	s_lshl_b32 s1, s1, 2
	s_lshl_b32 s20, s20, 2
	s_lshl_b32 s30, s30, 2
	s_lshl_b32 s3, s3, 2
	s_lshl_b32 s31, s31, 2
	s_lshl_b32 s63, s63, 2
	s_add_i32 s79, s49, s79
	s_lshl_b32 s70, s70, 2
	s_lshl_b32 s76, s76, 2
	s_lshl_b32 s19, s19, 2
	s_lshl_b32 s69, s69, 2
	s_lshl_b32 s53, s53, 2
	s_lshl_b32 s81, s81, 2
	s_lshl_b32 s88, s88, 2
	s_lshl_b32 s45, s45, 2
	v_mov_b32_e32 v13, s0
	s_add_i32 s0, s49, s1
	s_add_i32 s1, s49, s20
	s_add_i32 s20, s49, s30
	s_add_i32 s3, s49, s3
	s_add_i32 s30, s49, s31
	s_add_i32 s31, s49, s63
	v_mov_b32_e32 v15, s79
	s_add_i32 s63, s49, s70
	s_add_i32 s70, s49, s76
	s_add_i32 s19, s49, s19
	s_add_i32 s69, s49, s69
	s_add_i32 s53, s49, s53
	s_add_i32 s76, s49, s81
	s_add_i32 s79, s49, s88
	s_add_i32 s45, s49, s45
	v_mov_b32_e32 v19, s1
	v_mov_b32_e32 v20, s20
	v_mov_b32_e32 v24, s3
	v_mov_b32_e32 v25, s30
	v_mov_b32_e32 v26, s31
	v_mov_b32_e32 v27, s63
	v_mov_b32_e32 v28, s70
	v_mov_b32_e32 v29, s19
	v_mov_b32_e32 v30, s69
	v_mov_b32_e32 v31, s53
	v_mov_b32_e32 v32, s76
	v_mov_b32_e32 v33, s79
	v_mov_b32_e32 v17, s0
	v_mov_b32_e32 v40, s45
	ds_read_b32 v18, v13
	ds_read_b32 v21, v15
	ds_read_b32 v22, v17
	ds_read_b32 v19, v19
	ds_read_b32 v23, v20
	ds_read_b32 v24, v24
	ds_read_b32 v20, v25
	ds_read_b32 v25, v26
	ds_read_b32 v26, v27
	ds_read_b32 v28, v28
	ds_read_b32 v27, v29
	ds_read_b32 v29, v30
	ds_read_b32 v30, v31
	ds_read_b32 v32, v32
	ds_read_b32 v31, v33
	ds_read_b32 v33, v40
	s_add_i32 vcc_hi, vcc_hi, 2
	s_add_i32 s21, s21, s11
	s_add_i32 s10, s10, s12
	s_add_i32 s18, s18, s14
	s_add_i32 s4, s4, s15
	s_add_i32 s91, s91, s16
	s_add_i32 s13, s13, s17
	s_add_i32 vcc_lo, vcc_lo, s90
	s_add_i32 s42, s42, s5
	s_waitcnt vmcnt(30) lgkmcnt(0)
; __device__ __forceinline__ void p0_prologue(Frame& F) {
;     ...
; #pragma unroll 2
;             for (int m = 0; m < 128; ++m) { const float wv = wsrc[(size_t)m * 1024];
; #pragma unroll
;                 for (int j = 0; j < 8; ++j) acc8[j] += scr[(m * (c0 + j)) & 127] * wv; }
	v_pk_fma_f32 v[8:9], v[184:185], v[18:19], v[8:9] op_sel_hi:[0,1,1]
	v_pk_fma_f32 v[2:3], v[184:185], v[22:23], v[2:3] op_sel_hi:[0,1,1]
	v_pk_fma_f32 v[10:11], v[184:185], v[24:25], v[10:11] op_sel_hi:[0,1,1]
	v_pk_fma_f32 v[6:7], v[184:185], v[20:21], v[6:7] op_sel_hi:[0,1,1]
	v_pk_fma_f32 v[8:9], v[186:187], v[26:27], v[8:9] op_sel_hi:[0,1,1]
	v_pk_fma_f32 v[2:3], v[186:187], v[28:29], v[2:3] op_sel_hi:[0,1,1]
	v_pk_fma_f32 v[10:11], v[186:187], v[30:31], v[10:11] op_sel_hi:[0,1,1]
	v_pk_fma_f32 v[6:7], v[186:187], v[32:33], v[6:7] op_sel_hi:[0,1,1]
	s_and_b32 s20, s42, 0x70
	s_add_i32 s30, s21, -1
	s_add_i32 s31, s10, -2
	s_add_i32 s97, s18, -3
	s_add_i32 s3, s4, -4
	s_add_i32 s63, s91, -5
	s_add_i32 s79, s13, -6
	s_and_b32 s81, vcc_lo, 0x7e
	s_add_i32 s70, s44, s42
	s_add_i32 s76, s44, s21
	s_add_i32 s19, s44, s10
	s_add_i32 s69, s44, s18
	s_add_i32 s53, s44, s4
	s_add_i32 s94, s44, s91
	s_add_i32 s88, s44, s13
	s_add_i32 s45, s65, vcc_lo
	s_lshl_b32 s0, s20, 2
	s_and_b32 s1, s30, 0x7e
	s_and_b32 s20, s31, 0x7c
	s_and_b32 s30, s97, 0x7e
	s_and_b32 s3, s3, 0x78
	s_and_b32 s31, s63, 0x7e
	s_and_b32 s63, s79, 0x7c
	s_lshl_b32 s79, s81, 2
	s_and_b32 s70, s70, 0x78
	s_and_b32 s76, s76, 0x7f
	s_and_b32 s19, s19, 0x7e
	s_and_b32 s69, s69, 0x7f
	s_and_b32 s53, s53, 0x7c
	s_and_b32 s81, s94, 0x7f
	s_and_b32 s88, s88, 0x7e
	s_and_b32 s45, s45, 0x7f
	s_add_i32 s0, s49, s0
	s_lshl_b32 s1, s1, 2
	s_lshl_b32 s20, s20, 2
	s_lshl_b32 s30, s30, 2
	s_lshl_b32 s3, s3, 2
	s_lshl_b32 s31, s31, 2
	s_lshl_b32 s63, s63, 2
	s_add_i32 s79, s49, s79
	s_lshl_b32 s70, s70, 2
	s_lshl_b32 s76, s76, 2
	s_lshl_b32 s19, s19, 2
	s_lshl_b32 s69, s69, 2
	s_lshl_b32 s53, s53, 2
	s_lshl_b32 s81, s81, 2
	s_lshl_b32 s88, s88, 2
	s_lshl_b32 s45, s45, 2
	v_mov_b32_e32 v13, s0
	s_add_i32 s0, s49, s1
	s_add_i32 s1, s49, s20
	s_add_i32 s20, s49, s30
	s_add_i32 s3, s49, s3
	s_add_i32 s30, s49, s31
	s_add_i32 s31, s49, s63
	v_mov_b32_e32 v15, s79
	s_add_i32 s63, s49, s70
	s_add_i32 s70, s49, s76
	s_add_i32 s19, s49, s19
	s_add_i32 s69, s49, s69
	s_add_i32 s53, s49, s53
	s_add_i32 s76, s49, s81
	s_add_i32 s79, s49, s88
	s_add_i32 s45, s49, s45
	v_mov_b32_e32 v19, s1
	v_mov_b32_e32 v20, s20
	v_mov_b32_e32 v24, s3
	v_mov_b32_e32 v25, s30
	v_mov_b32_e32 v26, s31
	v_mov_b32_e32 v27, s63
	v_mov_b32_e32 v28, s70
	v_mov_b32_e32 v29, s19
	v_mov_b32_e32 v30, s69
	v_mov_b32_e32 v31, s53
	v_mov_b32_e32 v32, s76
	v_mov_b32_e32 v33, s79
	v_mov_b32_e32 v17, s0
	v_mov_b32_e32 v40, s45
	ds_read_b32 v18, v13
	ds_read_b32 v21, v15
	ds_read_b32 v22, v17
	ds_read_b32 v19, v19
	ds_read_b32 v23, v20
	ds_read_b32 v24, v24
	ds_read_b32 v20, v25
	ds_read_b32 v25, v26
	ds_read_b32 v26, v27
	ds_read_b32 v28, v28
	ds_read_b32 v27, v29
	ds_read_b32 v29, v30
	ds_read_b32 v30, v31
	ds_read_b32 v32, v32
	ds_read_b32 v31, v33
	ds_read_b32 v33, v40
	s_add_i32 vcc_hi, vcc_hi, 2
	s_add_i32 s21, s21, s11
	s_add_i32 s10, s10, s12
	s_add_i32 s18, s18, s14
	s_add_i32 s4, s4, s15
	s_add_i32 s91, s91, s16
	s_add_i32 s13, s13, s17
	s_add_i32 vcc_lo, vcc_lo, s90
	s_add_i32 s42, s42, s5
	s_waitcnt vmcnt(28) lgkmcnt(0)
	v_pk_fma_f32 v[8:9], v[188:189], v[18:19], v[8:9] op_sel_hi:[0,1,1]
	v_pk_fma_f32 v[2:3], v[188:189], v[22:23], v[2:3] op_sel_hi:[0,1,1]
	v_pk_fma_f32 v[10:11], v[188:189], v[24:25], v[10:11] op_sel_hi:[0,1,1]
	v_pk_fma_f32 v[6:7], v[188:189], v[20:21], v[6:7] op_sel_hi:[0,1,1]
	v_pk_fma_f32 v[8:9], v[190:191], v[26:27], v[8:9] op_sel_hi:[0,1,1]
	v_pk_fma_f32 v[2:3], v[190:191], v[28:29], v[2:3] op_sel_hi:[0,1,1]
	v_pk_fma_f32 v[10:11], v[190:191], v[30:31], v[10:11] op_sel_hi:[0,1,1]
	v_pk_fma_f32 v[6:7], v[190:191], v[32:33], v[6:7] op_sel_hi:[0,1,1]
	s_and_b32 s20, s42, 0x70
	s_add_i32 s30, s21, -1
	s_add_i32 s31, s10, -2
	s_add_i32 s97, s18, -3
	s_add_i32 s3, s4, -4
	s_add_i32 s63, s91, -5
	s_add_i32 s79, s13, -6
	s_and_b32 s81, vcc_lo, 0x7e
	s_add_i32 s70, s44, s42
	s_add_i32 s76, s44, s21
	s_add_i32 s19, s44, s10
	s_add_i32 s69, s44, s18
	s_add_i32 s53, s44, s4
	s_add_i32 s94, s44, s91
	s_add_i32 s88, s44, s13
	s_add_i32 s45, s65, vcc_lo
	s_lshl_b32 s0, s20, 2
	s_and_b32 s1, s30, 0x7e
	s_and_b32 s20, s31, 0x7c
	s_and_b32 s30, s97, 0x7e
	s_and_b32 s3, s3, 0x78
	s_and_b32 s31, s63, 0x7e
	s_and_b32 s63, s79, 0x7c
	s_lshl_b32 s79, s81, 2
	s_and_b32 s70, s70, 0x78
	s_and_b32 s76, s76, 0x7f
	s_and_b32 s19, s19, 0x7e
	s_and_b32 s69, s69, 0x7f
	s_and_b32 s53, s53, 0x7c
	s_and_b32 s81, s94, 0x7f
	s_and_b32 s88, s88, 0x7e
	s_and_b32 s45, s45, 0x7f
	s_add_i32 s0, s49, s0
	s_lshl_b32 s1, s1, 2
	s_lshl_b32 s20, s20, 2
	s_lshl_b32 s30, s30, 2
	s_lshl_b32 s3, s3, 2
	s_lshl_b32 s31, s31, 2
	s_lshl_b32 s63, s63, 2
	s_add_i32 s79, s49, s79
	s_lshl_b32 s70, s70, 2
	s_lshl_b32 s76, s76, 2
	s_lshl_b32 s19, s19, 2
	s_lshl_b32 s69, s69, 2
	s_lshl_b32 s53, s53, 2
	s_lshl_b32 s81, s81, 2
	s_lshl_b32 s88, s88, 2
	s_lshl_b32 s45, s45, 2
	v_mov_b32_e32 v13, s0
	s_add_i32 s0, s49, s1
	s_add_i32 s1, s49, s20
	s_add_i32 s20, s49, s30
	s_add_i32 s3, s49, s3
	s_add_i32 s30, s49, s31
	s_add_i32 s31, s49, s63
	v_mov_b32_e32 v15, s79
	s_add_i32 s63, s49, s70
	s_add_i32 s70, s49, s76
	s_add_i32 s19, s49, s19
	s_add_i32 s69, s49, s69
	s_add_i32 s53, s49, s53
	s_add_i32 s76, s49, s81
	s_add_i32 s79, s49, s88
	s_add_i32 s45, s49, s45
	v_mov_b32_e32 v19, s1
	v_mov_b32_e32 v20, s20
	v_mov_b32_e32 v24, s3
	v_mov_b32_e32 v25, s30
	v_mov_b32_e32 v26, s31
	v_mov_b32_e32 v27, s63
	v_mov_b32_e32 v28, s70
	v_mov_b32_e32 v29, s19
	v_mov_b32_e32 v30, s69
	v_mov_b32_e32 v31, s53
	v_mov_b32_e32 v32, s76
	v_mov_b32_e32 v33, s79
	v_mov_b32_e32 v17, s0
	v_mov_b32_e32 v40, s45
	ds_read_b32 v18, v13
	ds_read_b32 v21, v15
	ds_read_b32 v22, v17
	ds_read_b32 v19, v19
	ds_read_b32 v23, v20
	ds_read_b32 v24, v24
	ds_read_b32 v20, v25
	ds_read_b32 v25, v26
	ds_read_b32 v26, v27
	ds_read_b32 v28, v28
	ds_read_b32 v27, v29
	ds_read_b32 v29, v30
	ds_read_b32 v30, v31
	ds_read_b32 v32, v32
	ds_read_b32 v31, v33
	ds_read_b32 v33, v40
	s_add_i32 vcc_hi, vcc_hi, 2
	s_add_i32 s21, s21, s11
	s_add_i32 s10, s10, s12
	s_add_i32 s18, s18, s14
	s_add_i32 s4, s4, s15
	s_add_i32 s91, s91, s16
	s_add_i32 s13, s13, s17
	s_add_i32 vcc_lo, vcc_lo, s90
	s_add_i32 s42, s42, s5
	s_waitcnt vmcnt(26) lgkmcnt(0)
; __device__ __forceinline__ void p0_prologue(Frame& F) {
;     ...
; #pragma unroll 2
;             for (int m = 0; m < 128; ++m) { const float wv = wsrc[(size_t)m * 1024];
; #pragma unroll
;                 for (int j = 0; j < 8; ++j) acc8[j] += scr[(m * (c0 + j)) & 127] * wv; }
	v_pk_fma_f32 v[8:9], v[192:193], v[18:19], v[8:9] op_sel_hi:[0,1,1]
	v_pk_fma_f32 v[2:3], v[192:193], v[22:23], v[2:3] op_sel_hi:[0,1,1]
	v_pk_fma_f32 v[10:11], v[192:193], v[24:25], v[10:11] op_sel_hi:[0,1,1]
	v_pk_fma_f32 v[6:7], v[192:193], v[20:21], v[6:7] op_sel_hi:[0,1,1]
	v_pk_fma_f32 v[8:9], v[194:195], v[26:27], v[8:9] op_sel_hi:[0,1,1]
	v_pk_fma_f32 v[2:3], v[194:195], v[28:29], v[2:3] op_sel_hi:[0,1,1]
	v_pk_fma_f32 v[10:11], v[194:195], v[30:31], v[10:11] op_sel_hi:[0,1,1]
	v_pk_fma_f32 v[6:7], v[194:195], v[32:33], v[6:7] op_sel_hi:[0,1,1]
	s_and_b32 s20, s42, 0x70
	s_add_i32 s30, s21, -1
	s_add_i32 s31, s10, -2
	s_add_i32 s97, s18, -3
	s_add_i32 s3, s4, -4
	s_add_i32 s63, s91, -5
	s_add_i32 s79, s13, -6
	s_and_b32 s81, vcc_lo, 0x7e
	s_add_i32 s70, s44, s42
	s_add_i32 s76, s44, s21
	s_add_i32 s19, s44, s10
	s_add_i32 s69, s44, s18
	s_add_i32 s53, s44, s4
	s_add_i32 s94, s44, s91
	s_add_i32 s88, s44, s13
	s_add_i32 s45, s65, vcc_lo
	s_lshl_b32 s0, s20, 2
	s_and_b32 s1, s30, 0x7e
	s_and_b32 s20, s31, 0x7c
	s_and_b32 s30, s97, 0x7e
	s_and_b32 s3, s3, 0x78
	s_and_b32 s31, s63, 0x7e
	s_and_b32 s63, s79, 0x7c
	s_lshl_b32 s79, s81, 2
	s_and_b32 s70, s70, 0x78
	s_and_b32 s76, s76, 0x7f
	s_and_b32 s19, s19, 0x7e
	s_and_b32 s69, s69, 0x7f
	s_and_b32 s53, s53, 0x7c
	s_and_b32 s81, s94, 0x7f
	s_and_b32 s88, s88, 0x7e
	s_and_b32 s45, s45, 0x7f
	s_add_i32 s0, s49, s0
	s_lshl_b32 s1, s1, 2
	s_lshl_b32 s20, s20, 2
	s_lshl_b32 s30, s30, 2
	s_lshl_b32 s3, s3, 2
	s_lshl_b32 s31, s31, 2
	s_lshl_b32 s63, s63, 2
	s_add_i32 s79, s49, s79
	s_lshl_b32 s70, s70, 2
	s_lshl_b32 s76, s76, 2
	s_lshl_b32 s19, s19, 2
	s_lshl_b32 s69, s69, 2
	s_lshl_b32 s53, s53, 2
	s_lshl_b32 s81, s81, 2
	s_lshl_b32 s88, s88, 2
	s_lshl_b32 s45, s45, 2
	v_mov_b32_e32 v13, s0
	s_add_i32 s0, s49, s1
	s_add_i32 s1, s49, s20
	s_add_i32 s20, s49, s30
	s_add_i32 s3, s49, s3
	s_add_i32 s30, s49, s31
	s_add_i32 s31, s49, s63
	v_mov_b32_e32 v15, s79
	s_add_i32 s63, s49, s70
	s_add_i32 s70, s49, s76
	s_add_i32 s19, s49, s19
	s_add_i32 s69, s49, s69
	s_add_i32 s53, s49, s53
	s_add_i32 s76, s49, s81
	s_add_i32 s79, s49, s88
	s_add_i32 s45, s49, s45
	v_mov_b32_e32 v19, s1
	v_mov_b32_e32 v20, s20
	v_mov_b32_e32 v24, s3
	v_mov_b32_e32 v25, s30
	v_mov_b32_e32 v26, s31
	v_mov_b32_e32 v27, s63
	v_mov_b32_e32 v28, s70
	v_mov_b32_e32 v29, s19
	v_mov_b32_e32 v30, s69
	v_mov_b32_e32 v31, s53
	v_mov_b32_e32 v32, s76
	v_mov_b32_e32 v33, s79
	v_mov_b32_e32 v17, s0
	v_mov_b32_e32 v40, s45
	ds_read_b32 v18, v13
	ds_read_b32 v21, v15
	ds_read_b32 v22, v17
	ds_read_b32 v19, v19
	ds_read_b32 v23, v20
	ds_read_b32 v24, v24
	ds_read_b32 v20, v25
	ds_read_b32 v25, v26
	ds_read_b32 v26, v27
	ds_read_b32 v28, v28
	ds_read_b32 v27, v29
	ds_read_b32 v29, v30
	ds_read_b32 v30, v31
	ds_read_b32 v32, v32
	ds_read_b32 v31, v33
	ds_read_b32 v33, v40
	s_add_i32 vcc_hi, vcc_hi, 2
	s_add_i32 s21, s21, s11
	s_add_i32 s10, s10, s12
	s_add_i32 s18, s18, s14
	s_add_i32 s4, s4, s15
	s_add_i32 s91, s91, s16
	s_add_i32 s13, s13, s17
	s_add_i32 vcc_lo, vcc_lo, s90
	s_add_i32 s42, s42, s5
	s_waitcnt vmcnt(24) lgkmcnt(0)
	v_pk_fma_f32 v[8:9], v[196:197], v[18:19], v[8:9] op_sel_hi:[0,1,1]
	v_pk_fma_f32 v[2:3], v[196:197], v[22:23], v[2:3] op_sel_hi:[0,1,1]
	v_pk_fma_f32 v[10:11], v[196:197], v[24:25], v[10:11] op_sel_hi:[0,1,1]
	v_pk_fma_f32 v[6:7], v[196:197], v[20:21], v[6:7] op_sel_hi:[0,1,1]
	v_pk_fma_f32 v[8:9], v[198:199], v[26:27], v[8:9] op_sel_hi:[0,1,1]
	v_pk_fma_f32 v[2:3], v[198:199], v[28:29], v[2:3] op_sel_hi:[0,1,1]
	v_pk_fma_f32 v[10:11], v[198:199], v[30:31], v[10:11] op_sel_hi:[0,1,1]
	v_pk_fma_f32 v[6:7], v[198:199], v[32:33], v[6:7] op_sel_hi:[0,1,1]
	s_and_b32 s20, s42, 0x70
	s_add_i32 s30, s21, -1
	s_add_i32 s31, s10, -2
	s_add_i32 s97, s18, -3
	s_add_i32 s3, s4, -4
	s_add_i32 s63, s91, -5
	s_add_i32 s79, s13, -6
	s_and_b32 s81, vcc_lo, 0x7e
	s_add_i32 s70, s44, s42
	s_add_i32 s76, s44, s21
	s_add_i32 s19, s44, s10
	s_add_i32 s69, s44, s18
	s_add_i32 s53, s44, s4
	s_add_i32 s94, s44, s91
	s_add_i32 s88, s44, s13
	s_add_i32 s45, s65, vcc_lo
	s_lshl_b32 s0, s20, 2
	s_and_b32 s1, s30, 0x7e
	s_and_b32 s20, s31, 0x7c
	s_and_b32 s30, s97, 0x7e
	s_and_b32 s3, s3, 0x78
	s_and_b32 s31, s63, 0x7e
	s_and_b32 s63, s79, 0x7c
	s_lshl_b32 s79, s81, 2
	s_and_b32 s70, s70, 0x78
	s_and_b32 s76, s76, 0x7f
	s_and_b32 s19, s19, 0x7e
	s_and_b32 s69, s69, 0x7f
	s_and_b32 s53, s53, 0x7c
	s_and_b32 s81, s94, 0x7f
	s_and_b32 s88, s88, 0x7e
	s_and_b32 s45, s45, 0x7f
	s_add_i32 s0, s49, s0
	s_lshl_b32 s1, s1, 2
	s_lshl_b32 s20, s20, 2
	s_lshl_b32 s30, s30, 2
	s_lshl_b32 s3, s3, 2
	s_lshl_b32 s31, s31, 2
	s_lshl_b32 s63, s63, 2
	s_add_i32 s79, s49, s79
	s_lshl_b32 s70, s70, 2
	s_lshl_b32 s76, s76, 2
	s_lshl_b32 s19, s19, 2
	s_lshl_b32 s69, s69, 2
	s_lshl_b32 s53, s53, 2
	s_lshl_b32 s81, s81, 2
	s_lshl_b32 s88, s88, 2
	s_lshl_b32 s45, s45, 2
	v_mov_b32_e32 v13, s0
	s_add_i32 s0, s49, s1
	s_add_i32 s1, s49, s20
	s_add_i32 s20, s49, s30
	s_add_i32 s3, s49, s3
	s_add_i32 s30, s49, s31
	s_add_i32 s31, s49, s63
	v_mov_b32_e32 v15, s79
	s_add_i32 s63, s49, s70
	s_add_i32 s70, s49, s76
	s_add_i32 s19, s49, s19
	s_add_i32 s69, s49, s69
	s_add_i32 s53, s49, s53
	s_add_i32 s76, s49, s81
	s_add_i32 s79, s49, s88
	s_add_i32 s45, s49, s45
	v_mov_b32_e32 v19, s1
	v_mov_b32_e32 v20, s20
	v_mov_b32_e32 v24, s3
	v_mov_b32_e32 v25, s30
	v_mov_b32_e32 v26, s31
	v_mov_b32_e32 v27, s63
	v_mov_b32_e32 v28, s70
	v_mov_b32_e32 v29, s19
	v_mov_b32_e32 v30, s69
	v_mov_b32_e32 v31, s53
	v_mov_b32_e32 v32, s76
	v_mov_b32_e32 v33, s79
	v_mov_b32_e32 v17, s0
	v_mov_b32_e32 v40, s45
	ds_read_b32 v18, v13
	ds_read_b32 v21, v15
	ds_read_b32 v22, v17
	ds_read_b32 v19, v19
	ds_read_b32 v23, v20
	ds_read_b32 v24, v24
	ds_read_b32 v20, v25
	ds_read_b32 v25, v26
	ds_read_b32 v26, v27
	ds_read_b32 v28, v28
	ds_read_b32 v27, v29
	ds_read_b32 v29, v30
	ds_read_b32 v30, v31
	ds_read_b32 v32, v32
	ds_read_b32 v31, v33
	ds_read_b32 v33, v40
	s_add_i32 vcc_hi, vcc_hi, 2
	s_add_i32 s21, s21, s11
	s_add_i32 s10, s10, s12
	s_add_i32 s18, s18, s14
	s_add_i32 s4, s4, s15
	s_add_i32 s91, s91, s16
	s_add_i32 s13, s13, s17
	s_add_i32 vcc_lo, vcc_lo, s90
	s_add_i32 s42, s42, s5
	s_waitcnt vmcnt(22) lgkmcnt(0)
; __device__ __forceinline__ void p0_prologue(Frame& F) {
;     ...
; #pragma unroll 2
;             for (int m = 0; m < 128; ++m) { const float wv = wsrc[(size_t)m * 1024];
; #pragma unroll
;                 for (int j = 0; j < 8; ++j) acc8[j] += scr[(m * (c0 + j)) & 127] * wv; }
	v_pk_fma_f32 v[8:9], v[200:201], v[18:19], v[8:9] op_sel_hi:[0,1,1]
	v_pk_fma_f32 v[2:3], v[200:201], v[22:23], v[2:3] op_sel_hi:[0,1,1]
	v_pk_fma_f32 v[10:11], v[200:201], v[24:25], v[10:11] op_sel_hi:[0,1,1]
	v_pk_fma_f32 v[6:7], v[200:201], v[20:21], v[6:7] op_sel_hi:[0,1,1]
	v_pk_fma_f32 v[8:9], v[202:203], v[26:27], v[8:9] op_sel_hi:[0,1,1]
	v_pk_fma_f32 v[2:3], v[202:203], v[28:29], v[2:3] op_sel_hi:[0,1,1]
	v_pk_fma_f32 v[10:11], v[202:203], v[30:31], v[10:11] op_sel_hi:[0,1,1]
	v_pk_fma_f32 v[6:7], v[202:203], v[32:33], v[6:7] op_sel_hi:[0,1,1]
	s_and_b32 s20, s42, 0x70
	s_add_i32 s30, s21, -1
	s_add_i32 s31, s10, -2
	s_add_i32 s97, s18, -3
	s_add_i32 s3, s4, -4
	s_add_i32 s63, s91, -5
	s_add_i32 s79, s13, -6
	s_and_b32 s81, vcc_lo, 0x7e
	s_add_i32 s70, s44, s42
	s_add_i32 s76, s44, s21
	s_add_i32 s19, s44, s10
	s_add_i32 s69, s44, s18
	s_add_i32 s53, s44, s4
	s_add_i32 s94, s44, s91
	s_add_i32 s88, s44, s13
	s_add_i32 s45, s65, vcc_lo
	s_lshl_b32 s0, s20, 2
	s_and_b32 s1, s30, 0x7e
	s_and_b32 s20, s31, 0x7c
	s_and_b32 s30, s97, 0x7e
	s_and_b32 s3, s3, 0x78
	s_and_b32 s31, s63, 0x7e
	s_and_b32 s63, s79, 0x7c
	s_lshl_b32 s79, s81, 2
	s_and_b32 s70, s70, 0x78
	s_and_b32 s76, s76, 0x7f
	s_and_b32 s19, s19, 0x7e
	s_and_b32 s69, s69, 0x7f
	s_and_b32 s53, s53, 0x7c
	s_and_b32 s81, s94, 0x7f
	s_and_b32 s88, s88, 0x7e
	s_and_b32 s45, s45, 0x7f
	s_add_i32 s0, s49, s0
	s_lshl_b32 s1, s1, 2
	s_lshl_b32 s20, s20, 2
	s_lshl_b32 s30, s30, 2
	s_lshl_b32 s3, s3, 2
	s_lshl_b32 s31, s31, 2
	s_lshl_b32 s63, s63, 2
	s_add_i32 s79, s49, s79
	s_lshl_b32 s70, s70, 2
	s_lshl_b32 s76, s76, 2
	s_lshl_b32 s19, s19, 2
	s_lshl_b32 s69, s69, 2
	s_lshl_b32 s53, s53, 2
	s_lshl_b32 s81, s81, 2
	s_lshl_b32 s88, s88, 2
	s_lshl_b32 s45, s45, 2
	v_mov_b32_e32 v13, s0
	s_add_i32 s0, s49, s1
	s_add_i32 s1, s49, s20
	s_add_i32 s20, s49, s30
	s_add_i32 s3, s49, s3
	s_add_i32 s30, s49, s31
	s_add_i32 s31, s49, s63
	v_mov_b32_e32 v15, s79
	s_add_i32 s63, s49, s70
	s_add_i32 s70, s49, s76
	s_add_i32 s19, s49, s19
	s_add_i32 s69, s49, s69
	s_add_i32 s53, s49, s53
	s_add_i32 s76, s49, s81
	s_add_i32 s79, s49, s88
	s_add_i32 s45, s49, s45
	v_mov_b32_e32 v19, s1
	v_mov_b32_e32 v20, s20
	v_mov_b32_e32 v24, s3
	v_mov_b32_e32 v25, s30
	v_mov_b32_e32 v26, s31
	v_mov_b32_e32 v27, s63
	v_mov_b32_e32 v28, s70
	v_mov_b32_e32 v29, s19
	v_mov_b32_e32 v30, s69
	v_mov_b32_e32 v31, s53
	v_mov_b32_e32 v32, s76
	v_mov_b32_e32 v33, s79
	v_mov_b32_e32 v17, s0
	v_mov_b32_e32 v40, s45
	ds_read_b32 v18, v13
	ds_read_b32 v21, v15
	ds_read_b32 v22, v17
	ds_read_b32 v19, v19
	ds_read_b32 v23, v20
	ds_read_b32 v24, v24
	ds_read_b32 v20, v25
	ds_read_b32 v25, v26
	ds_read_b32 v26, v27
	ds_read_b32 v28, v28
	ds_read_b32 v27, v29
	ds_read_b32 v29, v30
	ds_read_b32 v30, v31
	ds_read_b32 v32, v32
	ds_read_b32 v31, v33
	ds_read_b32 v33, v40
	s_add_i32 vcc_hi, vcc_hi, 2
	s_add_i32 s21, s21, s11
	s_add_i32 s10, s10, s12
	s_add_i32 s18, s18, s14
	s_add_i32 s4, s4, s15
	s_add_i32 s91, s91, s16
	s_add_i32 s13, s13, s17
	s_add_i32 vcc_lo, vcc_lo, s90
	s_add_i32 s42, s42, s5
	s_waitcnt vmcnt(20) lgkmcnt(0)
	v_pk_fma_f32 v[8:9], v[204:205], v[18:19], v[8:9] op_sel_hi:[0,1,1]
	v_pk_fma_f32 v[2:3], v[204:205], v[22:23], v[2:3] op_sel_hi:[0,1,1]
	v_pk_fma_f32 v[10:11], v[204:205], v[24:25], v[10:11] op_sel_hi:[0,1,1]
	v_pk_fma_f32 v[6:7], v[204:205], v[20:21], v[6:7] op_sel_hi:[0,1,1]
	v_pk_fma_f32 v[8:9], v[206:207], v[26:27], v[8:9] op_sel_hi:[0,1,1]
	v_pk_fma_f32 v[2:3], v[206:207], v[28:29], v[2:3] op_sel_hi:[0,1,1]
	v_pk_fma_f32 v[10:11], v[206:207], v[30:31], v[10:11] op_sel_hi:[0,1,1]
	v_pk_fma_f32 v[6:7], v[206:207], v[32:33], v[6:7] op_sel_hi:[0,1,1]
	s_and_b32 s20, s42, 0x70
	s_add_i32 s30, s21, -1
	s_add_i32 s31, s10, -2
	s_add_i32 s97, s18, -3
	s_add_i32 s3, s4, -4
	s_add_i32 s63, s91, -5
	s_add_i32 s79, s13, -6
	s_and_b32 s81, vcc_lo, 0x7e
	s_add_i32 s70, s44, s42
	s_add_i32 s76, s44, s21
	s_add_i32 s19, s44, s10
	s_add_i32 s69, s44, s18
	s_add_i32 s53, s44, s4
	s_add_i32 s94, s44, s91
	s_add_i32 s88, s44, s13
	s_add_i32 s45, s65, vcc_lo
	s_lshl_b32 s0, s20, 2
	s_and_b32 s1, s30, 0x7e
	s_and_b32 s20, s31, 0x7c
	s_and_b32 s30, s97, 0x7e
	s_and_b32 s3, s3, 0x78
	s_and_b32 s31, s63, 0x7e
	s_and_b32 s63, s79, 0x7c
	s_lshl_b32 s79, s81, 2
	s_and_b32 s70, s70, 0x78
	s_and_b32 s76, s76, 0x7f
	s_and_b32 s19, s19, 0x7e
	s_and_b32 s69, s69, 0x7f
	s_and_b32 s53, s53, 0x7c
	s_and_b32 s81, s94, 0x7f
	s_and_b32 s88, s88, 0x7e
	s_and_b32 s45, s45, 0x7f
	s_add_i32 s0, s49, s0
	s_lshl_b32 s1, s1, 2
	s_lshl_b32 s20, s20, 2
	s_lshl_b32 s30, s30, 2
	s_lshl_b32 s3, s3, 2
	s_lshl_b32 s31, s31, 2
	s_lshl_b32 s63, s63, 2
	s_add_i32 s79, s49, s79
	s_lshl_b32 s70, s70, 2
	s_lshl_b32 s76, s76, 2
	s_lshl_b32 s19, s19, 2
	s_lshl_b32 s69, s69, 2
	s_lshl_b32 s53, s53, 2
	s_lshl_b32 s81, s81, 2
	s_lshl_b32 s88, s88, 2
	s_lshl_b32 s45, s45, 2
	v_mov_b32_e32 v13, s0
	s_add_i32 s0, s49, s1
	s_add_i32 s1, s49, s20
	s_add_i32 s20, s49, s30
	s_add_i32 s3, s49, s3
	s_add_i32 s30, s49, s31
	s_add_i32 s31, s49, s63
	v_mov_b32_e32 v15, s79
	s_add_i32 s63, s49, s70
	s_add_i32 s70, s49, s76
	s_add_i32 s19, s49, s19
	s_add_i32 s69, s49, s69
	s_add_i32 s53, s49, s53
	s_add_i32 s76, s49, s81
	s_add_i32 s79, s49, s88
	s_add_i32 s45, s49, s45
	v_mov_b32_e32 v19, s1
	v_mov_b32_e32 v20, s20
	v_mov_b32_e32 v24, s3
	v_mov_b32_e32 v25, s30
	v_mov_b32_e32 v26, s31
	v_mov_b32_e32 v27, s63
	v_mov_b32_e32 v28, s70
	v_mov_b32_e32 v29, s19
	v_mov_b32_e32 v30, s69
	v_mov_b32_e32 v31, s53
	v_mov_b32_e32 v32, s76
	v_mov_b32_e32 v33, s79
	v_mov_b32_e32 v17, s0
	v_mov_b32_e32 v40, s45
	ds_read_b32 v18, v13
	ds_read_b32 v21, v15
	ds_read_b32 v22, v17
	ds_read_b32 v19, v19
	ds_read_b32 v23, v20
	ds_read_b32 v24, v24
	ds_read_b32 v20, v25
	ds_read_b32 v25, v26
	ds_read_b32 v26, v27
	ds_read_b32 v28, v28
	ds_read_b32 v27, v29
	ds_read_b32 v29, v30
	ds_read_b32 v30, v31
	ds_read_b32 v32, v32
	ds_read_b32 v31, v33
	ds_read_b32 v33, v40
	s_add_i32 vcc_hi, vcc_hi, 2
	s_add_i32 s21, s21, s11
	s_add_i32 s10, s10, s12
	s_add_i32 s18, s18, s14
	s_add_i32 s4, s4, s15
	s_add_i32 s91, s91, s16
	s_add_i32 s13, s13, s17
	s_add_i32 vcc_lo, vcc_lo, s90
	s_add_i32 s42, s42, s5
	s_waitcnt vmcnt(18) lgkmcnt(0)
; __device__ __forceinline__ void p0_prologue(Frame& F) {
;     ...
; #pragma unroll 2
;             for (int m = 0; m < 128; ++m) { const float wv = wsrc[(size_t)m * 1024];
; #pragma unroll
;                 for (int j = 0; j < 8; ++j) acc8[j] += scr[(m * (c0 + j)) & 127] * wv; }
	v_pk_fma_f32 v[8:9], v[208:209], v[18:19], v[8:9] op_sel_hi:[0,1,1]
	v_pk_fma_f32 v[2:3], v[208:209], v[22:23], v[2:3] op_sel_hi:[0,1,1]
	v_pk_fma_f32 v[10:11], v[208:209], v[24:25], v[10:11] op_sel_hi:[0,1,1]
	v_pk_fma_f32 v[6:7], v[208:209], v[20:21], v[6:7] op_sel_hi:[0,1,1]
	v_pk_fma_f32 v[8:9], v[210:211], v[26:27], v[8:9] op_sel_hi:[0,1,1]
	v_pk_fma_f32 v[2:3], v[210:211], v[28:29], v[2:3] op_sel_hi:[0,1,1]
	v_pk_fma_f32 v[10:11], v[210:211], v[30:31], v[10:11] op_sel_hi:[0,1,1]
	v_pk_fma_f32 v[6:7], v[210:211], v[32:33], v[6:7] op_sel_hi:[0,1,1]
	s_and_b32 s20, s42, 0x70
	s_add_i32 s30, s21, -1
	s_add_i32 s31, s10, -2
	s_add_i32 s97, s18, -3
	s_add_i32 s3, s4, -4
	s_add_i32 s63, s91, -5
	s_add_i32 s79, s13, -6
	s_and_b32 s81, vcc_lo, 0x7e
	s_add_i32 s70, s44, s42
	s_add_i32 s76, s44, s21
	s_add_i32 s19, s44, s10
	s_add_i32 s69, s44, s18
	s_add_i32 s53, s44, s4
	s_add_i32 s94, s44, s91
	s_add_i32 s88, s44, s13
	s_add_i32 s45, s65, vcc_lo
	s_lshl_b32 s0, s20, 2
	s_and_b32 s1, s30, 0x7e
	s_and_b32 s20, s31, 0x7c
	s_and_b32 s30, s97, 0x7e
	s_and_b32 s3, s3, 0x78
	s_and_b32 s31, s63, 0x7e
	s_and_b32 s63, s79, 0x7c
	s_lshl_b32 s79, s81, 2
	s_and_b32 s70, s70, 0x78
	s_and_b32 s76, s76, 0x7f
	s_and_b32 s19, s19, 0x7e
	s_and_b32 s69, s69, 0x7f
	s_and_b32 s53, s53, 0x7c
	s_and_b32 s81, s94, 0x7f
	s_and_b32 s88, s88, 0x7e
	s_and_b32 s45, s45, 0x7f
	s_add_i32 s0, s49, s0
	s_lshl_b32 s1, s1, 2
	s_lshl_b32 s20, s20, 2
	s_lshl_b32 s30, s30, 2
	s_lshl_b32 s3, s3, 2
	s_lshl_b32 s31, s31, 2
	s_lshl_b32 s63, s63, 2
	s_add_i32 s79, s49, s79
	s_lshl_b32 s70, s70, 2
	s_lshl_b32 s76, s76, 2
	s_lshl_b32 s19, s19, 2
	s_lshl_b32 s69, s69, 2
	s_lshl_b32 s53, s53, 2
	s_lshl_b32 s81, s81, 2
	s_lshl_b32 s88, s88, 2
	s_lshl_b32 s45, s45, 2
	v_mov_b32_e32 v13, s0
	s_add_i32 s0, s49, s1
	s_add_i32 s1, s49, s20
	s_add_i32 s20, s49, s30
	s_add_i32 s3, s49, s3
	s_add_i32 s30, s49, s31
	s_add_i32 s31, s49, s63
	v_mov_b32_e32 v15, s79
	s_add_i32 s63, s49, s70
	s_add_i32 s70, s49, s76
	s_add_i32 s19, s49, s19
	s_add_i32 s69, s49, s69
	s_add_i32 s53, s49, s53
	s_add_i32 s76, s49, s81
	s_add_i32 s79, s49, s88
	s_add_i32 s45, s49, s45
	v_mov_b32_e32 v19, s1
	v_mov_b32_e32 v20, s20
	v_mov_b32_e32 v24, s3
	v_mov_b32_e32 v25, s30
	v_mov_b32_e32 v26, s31
	v_mov_b32_e32 v27, s63
	v_mov_b32_e32 v28, s70
	v_mov_b32_e32 v29, s19
	v_mov_b32_e32 v30, s69
	v_mov_b32_e32 v31, s53
	v_mov_b32_e32 v32, s76
	v_mov_b32_e32 v33, s79
	v_mov_b32_e32 v17, s0
	v_mov_b32_e32 v40, s45
	ds_read_b32 v18, v13
	ds_read_b32 v21, v15
	ds_read_b32 v22, v17
	ds_read_b32 v19, v19
	ds_read_b32 v23, v20
	ds_read_b32 v24, v24
	ds_read_b32 v20, v25
	ds_read_b32 v25, v26
	ds_read_b32 v26, v27
	ds_read_b32 v28, v28
	ds_read_b32 v27, v29
	ds_read_b32 v29, v30
	ds_read_b32 v30, v31
	ds_read_b32 v32, v32
	ds_read_b32 v31, v33
	ds_read_b32 v33, v40
	s_add_i32 vcc_hi, vcc_hi, 2
	s_add_i32 s21, s21, s11
	s_add_i32 s10, s10, s12
	s_add_i32 s18, s18, s14
	s_add_i32 s4, s4, s15
	s_add_i32 s91, s91, s16
	s_add_i32 s13, s13, s17
	s_add_i32 vcc_lo, vcc_lo, s90
	s_add_i32 s42, s42, s5
	s_waitcnt vmcnt(16) lgkmcnt(0)
	v_pk_fma_f32 v[8:9], v[212:213], v[18:19], v[8:9] op_sel_hi:[0,1,1]
	v_pk_fma_f32 v[2:3], v[212:213], v[22:23], v[2:3] op_sel_hi:[0,1,1]
	v_pk_fma_f32 v[10:11], v[212:213], v[24:25], v[10:11] op_sel_hi:[0,1,1]
	v_pk_fma_f32 v[6:7], v[212:213], v[20:21], v[6:7] op_sel_hi:[0,1,1]
	v_pk_fma_f32 v[8:9], v[214:215], v[26:27], v[8:9] op_sel_hi:[0,1,1]
	v_pk_fma_f32 v[2:3], v[214:215], v[28:29], v[2:3] op_sel_hi:[0,1,1]
	v_pk_fma_f32 v[10:11], v[214:215], v[30:31], v[10:11] op_sel_hi:[0,1,1]
	v_pk_fma_f32 v[6:7], v[214:215], v[32:33], v[6:7] op_sel_hi:[0,1,1]
	s_and_b32 s20, s42, 0x70
	s_add_i32 s30, s21, -1
	s_add_i32 s31, s10, -2
	s_add_i32 s97, s18, -3
	s_add_i32 s3, s4, -4
	s_add_i32 s63, s91, -5
	s_add_i32 s79, s13, -6
	s_and_b32 s81, vcc_lo, 0x7e
	s_add_i32 s70, s44, s42
	s_add_i32 s76, s44, s21
	s_add_i32 s19, s44, s10
	s_add_i32 s69, s44, s18
	s_add_i32 s53, s44, s4
	s_add_i32 s94, s44, s91
	s_add_i32 s88, s44, s13
	s_add_i32 s45, s65, vcc_lo
	s_lshl_b32 s0, s20, 2
	s_and_b32 s1, s30, 0x7e
	s_and_b32 s20, s31, 0x7c
	s_and_b32 s30, s97, 0x7e
	s_and_b32 s3, s3, 0x78
	s_and_b32 s31, s63, 0x7e
	s_and_b32 s63, s79, 0x7c
	s_lshl_b32 s79, s81, 2
	s_and_b32 s70, s70, 0x78
	s_and_b32 s76, s76, 0x7f
	s_and_b32 s19, s19, 0x7e
	s_and_b32 s69, s69, 0x7f
	s_and_b32 s53, s53, 0x7c
	s_and_b32 s81, s94, 0x7f
	s_and_b32 s88, s88, 0x7e
	s_and_b32 s45, s45, 0x7f
	s_add_i32 s0, s49, s0
	s_lshl_b32 s1, s1, 2
	s_lshl_b32 s20, s20, 2
	s_lshl_b32 s30, s30, 2
	s_lshl_b32 s3, s3, 2
	s_lshl_b32 s31, s31, 2
	s_lshl_b32 s63, s63, 2
	s_add_i32 s79, s49, s79
	s_lshl_b32 s70, s70, 2
	s_lshl_b32 s76, s76, 2
	s_lshl_b32 s19, s19, 2
	s_lshl_b32 s69, s69, 2
	s_lshl_b32 s53, s53, 2
	s_lshl_b32 s81, s81, 2
	s_lshl_b32 s88, s88, 2
	s_lshl_b32 s45, s45, 2
	v_mov_b32_e32 v13, s0
	s_add_i32 s0, s49, s1
	s_add_i32 s1, s49, s20
	s_add_i32 s20, s49, s30
	s_add_i32 s3, s49, s3
	s_add_i32 s30, s49, s31
	s_add_i32 s31, s49, s63
	v_mov_b32_e32 v15, s79
	s_add_i32 s63, s49, s70
	s_add_i32 s70, s49, s76
	s_add_i32 s19, s49, s19
	s_add_i32 s69, s49, s69
	s_add_i32 s53, s49, s53
	s_add_i32 s76, s49, s81
	s_add_i32 s79, s49, s88
	s_add_i32 s45, s49, s45
	v_mov_b32_e32 v19, s1
	v_mov_b32_e32 v20, s20
	v_mov_b32_e32 v24, s3
	v_mov_b32_e32 v25, s30
	v_mov_b32_e32 v26, s31
	v_mov_b32_e32 v27, s63
	v_mov_b32_e32 v28, s70
	v_mov_b32_e32 v29, s19
	v_mov_b32_e32 v30, s69
	v_mov_b32_e32 v31, s53
	v_mov_b32_e32 v32, s76
	v_mov_b32_e32 v33, s79
	v_mov_b32_e32 v17, s0
	v_mov_b32_e32 v40, s45
	ds_read_b32 v18, v13
	ds_read_b32 v21, v15
	ds_read_b32 v22, v17
	ds_read_b32 v19, v19
	ds_read_b32 v23, v20
	ds_read_b32 v24, v24
	ds_read_b32 v20, v25
	ds_read_b32 v25, v26
	ds_read_b32 v26, v27
	ds_read_b32 v28, v28
	ds_read_b32 v27, v29
	ds_read_b32 v29, v30
	ds_read_b32 v30, v31
	ds_read_b32 v32, v32
	ds_read_b32 v31, v33
	ds_read_b32 v33, v40
	s_add_i32 vcc_hi, vcc_hi, 2
	s_add_i32 s21, s21, s11
	s_add_i32 s10, s10, s12
	s_add_i32 s18, s18, s14
	s_add_i32 s4, s4, s15
	s_add_i32 s91, s91, s16
	s_add_i32 s13, s13, s17
	s_add_i32 vcc_lo, vcc_lo, s90
	s_add_i32 s42, s42, s5
	s_waitcnt vmcnt(14) lgkmcnt(0)
; __device__ __forceinline__ void p0_prologue(Frame& F) {
;     ...
; #pragma unroll 2
;             for (int m = 0; m < 128; ++m) { const float wv = wsrc[(size_t)m * 1024];
; #pragma unroll
;                 for (int j = 0; j < 8; ++j) acc8[j] += scr[(m * (c0 + j)) & 127] * wv; }
	v_pk_fma_f32 v[8:9], v[216:217], v[18:19], v[8:9] op_sel_hi:[0,1,1]
	v_pk_fma_f32 v[2:3], v[216:217], v[22:23], v[2:3] op_sel_hi:[0,1,1]
	v_pk_fma_f32 v[10:11], v[216:217], v[24:25], v[10:11] op_sel_hi:[0,1,1]
	v_pk_fma_f32 v[6:7], v[216:217], v[20:21], v[6:7] op_sel_hi:[0,1,1]
	v_pk_fma_f32 v[8:9], v[218:219], v[26:27], v[8:9] op_sel_hi:[0,1,1]
	v_pk_fma_f32 v[2:3], v[218:219], v[28:29], v[2:3] op_sel_hi:[0,1,1]
	v_pk_fma_f32 v[10:11], v[218:219], v[30:31], v[10:11] op_sel_hi:[0,1,1]
	v_pk_fma_f32 v[6:7], v[218:219], v[32:33], v[6:7] op_sel_hi:[0,1,1]
	s_and_b32 s20, s42, 0x70
	s_add_i32 s30, s21, -1
	s_add_i32 s31, s10, -2
	s_add_i32 s97, s18, -3
	s_add_i32 s3, s4, -4
	s_add_i32 s63, s91, -5
	s_add_i32 s79, s13, -6
	s_and_b32 s81, vcc_lo, 0x7e
	s_add_i32 s70, s44, s42
	s_add_i32 s76, s44, s21
	s_add_i32 s19, s44, s10
	s_add_i32 s69, s44, s18
	s_add_i32 s53, s44, s4
	s_add_i32 s94, s44, s91
	s_add_i32 s88, s44, s13
	s_add_i32 s45, s65, vcc_lo
	s_lshl_b32 s0, s20, 2
	s_and_b32 s1, s30, 0x7e
	s_and_b32 s20, s31, 0x7c
	s_and_b32 s30, s97, 0x7e
	s_and_b32 s3, s3, 0x78
	s_and_b32 s31, s63, 0x7e
	s_and_b32 s63, s79, 0x7c
	s_lshl_b32 s79, s81, 2
	s_and_b32 s70, s70, 0x78
	s_and_b32 s76, s76, 0x7f
	s_and_b32 s19, s19, 0x7e
	s_and_b32 s69, s69, 0x7f
	s_and_b32 s53, s53, 0x7c
	s_and_b32 s81, s94, 0x7f
	s_and_b32 s88, s88, 0x7e
	s_and_b32 s45, s45, 0x7f
	s_add_i32 s0, s49, s0
	s_lshl_b32 s1, s1, 2
	s_lshl_b32 s20, s20, 2
	s_lshl_b32 s30, s30, 2
	s_lshl_b32 s3, s3, 2
	s_lshl_b32 s31, s31, 2
	s_lshl_b32 s63, s63, 2
	s_add_i32 s79, s49, s79
	s_lshl_b32 s70, s70, 2
	s_lshl_b32 s76, s76, 2
	s_lshl_b32 s19, s19, 2
	s_lshl_b32 s69, s69, 2
	s_lshl_b32 s53, s53, 2
	s_lshl_b32 s81, s81, 2
	s_lshl_b32 s88, s88, 2
	s_lshl_b32 s45, s45, 2
	v_mov_b32_e32 v13, s0
	s_add_i32 s0, s49, s1
	s_add_i32 s1, s49, s20
	s_add_i32 s20, s49, s30
	s_add_i32 s3, s49, s3
	s_add_i32 s30, s49, s31
	s_add_i32 s31, s49, s63
	v_mov_b32_e32 v15, s79
	s_add_i32 s63, s49, s70
	s_add_i32 s70, s49, s76
	s_add_i32 s19, s49, s19
	s_add_i32 s69, s49, s69
	s_add_i32 s53, s49, s53
	s_add_i32 s76, s49, s81
	s_add_i32 s79, s49, s88
	s_add_i32 s45, s49, s45
	v_mov_b32_e32 v19, s1
	v_mov_b32_e32 v20, s20
	v_mov_b32_e32 v24, s3
	v_mov_b32_e32 v25, s30
	v_mov_b32_e32 v26, s31
	v_mov_b32_e32 v27, s63
	v_mov_b32_e32 v28, s70
	v_mov_b32_e32 v29, s19
	v_mov_b32_e32 v30, s69
	v_mov_b32_e32 v31, s53
	v_mov_b32_e32 v32, s76
	v_mov_b32_e32 v33, s79
	v_mov_b32_e32 v17, s0
	v_mov_b32_e32 v40, s45
	ds_read_b32 v18, v13
	ds_read_b32 v21, v15
	ds_read_b32 v22, v17
	ds_read_b32 v19, v19
	ds_read_b32 v23, v20
	ds_read_b32 v24, v24
	ds_read_b32 v20, v25
	ds_read_b32 v25, v26
	ds_read_b32 v26, v27
	ds_read_b32 v28, v28
	ds_read_b32 v27, v29
	ds_read_b32 v29, v30
	ds_read_b32 v30, v31
	ds_read_b32 v32, v32
	ds_read_b32 v31, v33
	ds_read_b32 v33, v40
	s_add_i32 vcc_hi, vcc_hi, 2
	s_add_i32 s21, s21, s11
	s_add_i32 s10, s10, s12
	s_add_i32 s18, s18, s14
	s_add_i32 s4, s4, s15
	s_add_i32 s91, s91, s16
	s_add_i32 s13, s13, s17
	s_add_i32 vcc_lo, vcc_lo, s90
	s_add_i32 s42, s42, s5
	s_waitcnt vmcnt(12) lgkmcnt(0)
	v_pk_fma_f32 v[8:9], v[220:221], v[18:19], v[8:9] op_sel_hi:[0,1,1]
	v_pk_fma_f32 v[2:3], v[220:221], v[22:23], v[2:3] op_sel_hi:[0,1,1]
	v_pk_fma_f32 v[10:11], v[220:221], v[24:25], v[10:11] op_sel_hi:[0,1,1]
	v_pk_fma_f32 v[6:7], v[220:221], v[20:21], v[6:7] op_sel_hi:[0,1,1]
	v_pk_fma_f32 v[8:9], v[222:223], v[26:27], v[8:9] op_sel_hi:[0,1,1]
	v_pk_fma_f32 v[2:3], v[222:223], v[28:29], v[2:3] op_sel_hi:[0,1,1]
	v_pk_fma_f32 v[10:11], v[222:223], v[30:31], v[10:11] op_sel_hi:[0,1,1]
	v_pk_fma_f32 v[6:7], v[222:223], v[32:33], v[6:7] op_sel_hi:[0,1,1]
	s_and_b32 s20, s42, 0x70
	s_add_i32 s30, s21, -1
	s_add_i32 s31, s10, -2
	s_add_i32 s97, s18, -3
	s_add_i32 s3, s4, -4
	s_add_i32 s63, s91, -5
	s_add_i32 s79, s13, -6
	s_and_b32 s81, vcc_lo, 0x7e
	s_add_i32 s70, s44, s42
	s_add_i32 s76, s44, s21
	s_add_i32 s19, s44, s10
	s_add_i32 s69, s44, s18
	s_add_i32 s53, s44, s4
	s_add_i32 s94, s44, s91
	s_add_i32 s88, s44, s13
	s_add_i32 s45, s65, vcc_lo
	s_lshl_b32 s0, s20, 2
	s_and_b32 s1, s30, 0x7e
	s_and_b32 s20, s31, 0x7c
	s_and_b32 s30, s97, 0x7e
	s_and_b32 s3, s3, 0x78
	s_and_b32 s31, s63, 0x7e
	s_and_b32 s63, s79, 0x7c
	s_lshl_b32 s79, s81, 2
	s_and_b32 s70, s70, 0x78
	s_and_b32 s76, s76, 0x7f
	s_and_b32 s19, s19, 0x7e
	s_and_b32 s69, s69, 0x7f
	s_and_b32 s53, s53, 0x7c
	s_and_b32 s81, s94, 0x7f
	s_and_b32 s88, s88, 0x7e
	s_and_b32 s45, s45, 0x7f
	s_add_i32 s0, s49, s0
	s_lshl_b32 s1, s1, 2
	s_lshl_b32 s20, s20, 2
	s_lshl_b32 s30, s30, 2
	s_lshl_b32 s3, s3, 2
	s_lshl_b32 s31, s31, 2
	s_lshl_b32 s63, s63, 2
	s_add_i32 s79, s49, s79
	s_lshl_b32 s70, s70, 2
	s_lshl_b32 s76, s76, 2
	s_lshl_b32 s19, s19, 2
	s_lshl_b32 s69, s69, 2
	s_lshl_b32 s53, s53, 2
	s_lshl_b32 s81, s81, 2
	s_lshl_b32 s88, s88, 2
	s_lshl_b32 s45, s45, 2
	v_mov_b32_e32 v13, s0
	s_add_i32 s0, s49, s1
	s_add_i32 s1, s49, s20
	s_add_i32 s20, s49, s30
	s_add_i32 s3, s49, s3
	s_add_i32 s30, s49, s31
	s_add_i32 s31, s49, s63
	v_mov_b32_e32 v15, s79
	s_add_i32 s63, s49, s70
	s_add_i32 s70, s49, s76
	s_add_i32 s19, s49, s19
	s_add_i32 s69, s49, s69
	s_add_i32 s53, s49, s53
	s_add_i32 s76, s49, s81
	s_add_i32 s79, s49, s88
	s_add_i32 s45, s49, s45
	v_mov_b32_e32 v19, s1
	v_mov_b32_e32 v20, s20
	v_mov_b32_e32 v24, s3
	v_mov_b32_e32 v25, s30
	v_mov_b32_e32 v26, s31
	v_mov_b32_e32 v27, s63
	v_mov_b32_e32 v28, s70
	v_mov_b32_e32 v29, s19
	v_mov_b32_e32 v30, s69
	v_mov_b32_e32 v31, s53
	v_mov_b32_e32 v32, s76
	v_mov_b32_e32 v33, s79
	v_mov_b32_e32 v17, s0
	v_mov_b32_e32 v40, s45
	ds_read_b32 v18, v13
	ds_read_b32 v21, v15
	ds_read_b32 v22, v17
	ds_read_b32 v19, v19
	ds_read_b32 v23, v20
	ds_read_b32 v24, v24
	ds_read_b32 v20, v25
	ds_read_b32 v25, v26
	ds_read_b32 v26, v27
	ds_read_b32 v28, v28
	ds_read_b32 v27, v29
	ds_read_b32 v29, v30
	ds_read_b32 v30, v31
	ds_read_b32 v32, v32
	ds_read_b32 v31, v33
	ds_read_b32 v33, v40
	s_add_i32 vcc_hi, vcc_hi, 2
	s_add_i32 s21, s21, s11
	s_add_i32 s10, s10, s12
	s_add_i32 s18, s18, s14
	s_add_i32 s4, s4, s15
	s_add_i32 s91, s91, s16
	s_add_i32 s13, s13, s17
	s_add_i32 vcc_lo, vcc_lo, s90
	s_add_i32 s42, s42, s5
	s_waitcnt vmcnt(10) lgkmcnt(0)
; __device__ __forceinline__ void p0_prologue(Frame& F) {
;     ...
; #pragma unroll 2
;             for (int m = 0; m < 128; ++m) { const float wv = wsrc[(size_t)m * 1024];
; #pragma unroll
;                 for (int j = 0; j < 8; ++j) acc8[j] += scr[(m * (c0 + j)) & 127] * wv; }
	v_pk_fma_f32 v[8:9], v[224:225], v[18:19], v[8:9] op_sel_hi:[0,1,1]
	v_pk_fma_f32 v[2:3], v[224:225], v[22:23], v[2:3] op_sel_hi:[0,1,1]
	v_pk_fma_f32 v[10:11], v[224:225], v[24:25], v[10:11] op_sel_hi:[0,1,1]
	v_pk_fma_f32 v[6:7], v[224:225], v[20:21], v[6:7] op_sel_hi:[0,1,1]
	v_pk_fma_f32 v[8:9], v[226:227], v[26:27], v[8:9] op_sel_hi:[0,1,1]
	v_pk_fma_f32 v[2:3], v[226:227], v[28:29], v[2:3] op_sel_hi:[0,1,1]
	v_pk_fma_f32 v[10:11], v[226:227], v[30:31], v[10:11] op_sel_hi:[0,1,1]
	v_pk_fma_f32 v[6:7], v[226:227], v[32:33], v[6:7] op_sel_hi:[0,1,1]
	s_and_b32 s20, s42, 0x70
	s_add_i32 s30, s21, -1
	s_add_i32 s31, s10, -2
	s_add_i32 s97, s18, -3
	s_add_i32 s3, s4, -4
	s_add_i32 s63, s91, -5
	s_add_i32 s79, s13, -6
	s_and_b32 s81, vcc_lo, 0x7e
	s_add_i32 s70, s44, s42
	s_add_i32 s76, s44, s21
	s_add_i32 s19, s44, s10
	s_add_i32 s69, s44, s18
	s_add_i32 s53, s44, s4
	s_add_i32 s94, s44, s91
	s_add_i32 s88, s44, s13
	s_add_i32 s45, s65, vcc_lo
	s_lshl_b32 s0, s20, 2
	s_and_b32 s1, s30, 0x7e
	s_and_b32 s20, s31, 0x7c
	s_and_b32 s30, s97, 0x7e
	s_and_b32 s3, s3, 0x78
	s_and_b32 s31, s63, 0x7e
	s_and_b32 s63, s79, 0x7c
	s_lshl_b32 s79, s81, 2
	s_and_b32 s70, s70, 0x78
	s_and_b32 s76, s76, 0x7f
	s_and_b32 s19, s19, 0x7e
	s_and_b32 s69, s69, 0x7f
	s_and_b32 s53, s53, 0x7c
	s_and_b32 s81, s94, 0x7f
	s_and_b32 s88, s88, 0x7e
	s_and_b32 s45, s45, 0x7f
	s_add_i32 s0, s49, s0
	s_lshl_b32 s1, s1, 2
	s_lshl_b32 s20, s20, 2
	s_lshl_b32 s30, s30, 2
	s_lshl_b32 s3, s3, 2
	s_lshl_b32 s31, s31, 2
	s_lshl_b32 s63, s63, 2
	s_add_i32 s79, s49, s79
	s_lshl_b32 s70, s70, 2
	s_lshl_b32 s76, s76, 2
	s_lshl_b32 s19, s19, 2
	s_lshl_b32 s69, s69, 2
	s_lshl_b32 s53, s53, 2
	s_lshl_b32 s81, s81, 2
	s_lshl_b32 s88, s88, 2
	s_lshl_b32 s45, s45, 2
	v_mov_b32_e32 v13, s0
	s_add_i32 s0, s49, s1
	s_add_i32 s1, s49, s20
	s_add_i32 s20, s49, s30
	s_add_i32 s3, s49, s3
	s_add_i32 s30, s49, s31
	s_add_i32 s31, s49, s63
	v_mov_b32_e32 v15, s79
	s_add_i32 s63, s49, s70
	s_add_i32 s70, s49, s76
	s_add_i32 s19, s49, s19
	s_add_i32 s69, s49, s69
	s_add_i32 s53, s49, s53
	s_add_i32 s76, s49, s81
	s_add_i32 s79, s49, s88
	s_add_i32 s45, s49, s45
	v_mov_b32_e32 v19, s1
	v_mov_b32_e32 v20, s20
	v_mov_b32_e32 v24, s3
	v_mov_b32_e32 v25, s30
	v_mov_b32_e32 v26, s31
	v_mov_b32_e32 v27, s63
	v_mov_b32_e32 v28, s70
	v_mov_b32_e32 v29, s19
	v_mov_b32_e32 v30, s69
	v_mov_b32_e32 v31, s53
	v_mov_b32_e32 v32, s76
	v_mov_b32_e32 v33, s79
	v_mov_b32_e32 v17, s0
	v_mov_b32_e32 v40, s45
	ds_read_b32 v18, v13
	ds_read_b32 v21, v15
	ds_read_b32 v22, v17
	ds_read_b32 v19, v19
	ds_read_b32 v23, v20
	ds_read_b32 v24, v24
	ds_read_b32 v20, v25
	ds_read_b32 v25, v26
	ds_read_b32 v26, v27
	ds_read_b32 v28, v28
	ds_read_b32 v27, v29
	ds_read_b32 v29, v30
	ds_read_b32 v30, v31
	ds_read_b32 v32, v32
	ds_read_b32 v31, v33
	ds_read_b32 v33, v40
	s_add_i32 vcc_hi, vcc_hi, 2
	s_add_i32 s21, s21, s11
	s_add_i32 s10, s10, s12
	s_add_i32 s18, s18, s14
	s_add_i32 s4, s4, s15
	s_add_i32 s91, s91, s16
	s_add_i32 s13, s13, s17
	s_add_i32 vcc_lo, vcc_lo, s90
	s_add_i32 s42, s42, s5
	s_waitcnt vmcnt(8) lgkmcnt(0)
	v_pk_fma_f32 v[8:9], v[228:229], v[18:19], v[8:9] op_sel_hi:[0,1,1]
	v_pk_fma_f32 v[2:3], v[228:229], v[22:23], v[2:3] op_sel_hi:[0,1,1]
	v_pk_fma_f32 v[10:11], v[228:229], v[24:25], v[10:11] op_sel_hi:[0,1,1]
	v_pk_fma_f32 v[6:7], v[228:229], v[20:21], v[6:7] op_sel_hi:[0,1,1]
	v_pk_fma_f32 v[8:9], v[230:231], v[26:27], v[8:9] op_sel_hi:[0,1,1]
	v_pk_fma_f32 v[2:3], v[230:231], v[28:29], v[2:3] op_sel_hi:[0,1,1]
	v_pk_fma_f32 v[10:11], v[230:231], v[30:31], v[10:11] op_sel_hi:[0,1,1]
	v_pk_fma_f32 v[6:7], v[230:231], v[32:33], v[6:7] op_sel_hi:[0,1,1]
	s_and_b32 s20, s42, 0x70
	s_add_i32 s30, s21, -1
	s_add_i32 s31, s10, -2
	s_add_i32 s97, s18, -3
	s_add_i32 s3, s4, -4
	s_add_i32 s63, s91, -5
	s_add_i32 s79, s13, -6
	s_and_b32 s81, vcc_lo, 0x7e
	s_add_i32 s70, s44, s42
	s_add_i32 s76, s44, s21
	s_add_i32 s19, s44, s10
	s_add_i32 s69, s44, s18
	s_add_i32 s53, s44, s4
	s_add_i32 s94, s44, s91
	s_add_i32 s88, s44, s13
	s_add_i32 s45, s65, vcc_lo
	s_lshl_b32 s0, s20, 2
	s_and_b32 s1, s30, 0x7e
	s_and_b32 s20, s31, 0x7c
	s_and_b32 s30, s97, 0x7e
	s_and_b32 s3, s3, 0x78
	s_and_b32 s31, s63, 0x7e
	s_and_b32 s63, s79, 0x7c
	s_lshl_b32 s79, s81, 2
	s_and_b32 s70, s70, 0x78
	s_and_b32 s76, s76, 0x7f
	s_and_b32 s19, s19, 0x7e
	s_and_b32 s69, s69, 0x7f
	s_and_b32 s53, s53, 0x7c
	s_and_b32 s81, s94, 0x7f
	s_and_b32 s88, s88, 0x7e
	s_and_b32 s45, s45, 0x7f
	s_add_i32 s0, s49, s0
	s_lshl_b32 s1, s1, 2
	s_lshl_b32 s20, s20, 2
	s_lshl_b32 s30, s30, 2
	s_lshl_b32 s3, s3, 2
	s_lshl_b32 s31, s31, 2
	s_lshl_b32 s63, s63, 2
	s_add_i32 s79, s49, s79
	s_lshl_b32 s70, s70, 2
	s_lshl_b32 s76, s76, 2
	s_lshl_b32 s19, s19, 2
	s_lshl_b32 s69, s69, 2
	s_lshl_b32 s53, s53, 2
	s_lshl_b32 s81, s81, 2
	s_lshl_b32 s88, s88, 2
	s_lshl_b32 s45, s45, 2
	v_mov_b32_e32 v13, s0
	s_add_i32 s0, s49, s1
	s_add_i32 s1, s49, s20
	s_add_i32 s20, s49, s30
	s_add_i32 s3, s49, s3
	s_add_i32 s30, s49, s31
	s_add_i32 s31, s49, s63
	v_mov_b32_e32 v15, s79
	s_add_i32 s63, s49, s70
	s_add_i32 s70, s49, s76
	s_add_i32 s19, s49, s19
	s_add_i32 s69, s49, s69
	s_add_i32 s53, s49, s53
	s_add_i32 s76, s49, s81
	s_add_i32 s79, s49, s88
	s_add_i32 s45, s49, s45
	v_mov_b32_e32 v19, s1
	v_mov_b32_e32 v20, s20
	v_mov_b32_e32 v24, s3
	v_mov_b32_e32 v25, s30
	v_mov_b32_e32 v26, s31
	v_mov_b32_e32 v27, s63
	v_mov_b32_e32 v28, s70
	v_mov_b32_e32 v29, s19
	v_mov_b32_e32 v30, s69
	v_mov_b32_e32 v31, s53
	v_mov_b32_e32 v32, s76
	v_mov_b32_e32 v33, s79
	v_mov_b32_e32 v17, s0
	v_mov_b32_e32 v40, s45
	ds_read_b32 v18, v13
	ds_read_b32 v21, v15
	ds_read_b32 v22, v17
	ds_read_b32 v19, v19
	ds_read_b32 v23, v20
	ds_read_b32 v24, v24
	ds_read_b32 v20, v25
	ds_read_b32 v25, v26
	ds_read_b32 v26, v27
	ds_read_b32 v28, v28
	ds_read_b32 v27, v29
	ds_read_b32 v29, v30
	ds_read_b32 v30, v31
	ds_read_b32 v32, v32
	ds_read_b32 v31, v33
	ds_read_b32 v33, v40
	s_add_i32 vcc_hi, vcc_hi, 2
	s_add_i32 s21, s21, s11
	s_add_i32 s10, s10, s12
	s_add_i32 s18, s18, s14
	s_add_i32 s4, s4, s15
	s_add_i32 s91, s91, s16
	s_add_i32 s13, s13, s17
	s_add_i32 vcc_lo, vcc_lo, s90
	s_add_i32 s42, s42, s5
	s_waitcnt vmcnt(6) lgkmcnt(0)
; __device__ __forceinline__ void p0_prologue(Frame& F) {
;     ...
; #pragma unroll 2
;             for (int m = 0; m < 128; ++m) { const float wv = wsrc[(size_t)m * 1024];
; #pragma unroll
;                 for (int j = 0; j < 8; ++j) acc8[j] += scr[(m * (c0 + j)) & 127] * wv; }
	v_pk_fma_f32 v[8:9], v[232:233], v[18:19], v[8:9] op_sel_hi:[0,1,1]
	v_pk_fma_f32 v[2:3], v[232:233], v[22:23], v[2:3] op_sel_hi:[0,1,1]
	v_pk_fma_f32 v[10:11], v[232:233], v[24:25], v[10:11] op_sel_hi:[0,1,1]
	v_pk_fma_f32 v[6:7], v[232:233], v[20:21], v[6:7] op_sel_hi:[0,1,1]
	v_pk_fma_f32 v[8:9], v[234:235], v[26:27], v[8:9] op_sel_hi:[0,1,1]
	v_pk_fma_f32 v[2:3], v[234:235], v[28:29], v[2:3] op_sel_hi:[0,1,1]
	v_pk_fma_f32 v[10:11], v[234:235], v[30:31], v[10:11] op_sel_hi:[0,1,1]
	v_pk_fma_f32 v[6:7], v[234:235], v[32:33], v[6:7] op_sel_hi:[0,1,1]
	s_and_b32 s20, s42, 0x70
	s_add_i32 s30, s21, -1
	s_add_i32 s31, s10, -2
	s_add_i32 s97, s18, -3
	s_add_i32 s3, s4, -4
	s_add_i32 s63, s91, -5
	s_add_i32 s79, s13, -6
	s_and_b32 s81, vcc_lo, 0x7e
	s_add_i32 s70, s44, s42
	s_add_i32 s76, s44, s21
	s_add_i32 s19, s44, s10
	s_add_i32 s69, s44, s18
	s_add_i32 s53, s44, s4
	s_add_i32 s94, s44, s91
	s_add_i32 s88, s44, s13
	s_add_i32 s45, s65, vcc_lo
	s_lshl_b32 s0, s20, 2
	s_and_b32 s1, s30, 0x7e
	s_and_b32 s20, s31, 0x7c
	s_and_b32 s30, s97, 0x7e
	s_and_b32 s3, s3, 0x78
	s_and_b32 s31, s63, 0x7e
	s_and_b32 s63, s79, 0x7c
	s_lshl_b32 s79, s81, 2
	s_and_b32 s70, s70, 0x78
	s_and_b32 s76, s76, 0x7f
	s_and_b32 s19, s19, 0x7e
	s_and_b32 s69, s69, 0x7f
	s_and_b32 s53, s53, 0x7c
	s_and_b32 s81, s94, 0x7f
	s_and_b32 s88, s88, 0x7e
	s_and_b32 s45, s45, 0x7f
	s_add_i32 s0, s49, s0
	s_lshl_b32 s1, s1, 2
	s_lshl_b32 s20, s20, 2
	s_lshl_b32 s30, s30, 2
	s_lshl_b32 s3, s3, 2
	s_lshl_b32 s31, s31, 2
	s_lshl_b32 s63, s63, 2
	s_add_i32 s79, s49, s79
	s_lshl_b32 s70, s70, 2
	s_lshl_b32 s76, s76, 2
	s_lshl_b32 s19, s19, 2
	s_lshl_b32 s69, s69, 2
	s_lshl_b32 s53, s53, 2
	s_lshl_b32 s81, s81, 2
	s_lshl_b32 s88, s88, 2
	s_lshl_b32 s45, s45, 2
	v_mov_b32_e32 v13, s0
	s_add_i32 s0, s49, s1
	s_add_i32 s1, s49, s20
	s_add_i32 s20, s49, s30
	s_add_i32 s3, s49, s3
	s_add_i32 s30, s49, s31
	s_add_i32 s31, s49, s63
	v_mov_b32_e32 v15, s79
	s_add_i32 s63, s49, s70
	s_add_i32 s70, s49, s76
	s_add_i32 s19, s49, s19
	s_add_i32 s69, s49, s69
	s_add_i32 s53, s49, s53
	s_add_i32 s76, s49, s81
	s_add_i32 s79, s49, s88
	s_add_i32 s45, s49, s45
	v_mov_b32_e32 v19, s1
	v_mov_b32_e32 v20, s20
	v_mov_b32_e32 v24, s3
	v_mov_b32_e32 v25, s30
	v_mov_b32_e32 v26, s31
	v_mov_b32_e32 v27, s63
	v_mov_b32_e32 v28, s70
	v_mov_b32_e32 v29, s19
	v_mov_b32_e32 v30, s69
	v_mov_b32_e32 v31, s53
	v_mov_b32_e32 v32, s76
	v_mov_b32_e32 v33, s79
	v_mov_b32_e32 v17, s0
	v_mov_b32_e32 v40, s45
	ds_read_b32 v18, v13
	ds_read_b32 v21, v15
	ds_read_b32 v22, v17
	ds_read_b32 v19, v19
	ds_read_b32 v23, v20
	ds_read_b32 v24, v24
	ds_read_b32 v20, v25
	ds_read_b32 v25, v26
	ds_read_b32 v26, v27
	ds_read_b32 v28, v28
	ds_read_b32 v27, v29
	ds_read_b32 v29, v30
	ds_read_b32 v30, v31
	ds_read_b32 v32, v32
	ds_read_b32 v31, v33
	ds_read_b32 v33, v40
	s_add_i32 vcc_hi, vcc_hi, 2
	s_add_i32 s21, s21, s11
	s_add_i32 s10, s10, s12
	s_add_i32 s18, s18, s14
	s_add_i32 s4, s4, s15
	s_add_i32 s91, s91, s16
	s_add_i32 s13, s13, s17
	s_add_i32 vcc_lo, vcc_lo, s90
	s_add_i32 s42, s42, s5
	s_waitcnt vmcnt(4) lgkmcnt(0)
	v_pk_fma_f32 v[8:9], v[236:237], v[18:19], v[8:9] op_sel_hi:[0,1,1]
	v_pk_fma_f32 v[2:3], v[236:237], v[22:23], v[2:3] op_sel_hi:[0,1,1]
	v_pk_fma_f32 v[10:11], v[236:237], v[24:25], v[10:11] op_sel_hi:[0,1,1]
	v_pk_fma_f32 v[6:7], v[236:237], v[20:21], v[6:7] op_sel_hi:[0,1,1]
	v_pk_fma_f32 v[8:9], v[238:239], v[26:27], v[8:9] op_sel_hi:[0,1,1]
	v_pk_fma_f32 v[2:3], v[238:239], v[28:29], v[2:3] op_sel_hi:[0,1,1]
	v_pk_fma_f32 v[10:11], v[238:239], v[30:31], v[10:11] op_sel_hi:[0,1,1]
	v_pk_fma_f32 v[6:7], v[238:239], v[32:33], v[6:7] op_sel_hi:[0,1,1]
	s_and_b32 s20, s42, 0x70
	s_add_i32 s30, s21, -1
	s_add_i32 s31, s10, -2
	s_add_i32 s97, s18, -3
	s_add_i32 s3, s4, -4
	s_add_i32 s63, s91, -5
	s_add_i32 s79, s13, -6
	s_and_b32 s81, vcc_lo, 0x7e
	s_add_i32 s70, s44, s42
	s_add_i32 s76, s44, s21
	s_add_i32 s19, s44, s10
	s_add_i32 s69, s44, s18
	s_add_i32 s53, s44, s4
	s_add_i32 s94, s44, s91
	s_add_i32 s88, s44, s13
	s_add_i32 s45, s65, vcc_lo
	s_lshl_b32 s0, s20, 2
	s_and_b32 s1, s30, 0x7e
	s_and_b32 s20, s31, 0x7c
	s_and_b32 s30, s97, 0x7e
	s_and_b32 s3, s3, 0x78
	s_and_b32 s31, s63, 0x7e
	s_and_b32 s63, s79, 0x7c
	s_lshl_b32 s79, s81, 2
	s_and_b32 s70, s70, 0x78
	s_and_b32 s76, s76, 0x7f
	s_and_b32 s19, s19, 0x7e
	s_and_b32 s69, s69, 0x7f
	s_and_b32 s53, s53, 0x7c
	s_and_b32 s81, s94, 0x7f
	s_and_b32 s88, s88, 0x7e
	s_and_b32 s45, s45, 0x7f
	s_add_i32 s0, s49, s0
	s_lshl_b32 s1, s1, 2
	s_lshl_b32 s20, s20, 2
	s_lshl_b32 s30, s30, 2
	s_lshl_b32 s3, s3, 2
	s_lshl_b32 s31, s31, 2
	s_lshl_b32 s63, s63, 2
	s_add_i32 s79, s49, s79
	s_lshl_b32 s70, s70, 2
	s_lshl_b32 s76, s76, 2
	s_lshl_b32 s19, s19, 2
	s_lshl_b32 s69, s69, 2
	s_lshl_b32 s53, s53, 2
	s_lshl_b32 s81, s81, 2
	s_lshl_b32 s88, s88, 2
	s_lshl_b32 s45, s45, 2
	v_mov_b32_e32 v13, s0
	s_add_i32 s0, s49, s1
	s_add_i32 s1, s49, s20
	s_add_i32 s20, s49, s30
	s_add_i32 s3, s49, s3
	s_add_i32 s30, s49, s31
	s_add_i32 s31, s49, s63
	v_mov_b32_e32 v15, s79
	s_add_i32 s63, s49, s70
	s_add_i32 s70, s49, s76
	s_add_i32 s19, s49, s19
	s_add_i32 s69, s49, s69
	s_add_i32 s53, s49, s53
	s_add_i32 s76, s49, s81
	s_add_i32 s79, s49, s88
	s_add_i32 s45, s49, s45
	v_mov_b32_e32 v19, s1
	v_mov_b32_e32 v20, s20
	v_mov_b32_e32 v24, s3
	v_mov_b32_e32 v25, s30
	v_mov_b32_e32 v26, s31
	v_mov_b32_e32 v27, s63
	v_mov_b32_e32 v28, s70
	v_mov_b32_e32 v29, s19
	v_mov_b32_e32 v30, s69
	v_mov_b32_e32 v31, s53
	v_mov_b32_e32 v32, s76
	v_mov_b32_e32 v33, s79
	v_mov_b32_e32 v17, s0
	v_mov_b32_e32 v40, s45
	ds_read_b32 v18, v13
	ds_read_b32 v21, v15
	ds_read_b32 v22, v17
	ds_read_b32 v19, v19
	ds_read_b32 v23, v20
	ds_read_b32 v24, v24
	ds_read_b32 v20, v25
	ds_read_b32 v25, v26
	ds_read_b32 v26, v27
	ds_read_b32 v28, v28
	ds_read_b32 v27, v29
	ds_read_b32 v29, v30
	ds_read_b32 v30, v31
	ds_read_b32 v32, v32
	ds_read_b32 v31, v33
	ds_read_b32 v33, v40
	s_add_i32 vcc_hi, vcc_hi, 2
	s_add_i32 s21, s21, s11
	s_add_i32 s10, s10, s12
	s_add_i32 s18, s18, s14
	s_add_i32 s4, s4, s15
	s_add_i32 s91, s91, s16
	s_add_i32 s13, s13, s17
	s_add_i32 vcc_lo, vcc_lo, s90
	s_add_i32 s42, s42, s5
	s_waitcnt vmcnt(2) lgkmcnt(0)
; __device__ __forceinline__ void p0_prologue(Frame& F) {
;     ...
; #pragma unroll 2
;             for (int m = 0; m < 128; ++m) { const float wv = wsrc[(size_t)m * 1024];
; #pragma unroll
;                 for (int j = 0; j < 8; ++j) acc8[j] += scr[(m * (c0 + j)) & 127] * wv; }
	v_pk_fma_f32 v[8:9], v[240:241], v[18:19], v[8:9] op_sel_hi:[0,1,1]
	v_pk_fma_f32 v[2:3], v[240:241], v[22:23], v[2:3] op_sel_hi:[0,1,1]
	v_pk_fma_f32 v[10:11], v[240:241], v[24:25], v[10:11] op_sel_hi:[0,1,1]
	v_pk_fma_f32 v[6:7], v[240:241], v[20:21], v[6:7] op_sel_hi:[0,1,1]
	v_pk_fma_f32 v[8:9], v[242:243], v[26:27], v[8:9] op_sel_hi:[0,1,1]
	v_pk_fma_f32 v[2:3], v[242:243], v[28:29], v[2:3] op_sel_hi:[0,1,1]
	v_pk_fma_f32 v[10:11], v[242:243], v[30:31], v[10:11] op_sel_hi:[0,1,1]
	v_pk_fma_f32 v[6:7], v[242:243], v[32:33], v[6:7] op_sel_hi:[0,1,1]
	s_and_b32 s20, s42, 0x70
	s_add_i32 s30, s21, -1
	s_add_i32 s31, s10, -2
	s_add_i32 s97, s18, -3
	s_add_i32 s3, s4, -4
	s_add_i32 s63, s91, -5
	s_add_i32 s79, s13, -6
	s_and_b32 s81, vcc_lo, 0x7e
	s_add_i32 s70, s44, s42
	s_add_i32 s76, s44, s21
	s_add_i32 s19, s44, s10
	s_add_i32 s69, s44, s18
	s_add_i32 s53, s44, s4
	s_add_i32 s94, s44, s91
	s_add_i32 s88, s44, s13
	s_add_i32 s45, s65, vcc_lo
	s_lshl_b32 s0, s20, 2
	s_and_b32 s1, s30, 0x7e
	s_and_b32 s20, s31, 0x7c
	s_and_b32 s30, s97, 0x7e
	s_and_b32 s3, s3, 0x78
	s_and_b32 s31, s63, 0x7e
	s_and_b32 s63, s79, 0x7c
	s_lshl_b32 s79, s81, 2
	s_and_b32 s70, s70, 0x78
	s_and_b32 s76, s76, 0x7f
	s_and_b32 s19, s19, 0x7e
	s_and_b32 s69, s69, 0x7f
	s_and_b32 s53, s53, 0x7c
	s_and_b32 s81, s94, 0x7f
	s_and_b32 s88, s88, 0x7e
	s_and_b32 s45, s45, 0x7f
	s_add_i32 s0, s49, s0
	s_lshl_b32 s1, s1, 2
	s_lshl_b32 s20, s20, 2
	s_lshl_b32 s30, s30, 2
	s_lshl_b32 s3, s3, 2
	s_lshl_b32 s31, s31, 2
	s_lshl_b32 s63, s63, 2
	s_add_i32 s79, s49, s79
	s_lshl_b32 s70, s70, 2
	s_lshl_b32 s76, s76, 2
	s_lshl_b32 s19, s19, 2
	s_lshl_b32 s69, s69, 2
	s_lshl_b32 s53, s53, 2
	s_lshl_b32 s81, s81, 2
	s_lshl_b32 s88, s88, 2
	s_lshl_b32 s45, s45, 2
	v_mov_b32_e32 v13, s0
	s_add_i32 s0, s49, s1
	s_add_i32 s1, s49, s20
	s_add_i32 s20, s49, s30
	s_add_i32 s3, s49, s3
	s_add_i32 s30, s49, s31
	s_add_i32 s31, s49, s63
	v_mov_b32_e32 v15, s79
	s_add_i32 s63, s49, s70
	s_add_i32 s70, s49, s76
	s_add_i32 s19, s49, s19
	s_add_i32 s69, s49, s69
	s_add_i32 s53, s49, s53
	s_add_i32 s76, s49, s81
	s_add_i32 s79, s49, s88
	s_add_i32 s45, s49, s45
	v_mov_b32_e32 v19, s1
	v_mov_b32_e32 v20, s20
	v_mov_b32_e32 v24, s3
	v_mov_b32_e32 v25, s30
	v_mov_b32_e32 v26, s31
	v_mov_b32_e32 v27, s63
	v_mov_b32_e32 v28, s70
	v_mov_b32_e32 v29, s19
	v_mov_b32_e32 v30, s69
	v_mov_b32_e32 v31, s53
	v_mov_b32_e32 v32, s76
	v_mov_b32_e32 v33, s79
	v_mov_b32_e32 v17, s0
	v_mov_b32_e32 v40, s45
	ds_read_b32 v18, v13
	ds_read_b32 v21, v15
	ds_read_b32 v22, v17
	ds_read_b32 v19, v19
	ds_read_b32 v23, v20
	ds_read_b32 v24, v24
	ds_read_b32 v20, v25
	ds_read_b32 v25, v26
	ds_read_b32 v26, v27
	ds_read_b32 v28, v28
	ds_read_b32 v27, v29
	ds_read_b32 v29, v30
	ds_read_b32 v30, v31
	ds_read_b32 v32, v32
	ds_read_b32 v31, v33
	ds_read_b32 v33, v40
	s_add_i32 vcc_hi, vcc_hi, 2
	s_add_i32 s21, s21, s11
	s_add_i32 s10, s10, s12
	s_add_i32 s18, s18, s14
	s_add_i32 s4, s4, s15
	s_add_i32 s91, s91, s16
	s_add_i32 s13, s13, s17
	s_add_i32 vcc_lo, vcc_lo, s90
	s_add_i32 s42, s42, s5
	s_waitcnt vmcnt(0) lgkmcnt(0)
	v_pk_fma_f32 v[8:9], v[244:245], v[18:19], v[8:9] op_sel_hi:[0,1,1]
	v_pk_fma_f32 v[2:3], v[244:245], v[22:23], v[2:3] op_sel_hi:[0,1,1]
	v_pk_fma_f32 v[10:11], v[244:245], v[24:25], v[10:11] op_sel_hi:[0,1,1]
	v_pk_fma_f32 v[6:7], v[244:245], v[20:21], v[6:7] op_sel_hi:[0,1,1]
	v_pk_fma_f32 v[8:9], v[246:247], v[26:27], v[8:9] op_sel_hi:[0,1,1]
	v_pk_fma_f32 v[2:3], v[246:247], v[28:29], v[2:3] op_sel_hi:[0,1,1]
	v_pk_fma_f32 v[10:11], v[246:247], v[30:31], v[10:11] op_sel_hi:[0,1,1]
	v_pk_fma_f32 v[6:7], v[246:247], v[32:33], v[6:7] op_sel_hi:[0,1,1]
	s_mov_b64 s[0:1], 0x2000
	global_load_dword v120, v[4:5], off offset:-4096
	global_load_dword v122, v[4:5], off
	v_lshl_add_u64 v[4:5], v[4:5], 0, s[0:1]
	global_load_dword v124, v[4:5], off offset:-4096
	global_load_dword v126, v[4:5], off
	v_lshl_add_u64 v[4:5], v[4:5], 0, s[0:1]
	global_load_dword v128, v[4:5], off offset:-4096
	global_load_dword v130, v[4:5], off
	v_lshl_add_u64 v[4:5], v[4:5], 0, s[0:1]
	global_load_dword v132, v[4:5], off offset:-4096
	global_load_dword v134, v[4:5], off
	v_lshl_add_u64 v[4:5], v[4:5], 0, s[0:1]
	global_load_dword v136, v[4:5], off offset:-4096
	global_load_dword v138, v[4:5], off
	v_lshl_add_u64 v[4:5], v[4:5], 0, s[0:1]
	global_load_dword v140, v[4:5], off offset:-4096
	global_load_dword v142, v[4:5], off
	v_lshl_add_u64 v[4:5], v[4:5], 0, s[0:1]
	global_load_dword v144, v[4:5], off offset:-4096
	global_load_dword v146, v[4:5], off
	v_lshl_add_u64 v[4:5], v[4:5], 0, s[0:1]
	global_load_dword v148, v[4:5], off offset:-4096
	global_load_dword v150, v[4:5], off
	v_lshl_add_u64 v[4:5], v[4:5], 0, s[0:1]
	global_load_dword v152, v[4:5], off offset:-4096
	global_load_dword v154, v[4:5], off
	v_lshl_add_u64 v[4:5], v[4:5], 0, s[0:1]
	global_load_dword v156, v[4:5], off offset:-4096
	global_load_dword v158, v[4:5], off
	v_lshl_add_u64 v[4:5], v[4:5], 0, s[0:1]
	global_load_dword v160, v[4:5], off offset:-4096
	global_load_dword v162, v[4:5], off
	v_lshl_add_u64 v[4:5], v[4:5], 0, s[0:1]
	global_load_dword v164, v[4:5], off offset:-4096
	global_load_dword v166, v[4:5], off
	v_lshl_add_u64 v[4:5], v[4:5], 0, s[0:1]
	global_load_dword v168, v[4:5], off offset:-4096
	global_load_dword v170, v[4:5], off
	v_lshl_add_u64 v[4:5], v[4:5], 0, s[0:1]
	global_load_dword v172, v[4:5], off offset:-4096
	global_load_dword v174, v[4:5], off
	v_lshl_add_u64 v[4:5], v[4:5], 0, s[0:1]
	global_load_dword v176, v[4:5], off offset:-4096
	global_load_dword v178, v[4:5], off
	v_lshl_add_u64 v[4:5], v[4:5], 0, s[0:1]
	global_load_dword v180, v[4:5], off offset:-4096
; __device__ __forceinline__ void p0_prologue(Frame& F) {
;     ...
; #pragma unroll 2
;             for (int m = 0; m < 128; ++m) { const float wv = wsrc[(size_t)m * 1024];
; #pragma unroll
;                 for (int j = 0; j < 8; ++j) acc8[j] += scr[(m * (c0 + j)) & 127] * wv; }
	global_load_dword v182, v[4:5], off
	v_lshl_add_u64 v[4:5], v[4:5], 0, s[0:1]
	global_load_dword v184, v[4:5], off offset:-4096
	global_load_dword v186, v[4:5], off
	v_lshl_add_u64 v[4:5], v[4:5], 0, s[0:1]
	global_load_dword v188, v[4:5], off offset:-4096
	global_load_dword v190, v[4:5], off
	v_lshl_add_u64 v[4:5], v[4:5], 0, s[0:1]
	global_load_dword v192, v[4:5], off offset:-4096
	global_load_dword v194, v[4:5], off
	v_lshl_add_u64 v[4:5], v[4:5], 0, s[0:1]
	global_load_dword v196, v[4:5], off offset:-4096
	global_load_dword v198, v[4:5], off
	v_lshl_add_u64 v[4:5], v[4:5], 0, s[0:1]
	global_load_dword v200, v[4:5], off offset:-4096
	global_load_dword v202, v[4:5], off
	v_lshl_add_u64 v[4:5], v[4:5], 0, s[0:1]
	global_load_dword v204, v[4:5], off offset:-4096
	global_load_dword v206, v[4:5], off
	v_lshl_add_u64 v[4:5], v[4:5], 0, s[0:1]
	global_load_dword v208, v[4:5], off offset:-4096
	global_load_dword v210, v[4:5], off
	v_lshl_add_u64 v[4:5], v[4:5], 0, s[0:1]
	global_load_dword v212, v[4:5], off offset:-4096
	global_load_dword v214, v[4:5], off
	v_lshl_add_u64 v[4:5], v[4:5], 0, s[0:1]
	global_load_dword v216, v[4:5], off offset:-4096
	global_load_dword v218, v[4:5], off
	v_lshl_add_u64 v[4:5], v[4:5], 0, s[0:1]
	global_load_dword v220, v[4:5], off offset:-4096
	global_load_dword v222, v[4:5], off
	v_lshl_add_u64 v[4:5], v[4:5], 0, s[0:1]
	global_load_dword v224, v[4:5], off offset:-4096
	global_load_dword v226, v[4:5], off
	v_lshl_add_u64 v[4:5], v[4:5], 0, s[0:1]
	global_load_dword v228, v[4:5], off offset:-4096
	global_load_dword v230, v[4:5], off
	v_lshl_add_u64 v[4:5], v[4:5], 0, s[0:1]
	global_load_dword v232, v[4:5], off offset:-4096
	global_load_dword v234, v[4:5], off
	v_lshl_add_u64 v[4:5], v[4:5], 0, s[0:1]
	global_load_dword v236, v[4:5], off offset:-4096
	global_load_dword v238, v[4:5], off
	v_lshl_add_u64 v[4:5], v[4:5], 0, s[0:1]
	global_load_dword v240, v[4:5], off offset:-4096
	global_load_dword v242, v[4:5], off
	v_lshl_add_u64 v[4:5], v[4:5], 0, s[0:1]
	global_load_dword v244, v[4:5], off offset:-4096
	global_load_dword v246, v[4:5], off
	v_lshl_add_u64 v[4:5], v[4:5], 0, s[0:1]
	s_and_b32 s20, s42, 0x70
	s_add_i32 s30, s21, -1
	s_add_i32 s31, s10, -2
	s_add_i32 s97, s18, -3
	s_add_i32 s3, s4, -4
	s_add_i32 s63, s91, -5
	s_add_i32 s79, s13, -6
	s_and_b32 s81, vcc_lo, 0x7e
	s_add_i32 s70, s44, s42
	s_add_i32 s76, s44, s21
	s_add_i32 s19, s44, s10
	s_add_i32 s69, s44, s18
	s_add_i32 s53, s44, s4
	s_add_i32 s94, s44, s91
	s_add_i32 s88, s44, s13
	s_add_i32 s45, s65, vcc_lo
	s_lshl_b32 s0, s20, 2
	s_and_b32 s1, s30, 0x7e
	s_and_b32 s20, s31, 0x7c
	s_and_b32 s30, s97, 0x7e
	s_and_b32 s3, s3, 0x78
	s_and_b32 s31, s63, 0x7e
	s_and_b32 s63, s79, 0x7c
	s_lshl_b32 s79, s81, 2
	s_and_b32 s70, s70, 0x78
	s_and_b32 s76, s76, 0x7f
	s_and_b32 s19, s19, 0x7e
	s_and_b32 s69, s69, 0x7f
	s_and_b32 s53, s53, 0x7c
	s_and_b32 s81, s94, 0x7f
	s_and_b32 s88, s88, 0x7e
	s_and_b32 s45, s45, 0x7f
	s_add_i32 s0, s49, s0
	s_lshl_b32 s1, s1, 2
	s_lshl_b32 s20, s20, 2
	s_lshl_b32 s30, s30, 2
	s_lshl_b32 s3, s3, 2
	s_lshl_b32 s31, s31, 2
	s_lshl_b32 s63, s63, 2
	s_add_i32 s79, s49, s79
	s_lshl_b32 s70, s70, 2
	s_lshl_b32 s76, s76, 2
	s_lshl_b32 s19, s19, 2
	s_lshl_b32 s69, s69, 2
	s_lshl_b32 s53, s53, 2
	s_lshl_b32 s81, s81, 2
	s_lshl_b32 s88, s88, 2
	s_lshl_b32 s45, s45, 2
	v_mov_b32_e32 v13, s0
	s_add_i32 s0, s49, s1
	s_add_i32 s1, s49, s20
	s_add_i32 s20, s49, s30
	s_add_i32 s3, s49, s3
	s_add_i32 s30, s49, s31
	s_add_i32 s31, s49, s63
	v_mov_b32_e32 v15, s79
	s_add_i32 s63, s49, s70
	s_add_i32 s70, s49, s76
	s_add_i32 s19, s49, s19
	s_add_i32 s69, s49, s69
	s_add_i32 s53, s49, s53
	s_add_i32 s76, s49, s81
	s_add_i32 s79, s49, s88
	s_add_i32 s45, s49, s45
	v_mov_b32_e32 v19, s1
	v_mov_b32_e32 v20, s20
	v_mov_b32_e32 v24, s3
	v_mov_b32_e32 v25, s30
	v_mov_b32_e32 v26, s31
	v_mov_b32_e32 v27, s63
	v_mov_b32_e32 v28, s70
	v_mov_b32_e32 v29, s19
	v_mov_b32_e32 v30, s69
	v_mov_b32_e32 v31, s53
	v_mov_b32_e32 v32, s76
	v_mov_b32_e32 v33, s79
	v_mov_b32_e32 v17, s0
	v_mov_b32_e32 v40, s45
	ds_read_b32 v18, v13
	ds_read_b32 v21, v15
	ds_read_b32 v22, v17
	ds_read_b32 v19, v19
	ds_read_b32 v23, v20
	ds_read_b32 v24, v24
	ds_read_b32 v20, v25
	ds_read_b32 v25, v26
	ds_read_b32 v26, v27
	ds_read_b32 v28, v28
	ds_read_b32 v27, v29
	ds_read_b32 v29, v30
	ds_read_b32 v30, v31
	ds_read_b32 v32, v32
	ds_read_b32 v31, v33
	ds_read_b32 v33, v40
	s_add_i32 vcc_hi, vcc_hi, 2
	s_add_i32 s21, s21, s11
	s_add_i32 s10, s10, s12
	s_add_i32 s18, s18, s14
	s_add_i32 s4, s4, s15
	s_add_i32 s91, s91, s16
	s_add_i32 s13, s13, s17
	s_add_i32 vcc_lo, vcc_lo, s90
	s_add_i32 s42, s42, s5
	s_waitcnt vmcnt(62) lgkmcnt(0)
; __device__ __forceinline__ void p0_prologue(Frame& F) {
;     ...
; #pragma unroll 2
;             for (int m = 0; m < 128; ++m) { const float wv = wsrc[(size_t)m * 1024];
; #pragma unroll
;                 for (int j = 0; j < 8; ++j) acc8[j] += scr[(m * (c0 + j)) & 127] * wv; }
	v_pk_fma_f32 v[8:9], v[120:121], v[18:19], v[8:9] op_sel_hi:[0,1,1]
	v_pk_fma_f32 v[2:3], v[120:121], v[22:23], v[2:3] op_sel_hi:[0,1,1]
	v_pk_fma_f32 v[10:11], v[120:121], v[24:25], v[10:11] op_sel_hi:[0,1,1]
	v_pk_fma_f32 v[6:7], v[120:121], v[20:21], v[6:7] op_sel_hi:[0,1,1]
	v_pk_fma_f32 v[8:9], v[122:123], v[26:27], v[8:9] op_sel_hi:[0,1,1]
	v_pk_fma_f32 v[2:3], v[122:123], v[28:29], v[2:3] op_sel_hi:[0,1,1]
	v_pk_fma_f32 v[10:11], v[122:123], v[30:31], v[10:11] op_sel_hi:[0,1,1]
	v_pk_fma_f32 v[6:7], v[122:123], v[32:33], v[6:7] op_sel_hi:[0,1,1]
	s_and_b32 s20, s42, 0x70
	s_add_i32 s30, s21, -1
	s_add_i32 s31, s10, -2
	s_add_i32 s97, s18, -3
	s_add_i32 s3, s4, -4
	s_add_i32 s63, s91, -5
	s_add_i32 s79, s13, -6
	s_and_b32 s81, vcc_lo, 0x7e
	s_add_i32 s70, s44, s42
	s_add_i32 s76, s44, s21
	s_add_i32 s19, s44, s10
	s_add_i32 s69, s44, s18
	s_add_i32 s53, s44, s4
	s_add_i32 s94, s44, s91
	s_add_i32 s88, s44, s13
	s_add_i32 s45, s65, vcc_lo
	s_lshl_b32 s0, s20, 2
	s_and_b32 s1, s30, 0x7e
	s_and_b32 s20, s31, 0x7c
	s_and_b32 s30, s97, 0x7e
	s_and_b32 s3, s3, 0x78
	s_and_b32 s31, s63, 0x7e
	s_and_b32 s63, s79, 0x7c
	s_lshl_b32 s79, s81, 2
	s_and_b32 s70, s70, 0x78
	s_and_b32 s76, s76, 0x7f
	s_and_b32 s19, s19, 0x7e
	s_and_b32 s69, s69, 0x7f
	s_and_b32 s53, s53, 0x7c
	s_and_b32 s81, s94, 0x7f
	s_and_b32 s88, s88, 0x7e
	s_and_b32 s45, s45, 0x7f
	s_add_i32 s0, s49, s0
	s_lshl_b32 s1, s1, 2
	s_lshl_b32 s20, s20, 2
	s_lshl_b32 s30, s30, 2
	s_lshl_b32 s3, s3, 2
	s_lshl_b32 s31, s31, 2
	s_lshl_b32 s63, s63, 2
	s_add_i32 s79, s49, s79
	s_lshl_b32 s70, s70, 2
	s_lshl_b32 s76, s76, 2
	s_lshl_b32 s19, s19, 2
	s_lshl_b32 s69, s69, 2
	s_lshl_b32 s53, s53, 2
	s_lshl_b32 s81, s81, 2
	s_lshl_b32 s88, s88, 2
	s_lshl_b32 s45, s45, 2
	v_mov_b32_e32 v13, s0
	s_add_i32 s0, s49, s1
	s_add_i32 s1, s49, s20
	s_add_i32 s20, s49, s30
	s_add_i32 s3, s49, s3
	s_add_i32 s30, s49, s31
	s_add_i32 s31, s49, s63
	v_mov_b32_e32 v15, s79
	s_add_i32 s63, s49, s70
	s_add_i32 s70, s49, s76
	s_add_i32 s19, s49, s19
	s_add_i32 s69, s49, s69
	s_add_i32 s53, s49, s53
	s_add_i32 s76, s49, s81
	s_add_i32 s79, s49, s88
	s_add_i32 s45, s49, s45
	v_mov_b32_e32 v19, s1
	v_mov_b32_e32 v20, s20
	v_mov_b32_e32 v24, s3
	v_mov_b32_e32 v25, s30
	v_mov_b32_e32 v26, s31
	v_mov_b32_e32 v27, s63
	v_mov_b32_e32 v28, s70
	v_mov_b32_e32 v29, s19
	v_mov_b32_e32 v30, s69
	v_mov_b32_e32 v31, s53
	v_mov_b32_e32 v32, s76
	v_mov_b32_e32 v33, s79
	v_mov_b32_e32 v17, s0
	v_mov_b32_e32 v40, s45
	ds_read_b32 v18, v13
	ds_read_b32 v21, v15
	ds_read_b32 v22, v17
	ds_read_b32 v19, v19
	ds_read_b32 v23, v20
	ds_read_b32 v24, v24
	ds_read_b32 v20, v25
	ds_read_b32 v25, v26
	ds_read_b32 v26, v27
	ds_read_b32 v28, v28
	ds_read_b32 v27, v29
	ds_read_b32 v29, v30
	ds_read_b32 v30, v31
	ds_read_b32 v32, v32
	ds_read_b32 v31, v33
	ds_read_b32 v33, v40
	s_add_i32 vcc_hi, vcc_hi, 2
	s_add_i32 s21, s21, s11
	s_add_i32 s10, s10, s12
	s_add_i32 s18, s18, s14
	s_add_i32 s4, s4, s15
	s_add_i32 s91, s91, s16
	s_add_i32 s13, s13, s17
	s_add_i32 vcc_lo, vcc_lo, s90
	s_add_i32 s42, s42, s5
	s_waitcnt vmcnt(60) lgkmcnt(0)
	v_pk_fma_f32 v[8:9], v[124:125], v[18:19], v[8:9] op_sel_hi:[0,1,1]
	v_pk_fma_f32 v[2:3], v[124:125], v[22:23], v[2:3] op_sel_hi:[0,1,1]
	v_pk_fma_f32 v[10:11], v[124:125], v[24:25], v[10:11] op_sel_hi:[0,1,1]
	v_pk_fma_f32 v[6:7], v[124:125], v[20:21], v[6:7] op_sel_hi:[0,1,1]
	v_pk_fma_f32 v[8:9], v[126:127], v[26:27], v[8:9] op_sel_hi:[0,1,1]
	v_pk_fma_f32 v[2:3], v[126:127], v[28:29], v[2:3] op_sel_hi:[0,1,1]
	v_pk_fma_f32 v[10:11], v[126:127], v[30:31], v[10:11] op_sel_hi:[0,1,1]
	v_pk_fma_f32 v[6:7], v[126:127], v[32:33], v[6:7] op_sel_hi:[0,1,1]
	s_and_b32 s20, s42, 0x70
	s_add_i32 s30, s21, -1
	s_add_i32 s31, s10, -2
	s_add_i32 s97, s18, -3
	s_add_i32 s3, s4, -4
	s_add_i32 s63, s91, -5
	s_add_i32 s79, s13, -6
	s_and_b32 s81, vcc_lo, 0x7e
	s_add_i32 s70, s44, s42
	s_add_i32 s76, s44, s21
	s_add_i32 s19, s44, s10
	s_add_i32 s69, s44, s18
	s_add_i32 s53, s44, s4
	s_add_i32 s94, s44, s91
	s_add_i32 s88, s44, s13
	s_add_i32 s45, s65, vcc_lo
	s_lshl_b32 s0, s20, 2
	s_and_b32 s1, s30, 0x7e
	s_and_b32 s20, s31, 0x7c
	s_and_b32 s30, s97, 0x7e
	s_and_b32 s3, s3, 0x78
	s_and_b32 s31, s63, 0x7e
	s_and_b32 s63, s79, 0x7c
	s_lshl_b32 s79, s81, 2
	s_and_b32 s70, s70, 0x78
	s_and_b32 s76, s76, 0x7f
	s_and_b32 s19, s19, 0x7e
	s_and_b32 s69, s69, 0x7f
	s_and_b32 s53, s53, 0x7c
	s_and_b32 s81, s94, 0x7f
	s_and_b32 s88, s88, 0x7e
	s_and_b32 s45, s45, 0x7f
	s_add_i32 s0, s49, s0
	s_lshl_b32 s1, s1, 2
	s_lshl_b32 s20, s20, 2
	s_lshl_b32 s30, s30, 2
	s_lshl_b32 s3, s3, 2
	s_lshl_b32 s31, s31, 2
	s_lshl_b32 s63, s63, 2
	s_add_i32 s79, s49, s79
	s_lshl_b32 s70, s70, 2
	s_lshl_b32 s76, s76, 2
	s_lshl_b32 s19, s19, 2
	s_lshl_b32 s69, s69, 2
	s_lshl_b32 s53, s53, 2
	s_lshl_b32 s81, s81, 2
	s_lshl_b32 s88, s88, 2
	s_lshl_b32 s45, s45, 2
	v_mov_b32_e32 v13, s0
	s_add_i32 s0, s49, s1
	s_add_i32 s1, s49, s20
	s_add_i32 s20, s49, s30
	s_add_i32 s3, s49, s3
	s_add_i32 s30, s49, s31
	s_add_i32 s31, s49, s63
	v_mov_b32_e32 v15, s79
	s_add_i32 s63, s49, s70
	s_add_i32 s70, s49, s76
	s_add_i32 s19, s49, s19
	s_add_i32 s69, s49, s69
	s_add_i32 s53, s49, s53
	s_add_i32 s76, s49, s81
	s_add_i32 s79, s49, s88
	s_add_i32 s45, s49, s45
	v_mov_b32_e32 v19, s1
	v_mov_b32_e32 v20, s20
	v_mov_b32_e32 v24, s3
	v_mov_b32_e32 v25, s30
	v_mov_b32_e32 v26, s31
	v_mov_b32_e32 v27, s63
	v_mov_b32_e32 v28, s70
	v_mov_b32_e32 v29, s19
	v_mov_b32_e32 v30, s69
	v_mov_b32_e32 v31, s53
	v_mov_b32_e32 v32, s76
	v_mov_b32_e32 v33, s79
	v_mov_b32_e32 v17, s0
	v_mov_b32_e32 v40, s45
	ds_read_b32 v18, v13
	ds_read_b32 v21, v15
	ds_read_b32 v22, v17
	ds_read_b32 v19, v19
	ds_read_b32 v23, v20
	ds_read_b32 v24, v24
	ds_read_b32 v20, v25
	ds_read_b32 v25, v26
	ds_read_b32 v26, v27
	ds_read_b32 v28, v28
	ds_read_b32 v27, v29
	ds_read_b32 v29, v30
	ds_read_b32 v30, v31
	ds_read_b32 v32, v32
	ds_read_b32 v31, v33
	ds_read_b32 v33, v40
	s_add_i32 vcc_hi, vcc_hi, 2
	s_add_i32 s21, s21, s11
	s_add_i32 s10, s10, s12
	s_add_i32 s18, s18, s14
	s_add_i32 s4, s4, s15
	s_add_i32 s91, s91, s16
	s_add_i32 s13, s13, s17
	s_add_i32 vcc_lo, vcc_lo, s90
	s_add_i32 s42, s42, s5
	s_waitcnt vmcnt(58) lgkmcnt(0)
; __device__ __forceinline__ void p0_prologue(Frame& F) {
;     ...
; #pragma unroll 2
;             for (int m = 0; m < 128; ++m) { const float wv = wsrc[(size_t)m * 1024];
; #pragma unroll
;                 for (int j = 0; j < 8; ++j) acc8[j] += scr[(m * (c0 + j)) & 127] * wv; }
	v_pk_fma_f32 v[8:9], v[128:129], v[18:19], v[8:9] op_sel_hi:[0,1,1]
	v_pk_fma_f32 v[2:3], v[128:129], v[22:23], v[2:3] op_sel_hi:[0,1,1]
	v_pk_fma_f32 v[10:11], v[128:129], v[24:25], v[10:11] op_sel_hi:[0,1,1]
	v_pk_fma_f32 v[6:7], v[128:129], v[20:21], v[6:7] op_sel_hi:[0,1,1]
	v_pk_fma_f32 v[8:9], v[130:131], v[26:27], v[8:9] op_sel_hi:[0,1,1]
	v_pk_fma_f32 v[2:3], v[130:131], v[28:29], v[2:3] op_sel_hi:[0,1,1]
	v_pk_fma_f32 v[10:11], v[130:131], v[30:31], v[10:11] op_sel_hi:[0,1,1]
	v_pk_fma_f32 v[6:7], v[130:131], v[32:33], v[6:7] op_sel_hi:[0,1,1]
	s_and_b32 s20, s42, 0x70
	s_add_i32 s30, s21, -1
	s_add_i32 s31, s10, -2
	s_add_i32 s97, s18, -3
	s_add_i32 s3, s4, -4
	s_add_i32 s63, s91, -5
	s_add_i32 s79, s13, -6
	s_and_b32 s81, vcc_lo, 0x7e
	s_add_i32 s70, s44, s42
	s_add_i32 s76, s44, s21
	s_add_i32 s19, s44, s10
	s_add_i32 s69, s44, s18
	s_add_i32 s53, s44, s4
	s_add_i32 s94, s44, s91
	s_add_i32 s88, s44, s13
	s_add_i32 s45, s65, vcc_lo
	s_lshl_b32 s0, s20, 2
	s_and_b32 s1, s30, 0x7e
	s_and_b32 s20, s31, 0x7c
	s_and_b32 s30, s97, 0x7e
	s_and_b32 s3, s3, 0x78
	s_and_b32 s31, s63, 0x7e
	s_and_b32 s63, s79, 0x7c
	s_lshl_b32 s79, s81, 2
	s_and_b32 s70, s70, 0x78
	s_and_b32 s76, s76, 0x7f
	s_and_b32 s19, s19, 0x7e
	s_and_b32 s69, s69, 0x7f
	s_and_b32 s53, s53, 0x7c
	s_and_b32 s81, s94, 0x7f
	s_and_b32 s88, s88, 0x7e
	s_and_b32 s45, s45, 0x7f
	s_add_i32 s0, s49, s0
	s_lshl_b32 s1, s1, 2
	s_lshl_b32 s20, s20, 2
	s_lshl_b32 s30, s30, 2
	s_lshl_b32 s3, s3, 2
	s_lshl_b32 s31, s31, 2
	s_lshl_b32 s63, s63, 2
	s_add_i32 s79, s49, s79
	s_lshl_b32 s70, s70, 2
	s_lshl_b32 s76, s76, 2
	s_lshl_b32 s19, s19, 2
	s_lshl_b32 s69, s69, 2
	s_lshl_b32 s53, s53, 2
	s_lshl_b32 s81, s81, 2
	s_lshl_b32 s88, s88, 2
	s_lshl_b32 s45, s45, 2
	v_mov_b32_e32 v13, s0
	s_add_i32 s0, s49, s1
	s_add_i32 s1, s49, s20
	s_add_i32 s20, s49, s30
	s_add_i32 s3, s49, s3
	s_add_i32 s30, s49, s31
	s_add_i32 s31, s49, s63
	v_mov_b32_e32 v15, s79
	s_add_i32 s63, s49, s70
	s_add_i32 s70, s49, s76
	s_add_i32 s19, s49, s19
	s_add_i32 s69, s49, s69
	s_add_i32 s53, s49, s53
	s_add_i32 s76, s49, s81
	s_add_i32 s79, s49, s88
	s_add_i32 s45, s49, s45
	v_mov_b32_e32 v19, s1
	v_mov_b32_e32 v20, s20
	v_mov_b32_e32 v24, s3
	v_mov_b32_e32 v25, s30
	v_mov_b32_e32 v26, s31
	v_mov_b32_e32 v27, s63
	v_mov_b32_e32 v28, s70
	v_mov_b32_e32 v29, s19
	v_mov_b32_e32 v30, s69
	v_mov_b32_e32 v31, s53
	v_mov_b32_e32 v32, s76
	v_mov_b32_e32 v33, s79
	v_mov_b32_e32 v17, s0
	v_mov_b32_e32 v40, s45
	ds_read_b32 v18, v13
	ds_read_b32 v21, v15
	ds_read_b32 v22, v17
	ds_read_b32 v19, v19
	ds_read_b32 v23, v20
	ds_read_b32 v24, v24
	ds_read_b32 v20, v25
	ds_read_b32 v25, v26
	ds_read_b32 v26, v27
	ds_read_b32 v28, v28
	ds_read_b32 v27, v29
	ds_read_b32 v29, v30
	ds_read_b32 v30, v31
	ds_read_b32 v32, v32
	ds_read_b32 v31, v33
	ds_read_b32 v33, v40
	s_add_i32 vcc_hi, vcc_hi, 2
	s_add_i32 s21, s21, s11
	s_add_i32 s10, s10, s12
	s_add_i32 s18, s18, s14
	s_add_i32 s4, s4, s15
	s_add_i32 s91, s91, s16
	s_add_i32 s13, s13, s17
	s_add_i32 vcc_lo, vcc_lo, s90
	s_add_i32 s42, s42, s5
	s_waitcnt vmcnt(56) lgkmcnt(0)
	v_pk_fma_f32 v[8:9], v[132:133], v[18:19], v[8:9] op_sel_hi:[0,1,1]
	v_pk_fma_f32 v[2:3], v[132:133], v[22:23], v[2:3] op_sel_hi:[0,1,1]
	v_pk_fma_f32 v[10:11], v[132:133], v[24:25], v[10:11] op_sel_hi:[0,1,1]
	v_pk_fma_f32 v[6:7], v[132:133], v[20:21], v[6:7] op_sel_hi:[0,1,1]
	v_pk_fma_f32 v[8:9], v[134:135], v[26:27], v[8:9] op_sel_hi:[0,1,1]
	v_pk_fma_f32 v[2:3], v[134:135], v[28:29], v[2:3] op_sel_hi:[0,1,1]
	v_pk_fma_f32 v[10:11], v[134:135], v[30:31], v[10:11] op_sel_hi:[0,1,1]
	v_pk_fma_f32 v[6:7], v[134:135], v[32:33], v[6:7] op_sel_hi:[0,1,1]
	s_and_b32 s20, s42, 0x70
	s_add_i32 s30, s21, -1
	s_add_i32 s31, s10, -2
	s_add_i32 s97, s18, -3
	s_add_i32 s3, s4, -4
	s_add_i32 s63, s91, -5
	s_add_i32 s79, s13, -6
	s_and_b32 s81, vcc_lo, 0x7e
	s_add_i32 s70, s44, s42
	s_add_i32 s76, s44, s21
	s_add_i32 s19, s44, s10
	s_add_i32 s69, s44, s18
	s_add_i32 s53, s44, s4
	s_add_i32 s94, s44, s91
	s_add_i32 s88, s44, s13
	s_add_i32 s45, s65, vcc_lo
	s_lshl_b32 s0, s20, 2
	s_and_b32 s1, s30, 0x7e
	s_and_b32 s20, s31, 0x7c
	s_and_b32 s30, s97, 0x7e
	s_and_b32 s3, s3, 0x78
	s_and_b32 s31, s63, 0x7e
	s_and_b32 s63, s79, 0x7c
	s_lshl_b32 s79, s81, 2
	s_and_b32 s70, s70, 0x78
	s_and_b32 s76, s76, 0x7f
	s_and_b32 s19, s19, 0x7e
	s_and_b32 s69, s69, 0x7f
	s_and_b32 s53, s53, 0x7c
	s_and_b32 s81, s94, 0x7f
	s_and_b32 s88, s88, 0x7e
	s_and_b32 s45, s45, 0x7f
	s_add_i32 s0, s49, s0
	s_lshl_b32 s1, s1, 2
	s_lshl_b32 s20, s20, 2
	s_lshl_b32 s30, s30, 2
	s_lshl_b32 s3, s3, 2
	s_lshl_b32 s31, s31, 2
	s_lshl_b32 s63, s63, 2
	s_add_i32 s79, s49, s79
	s_lshl_b32 s70, s70, 2
	s_lshl_b32 s76, s76, 2
	s_lshl_b32 s19, s19, 2
	s_lshl_b32 s69, s69, 2
	s_lshl_b32 s53, s53, 2
	s_lshl_b32 s81, s81, 2
	s_lshl_b32 s88, s88, 2
	s_lshl_b32 s45, s45, 2
	v_mov_b32_e32 v13, s0
	s_add_i32 s0, s49, s1
	s_add_i32 s1, s49, s20
	s_add_i32 s20, s49, s30
	s_add_i32 s3, s49, s3
	s_add_i32 s30, s49, s31
	s_add_i32 s31, s49, s63
	v_mov_b32_e32 v15, s79
	s_add_i32 s63, s49, s70
	s_add_i32 s70, s49, s76
	s_add_i32 s19, s49, s19
	s_add_i32 s69, s49, s69
	s_add_i32 s53, s49, s53
	s_add_i32 s76, s49, s81
	s_add_i32 s79, s49, s88
	s_add_i32 s45, s49, s45
	v_mov_b32_e32 v19, s1
	v_mov_b32_e32 v20, s20
	v_mov_b32_e32 v24, s3
	v_mov_b32_e32 v25, s30
	v_mov_b32_e32 v26, s31
	v_mov_b32_e32 v27, s63
	v_mov_b32_e32 v28, s70
	v_mov_b32_e32 v29, s19
	v_mov_b32_e32 v30, s69
	v_mov_b32_e32 v31, s53
	v_mov_b32_e32 v32, s76
	v_mov_b32_e32 v33, s79
	v_mov_b32_e32 v17, s0
	v_mov_b32_e32 v40, s45
	ds_read_b32 v18, v13
	ds_read_b32 v21, v15
	ds_read_b32 v22, v17
	ds_read_b32 v19, v19
	ds_read_b32 v23, v20
	ds_read_b32 v24, v24
	ds_read_b32 v20, v25
	ds_read_b32 v25, v26
	ds_read_b32 v26, v27
	ds_read_b32 v28, v28
	ds_read_b32 v27, v29
	ds_read_b32 v29, v30
	ds_read_b32 v30, v31
	ds_read_b32 v32, v32
	ds_read_b32 v31, v33
	ds_read_b32 v33, v40
	s_add_i32 vcc_hi, vcc_hi, 2
	s_add_i32 s21, s21, s11
	s_add_i32 s10, s10, s12
	s_add_i32 s18, s18, s14
	s_add_i32 s4, s4, s15
	s_add_i32 s91, s91, s16
	s_add_i32 s13, s13, s17
	s_add_i32 vcc_lo, vcc_lo, s90
	s_add_i32 s42, s42, s5
	s_waitcnt vmcnt(54) lgkmcnt(0)
; __device__ __forceinline__ void p0_prologue(Frame& F) {
;     ...
; #pragma unroll 2
;             for (int m = 0; m < 128; ++m) { const float wv = wsrc[(size_t)m * 1024];
; #pragma unroll
;                 for (int j = 0; j < 8; ++j) acc8[j] += scr[(m * (c0 + j)) & 127] * wv; }
	v_pk_fma_f32 v[8:9], v[136:137], v[18:19], v[8:9] op_sel_hi:[0,1,1]
	v_pk_fma_f32 v[2:3], v[136:137], v[22:23], v[2:3] op_sel_hi:[0,1,1]
	v_pk_fma_f32 v[10:11], v[136:137], v[24:25], v[10:11] op_sel_hi:[0,1,1]
	v_pk_fma_f32 v[6:7], v[136:137], v[20:21], v[6:7] op_sel_hi:[0,1,1]
	v_pk_fma_f32 v[8:9], v[138:139], v[26:27], v[8:9] op_sel_hi:[0,1,1]
	v_pk_fma_f32 v[2:3], v[138:139], v[28:29], v[2:3] op_sel_hi:[0,1,1]
	v_pk_fma_f32 v[10:11], v[138:139], v[30:31], v[10:11] op_sel_hi:[0,1,1]
	v_pk_fma_f32 v[6:7], v[138:139], v[32:33], v[6:7] op_sel_hi:[0,1,1]
	s_and_b32 s20, s42, 0x70
	s_add_i32 s30, s21, -1
	s_add_i32 s31, s10, -2
	s_add_i32 s97, s18, -3
	s_add_i32 s3, s4, -4
	s_add_i32 s63, s91, -5
	s_add_i32 s79, s13, -6
	s_and_b32 s81, vcc_lo, 0x7e
	s_add_i32 s70, s44, s42
	s_add_i32 s76, s44, s21
	s_add_i32 s19, s44, s10
	s_add_i32 s69, s44, s18
	s_add_i32 s53, s44, s4
	s_add_i32 s94, s44, s91
	s_add_i32 s88, s44, s13
	s_add_i32 s45, s65, vcc_lo
	s_lshl_b32 s0, s20, 2
	s_and_b32 s1, s30, 0x7e
	s_and_b32 s20, s31, 0x7c
	s_and_b32 s30, s97, 0x7e
	s_and_b32 s3, s3, 0x78
	s_and_b32 s31, s63, 0x7e
	s_and_b32 s63, s79, 0x7c
	s_lshl_b32 s79, s81, 2
	s_and_b32 s70, s70, 0x78
	s_and_b32 s76, s76, 0x7f
	s_and_b32 s19, s19, 0x7e
	s_and_b32 s69, s69, 0x7f
	s_and_b32 s53, s53, 0x7c
	s_and_b32 s81, s94, 0x7f
	s_and_b32 s88, s88, 0x7e
	s_and_b32 s45, s45, 0x7f
	s_add_i32 s0, s49, s0
	s_lshl_b32 s1, s1, 2
	s_lshl_b32 s20, s20, 2
	s_lshl_b32 s30, s30, 2
	s_lshl_b32 s3, s3, 2
	s_lshl_b32 s31, s31, 2
	s_lshl_b32 s63, s63, 2
	s_add_i32 s79, s49, s79
	s_lshl_b32 s70, s70, 2
	s_lshl_b32 s76, s76, 2
	s_lshl_b32 s19, s19, 2
	s_lshl_b32 s69, s69, 2
	s_lshl_b32 s53, s53, 2
	s_lshl_b32 s81, s81, 2
	s_lshl_b32 s88, s88, 2
	s_lshl_b32 s45, s45, 2
	v_mov_b32_e32 v13, s0
	s_add_i32 s0, s49, s1
	s_add_i32 s1, s49, s20
	s_add_i32 s20, s49, s30
	s_add_i32 s3, s49, s3
	s_add_i32 s30, s49, s31
	s_add_i32 s31, s49, s63
	v_mov_b32_e32 v15, s79
	s_add_i32 s63, s49, s70
	s_add_i32 s70, s49, s76
	s_add_i32 s19, s49, s19
	s_add_i32 s69, s49, s69
	s_add_i32 s53, s49, s53
	s_add_i32 s76, s49, s81
	s_add_i32 s79, s49, s88
	s_add_i32 s45, s49, s45
	v_mov_b32_e32 v19, s1
	v_mov_b32_e32 v20, s20
	v_mov_b32_e32 v24, s3
	v_mov_b32_e32 v25, s30
	v_mov_b32_e32 v26, s31
	v_mov_b32_e32 v27, s63
	v_mov_b32_e32 v28, s70
	v_mov_b32_e32 v29, s19
	v_mov_b32_e32 v30, s69
	v_mov_b32_e32 v31, s53
	v_mov_b32_e32 v32, s76
	v_mov_b32_e32 v33, s79
	v_mov_b32_e32 v17, s0
	v_mov_b32_e32 v40, s45
	ds_read_b32 v18, v13
	ds_read_b32 v21, v15
	ds_read_b32 v22, v17
	ds_read_b32 v19, v19
	ds_read_b32 v23, v20
	ds_read_b32 v24, v24
	ds_read_b32 v20, v25
	ds_read_b32 v25, v26
	ds_read_b32 v26, v27
	ds_read_b32 v28, v28
	ds_read_b32 v27, v29
	ds_read_b32 v29, v30
	ds_read_b32 v30, v31
	ds_read_b32 v32, v32
	ds_read_b32 v31, v33
	ds_read_b32 v33, v40
	s_add_i32 vcc_hi, vcc_hi, 2
	s_add_i32 s21, s21, s11
	s_add_i32 s10, s10, s12
	s_add_i32 s18, s18, s14
	s_add_i32 s4, s4, s15
	s_add_i32 s91, s91, s16
	s_add_i32 s13, s13, s17
	s_add_i32 vcc_lo, vcc_lo, s90
	s_add_i32 s42, s42, s5
	s_waitcnt vmcnt(52) lgkmcnt(0)
	v_pk_fma_f32 v[8:9], v[140:141], v[18:19], v[8:9] op_sel_hi:[0,1,1]
	v_pk_fma_f32 v[2:3], v[140:141], v[22:23], v[2:3] op_sel_hi:[0,1,1]
	v_pk_fma_f32 v[10:11], v[140:141], v[24:25], v[10:11] op_sel_hi:[0,1,1]
	v_pk_fma_f32 v[6:7], v[140:141], v[20:21], v[6:7] op_sel_hi:[0,1,1]
	v_pk_fma_f32 v[8:9], v[142:143], v[26:27], v[8:9] op_sel_hi:[0,1,1]
	v_pk_fma_f32 v[2:3], v[142:143], v[28:29], v[2:3] op_sel_hi:[0,1,1]
	v_pk_fma_f32 v[10:11], v[142:143], v[30:31], v[10:11] op_sel_hi:[0,1,1]
	v_pk_fma_f32 v[6:7], v[142:143], v[32:33], v[6:7] op_sel_hi:[0,1,1]
	s_and_b32 s20, s42, 0x70
	s_add_i32 s30, s21, -1
	s_add_i32 s31, s10, -2
	s_add_i32 s97, s18, -3
	s_add_i32 s3, s4, -4
	s_add_i32 s63, s91, -5
	s_add_i32 s79, s13, -6
	s_and_b32 s81, vcc_lo, 0x7e
	s_add_i32 s70, s44, s42
	s_add_i32 s76, s44, s21
	s_add_i32 s19, s44, s10
	s_add_i32 s69, s44, s18
	s_add_i32 s53, s44, s4
	s_add_i32 s94, s44, s91
	s_add_i32 s88, s44, s13
	s_add_i32 s45, s65, vcc_lo
	s_lshl_b32 s0, s20, 2
	s_and_b32 s1, s30, 0x7e
	s_and_b32 s20, s31, 0x7c
	s_and_b32 s30, s97, 0x7e
	s_and_b32 s3, s3, 0x78
	s_and_b32 s31, s63, 0x7e
	s_and_b32 s63, s79, 0x7c
	s_lshl_b32 s79, s81, 2
	s_and_b32 s70, s70, 0x78
	s_and_b32 s76, s76, 0x7f
	s_and_b32 s19, s19, 0x7e
	s_and_b32 s69, s69, 0x7f
	s_and_b32 s53, s53, 0x7c
	s_and_b32 s81, s94, 0x7f
	s_and_b32 s88, s88, 0x7e
	s_and_b32 s45, s45, 0x7f
	s_add_i32 s0, s49, s0
	s_lshl_b32 s1, s1, 2
	s_lshl_b32 s20, s20, 2
	s_lshl_b32 s30, s30, 2
	s_lshl_b32 s3, s3, 2
	s_lshl_b32 s31, s31, 2
	s_lshl_b32 s63, s63, 2
	s_add_i32 s79, s49, s79
	s_lshl_b32 s70, s70, 2
	s_lshl_b32 s76, s76, 2
	s_lshl_b32 s19, s19, 2
	s_lshl_b32 s69, s69, 2
	s_lshl_b32 s53, s53, 2
	s_lshl_b32 s81, s81, 2
	s_lshl_b32 s88, s88, 2
	s_lshl_b32 s45, s45, 2
	v_mov_b32_e32 v13, s0
	s_add_i32 s0, s49, s1
	s_add_i32 s1, s49, s20
	s_add_i32 s20, s49, s30
	s_add_i32 s3, s49, s3
	s_add_i32 s30, s49, s31
	s_add_i32 s31, s49, s63
	v_mov_b32_e32 v15, s79
	s_add_i32 s63, s49, s70
	s_add_i32 s70, s49, s76
	s_add_i32 s19, s49, s19
	s_add_i32 s69, s49, s69
	s_add_i32 s53, s49, s53
	s_add_i32 s76, s49, s81
	s_add_i32 s79, s49, s88
	s_add_i32 s45, s49, s45
	v_mov_b32_e32 v19, s1
	v_mov_b32_e32 v20, s20
	v_mov_b32_e32 v24, s3
	v_mov_b32_e32 v25, s30
	v_mov_b32_e32 v26, s31
	v_mov_b32_e32 v27, s63
	v_mov_b32_e32 v28, s70
	v_mov_b32_e32 v29, s19
	v_mov_b32_e32 v30, s69
	v_mov_b32_e32 v31, s53
	v_mov_b32_e32 v32, s76
	v_mov_b32_e32 v33, s79
	v_mov_b32_e32 v17, s0
	v_mov_b32_e32 v40, s45
	ds_read_b32 v18, v13
	ds_read_b32 v21, v15
	ds_read_b32 v22, v17
	ds_read_b32 v19, v19
	ds_read_b32 v23, v20
	ds_read_b32 v24, v24
	ds_read_b32 v20, v25
	ds_read_b32 v25, v26
	ds_read_b32 v26, v27
	ds_read_b32 v28, v28
	ds_read_b32 v27, v29
	ds_read_b32 v29, v30
	ds_read_b32 v30, v31
	ds_read_b32 v32, v32
	ds_read_b32 v31, v33
	ds_read_b32 v33, v40
	s_add_i32 vcc_hi, vcc_hi, 2
	s_add_i32 s21, s21, s11
	s_add_i32 s10, s10, s12
	s_add_i32 s18, s18, s14
	s_add_i32 s4, s4, s15
	s_add_i32 s91, s91, s16
	s_add_i32 s13, s13, s17
	s_add_i32 vcc_lo, vcc_lo, s90
	s_add_i32 s42, s42, s5
	s_waitcnt vmcnt(50) lgkmcnt(0)
; __device__ __forceinline__ void p0_prologue(Frame& F) {
;     ...
; #pragma unroll 2
;             for (int m = 0; m < 128; ++m) { const float wv = wsrc[(size_t)m * 1024];
; #pragma unroll
;                 for (int j = 0; j < 8; ++j) acc8[j] += scr[(m * (c0 + j)) & 127] * wv; }
	v_pk_fma_f32 v[8:9], v[144:145], v[18:19], v[8:9] op_sel_hi:[0,1,1]
	v_pk_fma_f32 v[2:3], v[144:145], v[22:23], v[2:3] op_sel_hi:[0,1,1]
	v_pk_fma_f32 v[10:11], v[144:145], v[24:25], v[10:11] op_sel_hi:[0,1,1]
	v_pk_fma_f32 v[6:7], v[144:145], v[20:21], v[6:7] op_sel_hi:[0,1,1]
	v_pk_fma_f32 v[8:9], v[146:147], v[26:27], v[8:9] op_sel_hi:[0,1,1]
	v_pk_fma_f32 v[2:3], v[146:147], v[28:29], v[2:3] op_sel_hi:[0,1,1]
	v_pk_fma_f32 v[10:11], v[146:147], v[30:31], v[10:11] op_sel_hi:[0,1,1]
	v_pk_fma_f32 v[6:7], v[146:147], v[32:33], v[6:7] op_sel_hi:[0,1,1]
	s_and_b32 s20, s42, 0x70
	s_add_i32 s30, s21, -1
	s_add_i32 s31, s10, -2
	s_add_i32 s97, s18, -3
	s_add_i32 s3, s4, -4
	s_add_i32 s63, s91, -5
	s_add_i32 s79, s13, -6
	s_and_b32 s81, vcc_lo, 0x7e
	s_add_i32 s70, s44, s42
	s_add_i32 s76, s44, s21
	s_add_i32 s19, s44, s10
	s_add_i32 s69, s44, s18
	s_add_i32 s53, s44, s4
	s_add_i32 s94, s44, s91
	s_add_i32 s88, s44, s13
	s_add_i32 s45, s65, vcc_lo
	s_lshl_b32 s0, s20, 2
	s_and_b32 s1, s30, 0x7e
	s_and_b32 s20, s31, 0x7c
	s_and_b32 s30, s97, 0x7e
	s_and_b32 s3, s3, 0x78
	s_and_b32 s31, s63, 0x7e
	s_and_b32 s63, s79, 0x7c
	s_lshl_b32 s79, s81, 2
	s_and_b32 s70, s70, 0x78
	s_and_b32 s76, s76, 0x7f
	s_and_b32 s19, s19, 0x7e
	s_and_b32 s69, s69, 0x7f
	s_and_b32 s53, s53, 0x7c
	s_and_b32 s81, s94, 0x7f
	s_and_b32 s88, s88, 0x7e
	s_and_b32 s45, s45, 0x7f
	s_add_i32 s0, s49, s0
	s_lshl_b32 s1, s1, 2
	s_lshl_b32 s20, s20, 2
	s_lshl_b32 s30, s30, 2
	s_lshl_b32 s3, s3, 2
	s_lshl_b32 s31, s31, 2
	s_lshl_b32 s63, s63, 2
	s_add_i32 s79, s49, s79
	s_lshl_b32 s70, s70, 2
	s_lshl_b32 s76, s76, 2
	s_lshl_b32 s19, s19, 2
	s_lshl_b32 s69, s69, 2
	s_lshl_b32 s53, s53, 2
	s_lshl_b32 s81, s81, 2
	s_lshl_b32 s88, s88, 2
	s_lshl_b32 s45, s45, 2
	v_mov_b32_e32 v13, s0
	s_add_i32 s0, s49, s1
	s_add_i32 s1, s49, s20
	s_add_i32 s20, s49, s30
	s_add_i32 s3, s49, s3
	s_add_i32 s30, s49, s31
	s_add_i32 s31, s49, s63
	v_mov_b32_e32 v15, s79
	s_add_i32 s63, s49, s70
	s_add_i32 s70, s49, s76
	s_add_i32 s19, s49, s19
	s_add_i32 s69, s49, s69
	s_add_i32 s53, s49, s53
	s_add_i32 s76, s49, s81
	s_add_i32 s79, s49, s88
	s_add_i32 s45, s49, s45
	v_mov_b32_e32 v19, s1
	v_mov_b32_e32 v20, s20
	v_mov_b32_e32 v24, s3
	v_mov_b32_e32 v25, s30
	v_mov_b32_e32 v26, s31
	v_mov_b32_e32 v27, s63
	v_mov_b32_e32 v28, s70
	v_mov_b32_e32 v29, s19
	v_mov_b32_e32 v30, s69
	v_mov_b32_e32 v31, s53
	v_mov_b32_e32 v32, s76
	v_mov_b32_e32 v33, s79
	v_mov_b32_e32 v17, s0
	v_mov_b32_e32 v40, s45
	ds_read_b32 v18, v13
	ds_read_b32 v21, v15
	ds_read_b32 v22, v17
	ds_read_b32 v19, v19
	ds_read_b32 v23, v20
	ds_read_b32 v24, v24
	ds_read_b32 v20, v25
	ds_read_b32 v25, v26
	ds_read_b32 v26, v27
	ds_read_b32 v28, v28
	ds_read_b32 v27, v29
	ds_read_b32 v29, v30
	ds_read_b32 v30, v31
	ds_read_b32 v32, v32
	ds_read_b32 v31, v33
	ds_read_b32 v33, v40
	s_add_i32 vcc_hi, vcc_hi, 2
	s_add_i32 s21, s21, s11
	s_add_i32 s10, s10, s12
	s_add_i32 s18, s18, s14
	s_add_i32 s4, s4, s15
	s_add_i32 s91, s91, s16
	s_add_i32 s13, s13, s17
	s_add_i32 vcc_lo, vcc_lo, s90
	s_add_i32 s42, s42, s5
	s_waitcnt vmcnt(48) lgkmcnt(0)
	v_pk_fma_f32 v[8:9], v[148:149], v[18:19], v[8:9] op_sel_hi:[0,1,1]
	v_pk_fma_f32 v[2:3], v[148:149], v[22:23], v[2:3] op_sel_hi:[0,1,1]
	v_pk_fma_f32 v[10:11], v[148:149], v[24:25], v[10:11] op_sel_hi:[0,1,1]
	v_pk_fma_f32 v[6:7], v[148:149], v[20:21], v[6:7] op_sel_hi:[0,1,1]
	v_pk_fma_f32 v[8:9], v[150:151], v[26:27], v[8:9] op_sel_hi:[0,1,1]
	v_pk_fma_f32 v[2:3], v[150:151], v[28:29], v[2:3] op_sel_hi:[0,1,1]
	v_pk_fma_f32 v[10:11], v[150:151], v[30:31], v[10:11] op_sel_hi:[0,1,1]
	v_pk_fma_f32 v[6:7], v[150:151], v[32:33], v[6:7] op_sel_hi:[0,1,1]
	s_and_b32 s20, s42, 0x70
	s_add_i32 s30, s21, -1
	s_add_i32 s31, s10, -2
	s_add_i32 s97, s18, -3
	s_add_i32 s3, s4, -4
	s_add_i32 s63, s91, -5
	s_add_i32 s79, s13, -6
	s_and_b32 s81, vcc_lo, 0x7e
	s_add_i32 s70, s44, s42
	s_add_i32 s76, s44, s21
	s_add_i32 s19, s44, s10
	s_add_i32 s69, s44, s18
	s_add_i32 s53, s44, s4
	s_add_i32 s94, s44, s91
	s_add_i32 s88, s44, s13
	s_add_i32 s45, s65, vcc_lo
	s_lshl_b32 s0, s20, 2
	s_and_b32 s1, s30, 0x7e
	s_and_b32 s20, s31, 0x7c
	s_and_b32 s30, s97, 0x7e
	s_and_b32 s3, s3, 0x78
	s_and_b32 s31, s63, 0x7e
	s_and_b32 s63, s79, 0x7c
	s_lshl_b32 s79, s81, 2
	s_and_b32 s70, s70, 0x78
	s_and_b32 s76, s76, 0x7f
	s_and_b32 s19, s19, 0x7e
	s_and_b32 s69, s69, 0x7f
	s_and_b32 s53, s53, 0x7c
	s_and_b32 s81, s94, 0x7f
	s_and_b32 s88, s88, 0x7e
	s_and_b32 s45, s45, 0x7f
	s_add_i32 s0, s49, s0
	s_lshl_b32 s1, s1, 2
	s_lshl_b32 s20, s20, 2
	s_lshl_b32 s30, s30, 2
	s_lshl_b32 s3, s3, 2
	s_lshl_b32 s31, s31, 2
	s_lshl_b32 s63, s63, 2
	s_add_i32 s79, s49, s79
	s_lshl_b32 s70, s70, 2
	s_lshl_b32 s76, s76, 2
	s_lshl_b32 s19, s19, 2
	s_lshl_b32 s69, s69, 2
	s_lshl_b32 s53, s53, 2
	s_lshl_b32 s81, s81, 2
	s_lshl_b32 s88, s88, 2
	s_lshl_b32 s45, s45, 2
	v_mov_b32_e32 v13, s0
	s_add_i32 s0, s49, s1
	s_add_i32 s1, s49, s20
	s_add_i32 s20, s49, s30
	s_add_i32 s3, s49, s3
	s_add_i32 s30, s49, s31
	s_add_i32 s31, s49, s63
	v_mov_b32_e32 v15, s79
	s_add_i32 s63, s49, s70
	s_add_i32 s70, s49, s76
	s_add_i32 s19, s49, s19
	s_add_i32 s69, s49, s69
	s_add_i32 s53, s49, s53
	s_add_i32 s76, s49, s81
	s_add_i32 s79, s49, s88
	s_add_i32 s45, s49, s45
	v_mov_b32_e32 v19, s1
	v_mov_b32_e32 v20, s20
	v_mov_b32_e32 v24, s3
	v_mov_b32_e32 v25, s30
	v_mov_b32_e32 v26, s31
	v_mov_b32_e32 v27, s63
	v_mov_b32_e32 v28, s70
	v_mov_b32_e32 v29, s19
	v_mov_b32_e32 v30, s69
	v_mov_b32_e32 v31, s53
	v_mov_b32_e32 v32, s76
	v_mov_b32_e32 v33, s79
	v_mov_b32_e32 v17, s0
	v_mov_b32_e32 v40, s45
	ds_read_b32 v18, v13
	ds_read_b32 v21, v15
	ds_read_b32 v22, v17
	ds_read_b32 v19, v19
	ds_read_b32 v23, v20
	ds_read_b32 v24, v24
	ds_read_b32 v20, v25
	ds_read_b32 v25, v26
	ds_read_b32 v26, v27
	ds_read_b32 v28, v28
	ds_read_b32 v27, v29
	ds_read_b32 v29, v30
	ds_read_b32 v30, v31
	ds_read_b32 v32, v32
	ds_read_b32 v31, v33
	ds_read_b32 v33, v40
	s_add_i32 vcc_hi, vcc_hi, 2
	s_add_i32 s21, s21, s11
	s_add_i32 s10, s10, s12
	s_add_i32 s18, s18, s14
	s_add_i32 s4, s4, s15
	s_add_i32 s91, s91, s16
	s_add_i32 s13, s13, s17
	s_add_i32 vcc_lo, vcc_lo, s90
	s_add_i32 s42, s42, s5
	s_waitcnt vmcnt(46) lgkmcnt(0)
; __device__ __forceinline__ void p0_prologue(Frame& F) {
;     ...
; #pragma unroll 2
;             for (int m = 0; m < 128; ++m) { const float wv = wsrc[(size_t)m * 1024];
; #pragma unroll
;                 for (int j = 0; j < 8; ++j) acc8[j] += scr[(m * (c0 + j)) & 127] * wv; }
	v_pk_fma_f32 v[8:9], v[152:153], v[18:19], v[8:9] op_sel_hi:[0,1,1]
	v_pk_fma_f32 v[2:3], v[152:153], v[22:23], v[2:3] op_sel_hi:[0,1,1]
	v_pk_fma_f32 v[10:11], v[152:153], v[24:25], v[10:11] op_sel_hi:[0,1,1]
	v_pk_fma_f32 v[6:7], v[152:153], v[20:21], v[6:7] op_sel_hi:[0,1,1]
	v_pk_fma_f32 v[8:9], v[154:155], v[26:27], v[8:9] op_sel_hi:[0,1,1]
	v_pk_fma_f32 v[2:3], v[154:155], v[28:29], v[2:3] op_sel_hi:[0,1,1]
	v_pk_fma_f32 v[10:11], v[154:155], v[30:31], v[10:11] op_sel_hi:[0,1,1]
	v_pk_fma_f32 v[6:7], v[154:155], v[32:33], v[6:7] op_sel_hi:[0,1,1]
	s_and_b32 s20, s42, 0x70
	s_add_i32 s30, s21, -1
	s_add_i32 s31, s10, -2
	s_add_i32 s97, s18, -3
	s_add_i32 s3, s4, -4
	s_add_i32 s63, s91, -5
	s_add_i32 s79, s13, -6
	s_and_b32 s81, vcc_lo, 0x7e
	s_add_i32 s70, s44, s42
	s_add_i32 s76, s44, s21
	s_add_i32 s19, s44, s10
	s_add_i32 s69, s44, s18
	s_add_i32 s53, s44, s4
	s_add_i32 s94, s44, s91
	s_add_i32 s88, s44, s13
	s_add_i32 s45, s65, vcc_lo
	s_lshl_b32 s0, s20, 2
	s_and_b32 s1, s30, 0x7e
	s_and_b32 s20, s31, 0x7c
	s_and_b32 s30, s97, 0x7e
	s_and_b32 s3, s3, 0x78
	s_and_b32 s31, s63, 0x7e
	s_and_b32 s63, s79, 0x7c
	s_lshl_b32 s79, s81, 2
	s_and_b32 s70, s70, 0x78
	s_and_b32 s76, s76, 0x7f
	s_and_b32 s19, s19, 0x7e
	s_and_b32 s69, s69, 0x7f
	s_and_b32 s53, s53, 0x7c
	s_and_b32 s81, s94, 0x7f
	s_and_b32 s88, s88, 0x7e
	s_and_b32 s45, s45, 0x7f
	s_add_i32 s0, s49, s0
	s_lshl_b32 s1, s1, 2
	s_lshl_b32 s20, s20, 2
	s_lshl_b32 s30, s30, 2
	s_lshl_b32 s3, s3, 2
	s_lshl_b32 s31, s31, 2
	s_lshl_b32 s63, s63, 2
	s_add_i32 s79, s49, s79
	s_lshl_b32 s70, s70, 2
	s_lshl_b32 s76, s76, 2
	s_lshl_b32 s19, s19, 2
	s_lshl_b32 s69, s69, 2
	s_lshl_b32 s53, s53, 2
	s_lshl_b32 s81, s81, 2
	s_lshl_b32 s88, s88, 2
	s_lshl_b32 s45, s45, 2
	v_mov_b32_e32 v13, s0
	s_add_i32 s0, s49, s1
	s_add_i32 s1, s49, s20
	s_add_i32 s20, s49, s30
	s_add_i32 s3, s49, s3
	s_add_i32 s30, s49, s31
	s_add_i32 s31, s49, s63
	v_mov_b32_e32 v15, s79
	s_add_i32 s63, s49, s70
	s_add_i32 s70, s49, s76
	s_add_i32 s19, s49, s19
	s_add_i32 s69, s49, s69
	s_add_i32 s53, s49, s53
	s_add_i32 s76, s49, s81
	s_add_i32 s79, s49, s88
	s_add_i32 s45, s49, s45
	v_mov_b32_e32 v19, s1
	v_mov_b32_e32 v20, s20
	v_mov_b32_e32 v24, s3
	v_mov_b32_e32 v25, s30
	v_mov_b32_e32 v26, s31
	v_mov_b32_e32 v27, s63
	v_mov_b32_e32 v28, s70
	v_mov_b32_e32 v29, s19
	v_mov_b32_e32 v30, s69
	v_mov_b32_e32 v31, s53
	v_mov_b32_e32 v32, s76
	v_mov_b32_e32 v33, s79
	v_mov_b32_e32 v17, s0
	v_mov_b32_e32 v40, s45
	ds_read_b32 v18, v13
	ds_read_b32 v21, v15
	ds_read_b32 v22, v17
	ds_read_b32 v19, v19
	ds_read_b32 v23, v20
	ds_read_b32 v24, v24
	ds_read_b32 v20, v25
	ds_read_b32 v25, v26
	ds_read_b32 v26, v27
	ds_read_b32 v28, v28
	ds_read_b32 v27, v29
	ds_read_b32 v29, v30
	ds_read_b32 v30, v31
	ds_read_b32 v32, v32
	ds_read_b32 v31, v33
	ds_read_b32 v33, v40
	s_add_i32 vcc_hi, vcc_hi, 2
	s_add_i32 s21, s21, s11
	s_add_i32 s10, s10, s12
	s_add_i32 s18, s18, s14
	s_add_i32 s4, s4, s15
	s_add_i32 s91, s91, s16
	s_add_i32 s13, s13, s17
	s_add_i32 vcc_lo, vcc_lo, s90
	s_add_i32 s42, s42, s5
	s_waitcnt vmcnt(44) lgkmcnt(0)
	v_pk_fma_f32 v[8:9], v[156:157], v[18:19], v[8:9] op_sel_hi:[0,1,1]
	v_pk_fma_f32 v[2:3], v[156:157], v[22:23], v[2:3] op_sel_hi:[0,1,1]
	v_pk_fma_f32 v[10:11], v[156:157], v[24:25], v[10:11] op_sel_hi:[0,1,1]
	v_pk_fma_f32 v[6:7], v[156:157], v[20:21], v[6:7] op_sel_hi:[0,1,1]
	v_pk_fma_f32 v[8:9], v[158:159], v[26:27], v[8:9] op_sel_hi:[0,1,1]
	v_pk_fma_f32 v[2:3], v[158:159], v[28:29], v[2:3] op_sel_hi:[0,1,1]
	v_pk_fma_f32 v[10:11], v[158:159], v[30:31], v[10:11] op_sel_hi:[0,1,1]
	v_pk_fma_f32 v[6:7], v[158:159], v[32:33], v[6:7] op_sel_hi:[0,1,1]
	s_and_b32 s20, s42, 0x70
	s_add_i32 s30, s21, -1
	s_add_i32 s31, s10, -2
	s_add_i32 s97, s18, -3
	s_add_i32 s3, s4, -4
	s_add_i32 s63, s91, -5
	s_add_i32 s79, s13, -6
	s_and_b32 s81, vcc_lo, 0x7e
	s_add_i32 s70, s44, s42
	s_add_i32 s76, s44, s21
	s_add_i32 s19, s44, s10
	s_add_i32 s69, s44, s18
	s_add_i32 s53, s44, s4
	s_add_i32 s94, s44, s91
	s_add_i32 s88, s44, s13
	s_add_i32 s45, s65, vcc_lo
	s_lshl_b32 s0, s20, 2
	s_and_b32 s1, s30, 0x7e
	s_and_b32 s20, s31, 0x7c
	s_and_b32 s30, s97, 0x7e
	s_and_b32 s3, s3, 0x78
	s_and_b32 s31, s63, 0x7e
	s_and_b32 s63, s79, 0x7c
	s_lshl_b32 s79, s81, 2
	s_and_b32 s70, s70, 0x78
	s_and_b32 s76, s76, 0x7f
	s_and_b32 s19, s19, 0x7e
	s_and_b32 s69, s69, 0x7f
	s_and_b32 s53, s53, 0x7c
	s_and_b32 s81, s94, 0x7f
	s_and_b32 s88, s88, 0x7e
	s_and_b32 s45, s45, 0x7f
	s_add_i32 s0, s49, s0
	s_lshl_b32 s1, s1, 2
	s_lshl_b32 s20, s20, 2
	s_lshl_b32 s30, s30, 2
	s_lshl_b32 s3, s3, 2
	s_lshl_b32 s31, s31, 2
	s_lshl_b32 s63, s63, 2
	s_add_i32 s79, s49, s79
	s_lshl_b32 s70, s70, 2
	s_lshl_b32 s76, s76, 2
	s_lshl_b32 s19, s19, 2
	s_lshl_b32 s69, s69, 2
	s_lshl_b32 s53, s53, 2
	s_lshl_b32 s81, s81, 2
	s_lshl_b32 s88, s88, 2
	s_lshl_b32 s45, s45, 2
	v_mov_b32_e32 v13, s0
	s_add_i32 s0, s49, s1
	s_add_i32 s1, s49, s20
	s_add_i32 s20, s49, s30
	s_add_i32 s3, s49, s3
	s_add_i32 s30, s49, s31
	s_add_i32 s31, s49, s63
	v_mov_b32_e32 v15, s79
	s_add_i32 s63, s49, s70
	s_add_i32 s70, s49, s76
	s_add_i32 s19, s49, s19
	s_add_i32 s69, s49, s69
	s_add_i32 s53, s49, s53
	s_add_i32 s76, s49, s81
	s_add_i32 s79, s49, s88
	s_add_i32 s45, s49, s45
	v_mov_b32_e32 v19, s1
	v_mov_b32_e32 v20, s20
	v_mov_b32_e32 v24, s3
	v_mov_b32_e32 v25, s30
	v_mov_b32_e32 v26, s31
	v_mov_b32_e32 v27, s63
	v_mov_b32_e32 v28, s70
	v_mov_b32_e32 v29, s19
	v_mov_b32_e32 v30, s69
	v_mov_b32_e32 v31, s53
	v_mov_b32_e32 v32, s76
	v_mov_b32_e32 v33, s79
	v_mov_b32_e32 v17, s0
	v_mov_b32_e32 v40, s45
	ds_read_b32 v18, v13
	ds_read_b32 v21, v15
	ds_read_b32 v22, v17
	ds_read_b32 v19, v19
	ds_read_b32 v23, v20
	ds_read_b32 v24, v24
	ds_read_b32 v20, v25
	ds_read_b32 v25, v26
	ds_read_b32 v26, v27
	ds_read_b32 v28, v28
	ds_read_b32 v27, v29
	ds_read_b32 v29, v30
	ds_read_b32 v30, v31
	ds_read_b32 v32, v32
	ds_read_b32 v31, v33
	ds_read_b32 v33, v40
	s_add_i32 vcc_hi, vcc_hi, 2
	s_add_i32 s21, s21, s11
	s_add_i32 s10, s10, s12
	s_add_i32 s18, s18, s14
	s_add_i32 s4, s4, s15
	s_add_i32 s91, s91, s16
	s_add_i32 s13, s13, s17
	s_add_i32 vcc_lo, vcc_lo, s90
	s_add_i32 s42, s42, s5
	s_waitcnt vmcnt(42) lgkmcnt(0)
; __device__ __forceinline__ void p0_prologue(Frame& F) {
;     ...
; #pragma unroll 2
;             for (int m = 0; m < 128; ++m) { const float wv = wsrc[(size_t)m * 1024];
; #pragma unroll
;                 for (int j = 0; j < 8; ++j) acc8[j] += scr[(m * (c0 + j)) & 127] * wv; }
	v_pk_fma_f32 v[8:9], v[160:161], v[18:19], v[8:9] op_sel_hi:[0,1,1]
	v_pk_fma_f32 v[2:3], v[160:161], v[22:23], v[2:3] op_sel_hi:[0,1,1]
	v_pk_fma_f32 v[10:11], v[160:161], v[24:25], v[10:11] op_sel_hi:[0,1,1]
	v_pk_fma_f32 v[6:7], v[160:161], v[20:21], v[6:7] op_sel_hi:[0,1,1]
	v_pk_fma_f32 v[8:9], v[162:163], v[26:27], v[8:9] op_sel_hi:[0,1,1]
	v_pk_fma_f32 v[2:3], v[162:163], v[28:29], v[2:3] op_sel_hi:[0,1,1]
	v_pk_fma_f32 v[10:11], v[162:163], v[30:31], v[10:11] op_sel_hi:[0,1,1]
	v_pk_fma_f32 v[6:7], v[162:163], v[32:33], v[6:7] op_sel_hi:[0,1,1]
	s_and_b32 s20, s42, 0x70
	s_add_i32 s30, s21, -1
	s_add_i32 s31, s10, -2
	s_add_i32 s97, s18, -3
	s_add_i32 s3, s4, -4
	s_add_i32 s63, s91, -5
	s_add_i32 s79, s13, -6
	s_and_b32 s81, vcc_lo, 0x7e
	s_add_i32 s70, s44, s42
	s_add_i32 s76, s44, s21
	s_add_i32 s19, s44, s10
	s_add_i32 s69, s44, s18
	s_add_i32 s53, s44, s4
	s_add_i32 s94, s44, s91
	s_add_i32 s88, s44, s13
	s_add_i32 s45, s65, vcc_lo
	s_lshl_b32 s0, s20, 2
	s_and_b32 s1, s30, 0x7e
	s_and_b32 s20, s31, 0x7c
	s_and_b32 s30, s97, 0x7e
	s_and_b32 s3, s3, 0x78
	s_and_b32 s31, s63, 0x7e
	s_and_b32 s63, s79, 0x7c
	s_lshl_b32 s79, s81, 2
	s_and_b32 s70, s70, 0x78
	s_and_b32 s76, s76, 0x7f
	s_and_b32 s19, s19, 0x7e
	s_and_b32 s69, s69, 0x7f
	s_and_b32 s53, s53, 0x7c
	s_and_b32 s81, s94, 0x7f
	s_and_b32 s88, s88, 0x7e
	s_and_b32 s45, s45, 0x7f
	s_add_i32 s0, s49, s0
	s_lshl_b32 s1, s1, 2
	s_lshl_b32 s20, s20, 2
	s_lshl_b32 s30, s30, 2
	s_lshl_b32 s3, s3, 2
	s_lshl_b32 s31, s31, 2
	s_lshl_b32 s63, s63, 2
	s_add_i32 s79, s49, s79
	s_lshl_b32 s70, s70, 2
	s_lshl_b32 s76, s76, 2
	s_lshl_b32 s19, s19, 2
	s_lshl_b32 s69, s69, 2
	s_lshl_b32 s53, s53, 2
	s_lshl_b32 s81, s81, 2
	s_lshl_b32 s88, s88, 2
	s_lshl_b32 s45, s45, 2
	v_mov_b32_e32 v13, s0
	s_add_i32 s0, s49, s1
	s_add_i32 s1, s49, s20
	s_add_i32 s20, s49, s30
	s_add_i32 s3, s49, s3
	s_add_i32 s30, s49, s31
	s_add_i32 s31, s49, s63
	v_mov_b32_e32 v15, s79
	s_add_i32 s63, s49, s70
	s_add_i32 s70, s49, s76
	s_add_i32 s19, s49, s19
	s_add_i32 s69, s49, s69
	s_add_i32 s53, s49, s53
	s_add_i32 s76, s49, s81
	s_add_i32 s79, s49, s88
	s_add_i32 s45, s49, s45
	v_mov_b32_e32 v19, s1
	v_mov_b32_e32 v20, s20
	v_mov_b32_e32 v24, s3
	v_mov_b32_e32 v25, s30
	v_mov_b32_e32 v26, s31
	v_mov_b32_e32 v27, s63
	v_mov_b32_e32 v28, s70
	v_mov_b32_e32 v29, s19
	v_mov_b32_e32 v30, s69
	v_mov_b32_e32 v31, s53
	v_mov_b32_e32 v32, s76
	v_mov_b32_e32 v33, s79
	v_mov_b32_e32 v17, s0
	v_mov_b32_e32 v40, s45
	ds_read_b32 v18, v13
	ds_read_b32 v21, v15
	ds_read_b32 v22, v17
	ds_read_b32 v19, v19
	ds_read_b32 v23, v20
	ds_read_b32 v24, v24
	ds_read_b32 v20, v25
	ds_read_b32 v25, v26
	ds_read_b32 v26, v27
	ds_read_b32 v28, v28
	ds_read_b32 v27, v29
	ds_read_b32 v29, v30
	ds_read_b32 v30, v31
	ds_read_b32 v32, v32
	ds_read_b32 v31, v33
	ds_read_b32 v33, v40
	s_add_i32 vcc_hi, vcc_hi, 2
	s_add_i32 s21, s21, s11
	s_add_i32 s10, s10, s12
	s_add_i32 s18, s18, s14
	s_add_i32 s4, s4, s15
	s_add_i32 s91, s91, s16
	s_add_i32 s13, s13, s17
	s_add_i32 vcc_lo, vcc_lo, s90
	s_add_i32 s42, s42, s5
	s_waitcnt vmcnt(40) lgkmcnt(0)
	v_pk_fma_f32 v[8:9], v[164:165], v[18:19], v[8:9] op_sel_hi:[0,1,1]
	v_pk_fma_f32 v[2:3], v[164:165], v[22:23], v[2:3] op_sel_hi:[0,1,1]
	v_pk_fma_f32 v[10:11], v[164:165], v[24:25], v[10:11] op_sel_hi:[0,1,1]
	v_pk_fma_f32 v[6:7], v[164:165], v[20:21], v[6:7] op_sel_hi:[0,1,1]
	v_pk_fma_f32 v[8:9], v[166:167], v[26:27], v[8:9] op_sel_hi:[0,1,1]
	v_pk_fma_f32 v[2:3], v[166:167], v[28:29], v[2:3] op_sel_hi:[0,1,1]
	v_pk_fma_f32 v[10:11], v[166:167], v[30:31], v[10:11] op_sel_hi:[0,1,1]
	v_pk_fma_f32 v[6:7], v[166:167], v[32:33], v[6:7] op_sel_hi:[0,1,1]
	s_and_b32 s20, s42, 0x70
	s_add_i32 s30, s21, -1
	s_add_i32 s31, s10, -2
	s_add_i32 s97, s18, -3
	s_add_i32 s3, s4, -4
	s_add_i32 s63, s91, -5
	s_add_i32 s79, s13, -6
	s_and_b32 s81, vcc_lo, 0x7e
	s_add_i32 s70, s44, s42
	s_add_i32 s76, s44, s21
	s_add_i32 s19, s44, s10
	s_add_i32 s69, s44, s18
	s_add_i32 s53, s44, s4
	s_add_i32 s94, s44, s91
	s_add_i32 s88, s44, s13
	s_add_i32 s45, s65, vcc_lo
	s_lshl_b32 s0, s20, 2
	s_and_b32 s1, s30, 0x7e
	s_and_b32 s20, s31, 0x7c
	s_and_b32 s30, s97, 0x7e
	s_and_b32 s3, s3, 0x78
	s_and_b32 s31, s63, 0x7e
	s_and_b32 s63, s79, 0x7c
	s_lshl_b32 s79, s81, 2
	s_and_b32 s70, s70, 0x78
	s_and_b32 s76, s76, 0x7f
	s_and_b32 s19, s19, 0x7e
	s_and_b32 s69, s69, 0x7f
	s_and_b32 s53, s53, 0x7c
	s_and_b32 s81, s94, 0x7f
	s_and_b32 s88, s88, 0x7e
	s_and_b32 s45, s45, 0x7f
	s_add_i32 s0, s49, s0
	s_lshl_b32 s1, s1, 2
	s_lshl_b32 s20, s20, 2
	s_lshl_b32 s30, s30, 2
	s_lshl_b32 s3, s3, 2
	s_lshl_b32 s31, s31, 2
	s_lshl_b32 s63, s63, 2
	s_add_i32 s79, s49, s79
	s_lshl_b32 s70, s70, 2
	s_lshl_b32 s76, s76, 2
	s_lshl_b32 s19, s19, 2
	s_lshl_b32 s69, s69, 2
	s_lshl_b32 s53, s53, 2
	s_lshl_b32 s81, s81, 2
	s_lshl_b32 s88, s88, 2
	s_lshl_b32 s45, s45, 2
	v_mov_b32_e32 v13, s0
	s_add_i32 s0, s49, s1
	s_add_i32 s1, s49, s20
	s_add_i32 s20, s49, s30
	s_add_i32 s3, s49, s3
	s_add_i32 s30, s49, s31
	s_add_i32 s31, s49, s63
	v_mov_b32_e32 v15, s79
	s_add_i32 s63, s49, s70
	s_add_i32 s70, s49, s76
	s_add_i32 s19, s49, s19
	s_add_i32 s69, s49, s69
	s_add_i32 s53, s49, s53
	s_add_i32 s76, s49, s81
	s_add_i32 s79, s49, s88
	s_add_i32 s45, s49, s45
	v_mov_b32_e32 v19, s1
	v_mov_b32_e32 v20, s20
	v_mov_b32_e32 v24, s3
	v_mov_b32_e32 v25, s30
	v_mov_b32_e32 v26, s31
	v_mov_b32_e32 v27, s63
	v_mov_b32_e32 v28, s70
	v_mov_b32_e32 v29, s19
	v_mov_b32_e32 v30, s69
	v_mov_b32_e32 v31, s53
	v_mov_b32_e32 v32, s76
	v_mov_b32_e32 v33, s79
	v_mov_b32_e32 v17, s0
	v_mov_b32_e32 v40, s45
	ds_read_b32 v18, v13
	ds_read_b32 v21, v15
	ds_read_b32 v22, v17
	ds_read_b32 v19, v19
	ds_read_b32 v23, v20
	ds_read_b32 v24, v24
	ds_read_b32 v20, v25
	ds_read_b32 v25, v26
	ds_read_b32 v26, v27
	ds_read_b32 v28, v28
	ds_read_b32 v27, v29
	ds_read_b32 v29, v30
	ds_read_b32 v30, v31
	ds_read_b32 v32, v32
	ds_read_b32 v31, v33
	ds_read_b32 v33, v40
	s_add_i32 vcc_hi, vcc_hi, 2
	s_add_i32 s21, s21, s11
	s_add_i32 s10, s10, s12
	s_add_i32 s18, s18, s14
	s_add_i32 s4, s4, s15
	s_add_i32 s91, s91, s16
	s_add_i32 s13, s13, s17
	s_add_i32 vcc_lo, vcc_lo, s90
	s_add_i32 s42, s42, s5
	s_waitcnt vmcnt(38) lgkmcnt(0)
; __device__ __forceinline__ void p0_prologue(Frame& F) {
;     ...
; #pragma unroll 2
;             for (int m = 0; m < 128; ++m) { const float wv = wsrc[(size_t)m * 1024];
; #pragma unroll
;                 for (int j = 0; j < 8; ++j) acc8[j] += scr[(m * (c0 + j)) & 127] * wv; }
	v_pk_fma_f32 v[8:9], v[168:169], v[18:19], v[8:9] op_sel_hi:[0,1,1]
	v_pk_fma_f32 v[2:3], v[168:169], v[22:23], v[2:3] op_sel_hi:[0,1,1]
	v_pk_fma_f32 v[10:11], v[168:169], v[24:25], v[10:11] op_sel_hi:[0,1,1]
	v_pk_fma_f32 v[6:7], v[168:169], v[20:21], v[6:7] op_sel_hi:[0,1,1]
	v_pk_fma_f32 v[8:9], v[170:171], v[26:27], v[8:9] op_sel_hi:[0,1,1]
	v_pk_fma_f32 v[2:3], v[170:171], v[28:29], v[2:3] op_sel_hi:[0,1,1]
	v_pk_fma_f32 v[10:11], v[170:171], v[30:31], v[10:11] op_sel_hi:[0,1,1]
	v_pk_fma_f32 v[6:7], v[170:171], v[32:33], v[6:7] op_sel_hi:[0,1,1]
	s_and_b32 s20, s42, 0x70
	s_add_i32 s30, s21, -1
	s_add_i32 s31, s10, -2
	s_add_i32 s97, s18, -3
	s_add_i32 s3, s4, -4
	s_add_i32 s63, s91, -5
	s_add_i32 s79, s13, -6
	s_and_b32 s81, vcc_lo, 0x7e
	s_add_i32 s70, s44, s42
	s_add_i32 s76, s44, s21
	s_add_i32 s19, s44, s10
	s_add_i32 s69, s44, s18
	s_add_i32 s53, s44, s4
	s_add_i32 s94, s44, s91
	s_add_i32 s88, s44, s13
	s_add_i32 s45, s65, vcc_lo
	s_lshl_b32 s0, s20, 2
	s_and_b32 s1, s30, 0x7e
	s_and_b32 s20, s31, 0x7c
	s_and_b32 s30, s97, 0x7e
	s_and_b32 s3, s3, 0x78
	s_and_b32 s31, s63, 0x7e
	s_and_b32 s63, s79, 0x7c
	s_lshl_b32 s79, s81, 2
	s_and_b32 s70, s70, 0x78
	s_and_b32 s76, s76, 0x7f
	s_and_b32 s19, s19, 0x7e
	s_and_b32 s69, s69, 0x7f
	s_and_b32 s53, s53, 0x7c
	s_and_b32 s81, s94, 0x7f
	s_and_b32 s88, s88, 0x7e
	s_and_b32 s45, s45, 0x7f
	s_add_i32 s0, s49, s0
	s_lshl_b32 s1, s1, 2
	s_lshl_b32 s20, s20, 2
	s_lshl_b32 s30, s30, 2
	s_lshl_b32 s3, s3, 2
	s_lshl_b32 s31, s31, 2
	s_lshl_b32 s63, s63, 2
	s_add_i32 s79, s49, s79
	s_lshl_b32 s70, s70, 2
	s_lshl_b32 s76, s76, 2
	s_lshl_b32 s19, s19, 2
	s_lshl_b32 s69, s69, 2
	s_lshl_b32 s53, s53, 2
	s_lshl_b32 s81, s81, 2
	s_lshl_b32 s88, s88, 2
	s_lshl_b32 s45, s45, 2
	v_mov_b32_e32 v13, s0
	s_add_i32 s0, s49, s1
	s_add_i32 s1, s49, s20
	s_add_i32 s20, s49, s30
	s_add_i32 s3, s49, s3
	s_add_i32 s30, s49, s31
	s_add_i32 s31, s49, s63
	v_mov_b32_e32 v15, s79
	s_add_i32 s63, s49, s70
	s_add_i32 s70, s49, s76
	s_add_i32 s19, s49, s19
	s_add_i32 s69, s49, s69
	s_add_i32 s53, s49, s53
	s_add_i32 s76, s49, s81
	s_add_i32 s79, s49, s88
	s_add_i32 s45, s49, s45
	v_mov_b32_e32 v19, s1
	v_mov_b32_e32 v20, s20
	v_mov_b32_e32 v24, s3
	v_mov_b32_e32 v25, s30
	v_mov_b32_e32 v26, s31
	v_mov_b32_e32 v27, s63
	v_mov_b32_e32 v28, s70
	v_mov_b32_e32 v29, s19
	v_mov_b32_e32 v30, s69
	v_mov_b32_e32 v31, s53
	v_mov_b32_e32 v32, s76
	v_mov_b32_e32 v33, s79
	v_mov_b32_e32 v17, s0
	v_mov_b32_e32 v40, s45
	ds_read_b32 v18, v13
	ds_read_b32 v21, v15
	ds_read_b32 v22, v17
	ds_read_b32 v19, v19
	ds_read_b32 v23, v20
	ds_read_b32 v24, v24
	ds_read_b32 v20, v25
	ds_read_b32 v25, v26
	ds_read_b32 v26, v27
	ds_read_b32 v28, v28
	ds_read_b32 v27, v29
	ds_read_b32 v29, v30
	ds_read_b32 v30, v31
	ds_read_b32 v32, v32
	ds_read_b32 v31, v33
	ds_read_b32 v33, v40
	s_add_i32 vcc_hi, vcc_hi, 2
	s_add_i32 s21, s21, s11
	s_add_i32 s10, s10, s12
	s_add_i32 s18, s18, s14
	s_add_i32 s4, s4, s15
	s_add_i32 s91, s91, s16
	s_add_i32 s13, s13, s17
	s_add_i32 vcc_lo, vcc_lo, s90
	s_add_i32 s42, s42, s5
	s_waitcnt vmcnt(36) lgkmcnt(0)
	v_pk_fma_f32 v[8:9], v[172:173], v[18:19], v[8:9] op_sel_hi:[0,1,1]
	v_pk_fma_f32 v[2:3], v[172:173], v[22:23], v[2:3] op_sel_hi:[0,1,1]
	v_pk_fma_f32 v[10:11], v[172:173], v[24:25], v[10:11] op_sel_hi:[0,1,1]
	v_pk_fma_f32 v[6:7], v[172:173], v[20:21], v[6:7] op_sel_hi:[0,1,1]
	v_pk_fma_f32 v[8:9], v[174:175], v[26:27], v[8:9] op_sel_hi:[0,1,1]
	v_pk_fma_f32 v[2:3], v[174:175], v[28:29], v[2:3] op_sel_hi:[0,1,1]
	v_pk_fma_f32 v[10:11], v[174:175], v[30:31], v[10:11] op_sel_hi:[0,1,1]
	v_pk_fma_f32 v[6:7], v[174:175], v[32:33], v[6:7] op_sel_hi:[0,1,1]
	s_and_b32 s20, s42, 0x70
	s_add_i32 s30, s21, -1
	s_add_i32 s31, s10, -2
	s_add_i32 s97, s18, -3
	s_add_i32 s3, s4, -4
	s_add_i32 s63, s91, -5
	s_add_i32 s79, s13, -6
	s_and_b32 s81, vcc_lo, 0x7e
	s_add_i32 s70, s44, s42
	s_add_i32 s76, s44, s21
	s_add_i32 s19, s44, s10
	s_add_i32 s69, s44, s18
	s_add_i32 s53, s44, s4
	s_add_i32 s94, s44, s91
	s_add_i32 s88, s44, s13
	s_add_i32 s45, s65, vcc_lo
	s_lshl_b32 s0, s20, 2
	s_and_b32 s1, s30, 0x7e
	s_and_b32 s20, s31, 0x7c
	s_and_b32 s30, s97, 0x7e
	s_and_b32 s3, s3, 0x78
	s_and_b32 s31, s63, 0x7e
	s_and_b32 s63, s79, 0x7c
	s_lshl_b32 s79, s81, 2
	s_and_b32 s70, s70, 0x78
	s_and_b32 s76, s76, 0x7f
	s_and_b32 s19, s19, 0x7e
	s_and_b32 s69, s69, 0x7f
	s_and_b32 s53, s53, 0x7c
	s_and_b32 s81, s94, 0x7f
	s_and_b32 s88, s88, 0x7e
	s_and_b32 s45, s45, 0x7f
	s_add_i32 s0, s49, s0
	s_lshl_b32 s1, s1, 2
	s_lshl_b32 s20, s20, 2
	s_lshl_b32 s30, s30, 2
	s_lshl_b32 s3, s3, 2
	s_lshl_b32 s31, s31, 2
	s_lshl_b32 s63, s63, 2
	s_add_i32 s79, s49, s79
	s_lshl_b32 s70, s70, 2
	s_lshl_b32 s76, s76, 2
	s_lshl_b32 s19, s19, 2
	s_lshl_b32 s69, s69, 2
	s_lshl_b32 s53, s53, 2
	s_lshl_b32 s81, s81, 2
	s_lshl_b32 s88, s88, 2
	s_lshl_b32 s45, s45, 2
	v_mov_b32_e32 v13, s0
	s_add_i32 s0, s49, s1
	s_add_i32 s1, s49, s20
	s_add_i32 s20, s49, s30
	s_add_i32 s3, s49, s3
	s_add_i32 s30, s49, s31
	s_add_i32 s31, s49, s63
	v_mov_b32_e32 v15, s79
	s_add_i32 s63, s49, s70
	s_add_i32 s70, s49, s76
	s_add_i32 s19, s49, s19
	s_add_i32 s69, s49, s69
	s_add_i32 s53, s49, s53
	s_add_i32 s76, s49, s81
	s_add_i32 s79, s49, s88
	s_add_i32 s45, s49, s45
	v_mov_b32_e32 v19, s1
	v_mov_b32_e32 v20, s20
	v_mov_b32_e32 v24, s3
	v_mov_b32_e32 v25, s30
	v_mov_b32_e32 v26, s31
	v_mov_b32_e32 v27, s63
	v_mov_b32_e32 v28, s70
	v_mov_b32_e32 v29, s19
	v_mov_b32_e32 v30, s69
	v_mov_b32_e32 v31, s53
	v_mov_b32_e32 v32, s76
	v_mov_b32_e32 v33, s79
	v_mov_b32_e32 v17, s0
	v_mov_b32_e32 v40, s45
	ds_read_b32 v18, v13
	ds_read_b32 v21, v15
	ds_read_b32 v22, v17
	ds_read_b32 v19, v19
	ds_read_b32 v23, v20
	ds_read_b32 v24, v24
	ds_read_b32 v20, v25
	ds_read_b32 v25, v26
	ds_read_b32 v26, v27
	ds_read_b32 v28, v28
	ds_read_b32 v27, v29
	ds_read_b32 v29, v30
	ds_read_b32 v30, v31
	ds_read_b32 v32, v32
	ds_read_b32 v31, v33
	ds_read_b32 v33, v40
	s_add_i32 vcc_hi, vcc_hi, 2
	s_add_i32 s21, s21, s11
	s_add_i32 s10, s10, s12
	s_add_i32 s18, s18, s14
	s_add_i32 s4, s4, s15
	s_add_i32 s91, s91, s16
	s_add_i32 s13, s13, s17
	s_add_i32 vcc_lo, vcc_lo, s90
	s_add_i32 s42, s42, s5
	s_waitcnt vmcnt(34) lgkmcnt(0)
; __device__ __forceinline__ void p0_prologue(Frame& F) {
;     ...
; #pragma unroll 2
;             for (int m = 0; m < 128; ++m) { const float wv = wsrc[(size_t)m * 1024];
; #pragma unroll
;                 for (int j = 0; j < 8; ++j) acc8[j] += scr[(m * (c0 + j)) & 127] * wv; }
	v_pk_fma_f32 v[8:9], v[176:177], v[18:19], v[8:9] op_sel_hi:[0,1,1]
	v_pk_fma_f32 v[2:3], v[176:177], v[22:23], v[2:3] op_sel_hi:[0,1,1]
	v_pk_fma_f32 v[10:11], v[176:177], v[24:25], v[10:11] op_sel_hi:[0,1,1]
	v_pk_fma_f32 v[6:7], v[176:177], v[20:21], v[6:7] op_sel_hi:[0,1,1]
	v_pk_fma_f32 v[8:9], v[178:179], v[26:27], v[8:9] op_sel_hi:[0,1,1]
	v_pk_fma_f32 v[2:3], v[178:179], v[28:29], v[2:3] op_sel_hi:[0,1,1]
	v_pk_fma_f32 v[10:11], v[178:179], v[30:31], v[10:11] op_sel_hi:[0,1,1]
	v_pk_fma_f32 v[6:7], v[178:179], v[32:33], v[6:7] op_sel_hi:[0,1,1]
	s_and_b32 s20, s42, 0x70
	s_add_i32 s30, s21, -1
	s_add_i32 s31, s10, -2
	s_add_i32 s97, s18, -3
	s_add_i32 s3, s4, -4
	s_add_i32 s63, s91, -5
	s_add_i32 s79, s13, -6
	s_and_b32 s81, vcc_lo, 0x7e
	s_add_i32 s70, s44, s42
	s_add_i32 s76, s44, s21
	s_add_i32 s19, s44, s10
	s_add_i32 s69, s44, s18
	s_add_i32 s53, s44, s4
	s_add_i32 s94, s44, s91
	s_add_i32 s88, s44, s13
	s_add_i32 s45, s65, vcc_lo
	s_lshl_b32 s0, s20, 2
	s_and_b32 s1, s30, 0x7e
	s_and_b32 s20, s31, 0x7c
	s_and_b32 s30, s97, 0x7e
	s_and_b32 s3, s3, 0x78
	s_and_b32 s31, s63, 0x7e
	s_and_b32 s63, s79, 0x7c
	s_lshl_b32 s79, s81, 2
	s_and_b32 s70, s70, 0x78
	s_and_b32 s76, s76, 0x7f
	s_and_b32 s19, s19, 0x7e
	s_and_b32 s69, s69, 0x7f
	s_and_b32 s53, s53, 0x7c
	s_and_b32 s81, s94, 0x7f
	s_and_b32 s88, s88, 0x7e
	s_and_b32 s45, s45, 0x7f
	s_add_i32 s0, s49, s0
	s_lshl_b32 s1, s1, 2
	s_lshl_b32 s20, s20, 2
	s_lshl_b32 s30, s30, 2
	s_lshl_b32 s3, s3, 2
	s_lshl_b32 s31, s31, 2
	s_lshl_b32 s63, s63, 2
	s_add_i32 s79, s49, s79
	s_lshl_b32 s70, s70, 2
	s_lshl_b32 s76, s76, 2
	s_lshl_b32 s19, s19, 2
	s_lshl_b32 s69, s69, 2
	s_lshl_b32 s53, s53, 2
	s_lshl_b32 s81, s81, 2
	s_lshl_b32 s88, s88, 2
	s_lshl_b32 s45, s45, 2
	v_mov_b32_e32 v13, s0
	s_add_i32 s0, s49, s1
	s_add_i32 s1, s49, s20
	s_add_i32 s20, s49, s30
	s_add_i32 s3, s49, s3
	s_add_i32 s30, s49, s31
	s_add_i32 s31, s49, s63
	v_mov_b32_e32 v15, s79
	s_add_i32 s63, s49, s70
	s_add_i32 s70, s49, s76
	s_add_i32 s19, s49, s19
	s_add_i32 s69, s49, s69
	s_add_i32 s53, s49, s53
	s_add_i32 s76, s49, s81
	s_add_i32 s79, s49, s88
	s_add_i32 s45, s49, s45
	v_mov_b32_e32 v19, s1
	v_mov_b32_e32 v20, s20
	v_mov_b32_e32 v24, s3
	v_mov_b32_e32 v25, s30
	v_mov_b32_e32 v26, s31
	v_mov_b32_e32 v27, s63
	v_mov_b32_e32 v28, s70
	v_mov_b32_e32 v29, s19
	v_mov_b32_e32 v30, s69
	v_mov_b32_e32 v31, s53
	v_mov_b32_e32 v32, s76
	v_mov_b32_e32 v33, s79
	v_mov_b32_e32 v17, s0
	v_mov_b32_e32 v40, s45
	ds_read_b32 v18, v13
	ds_read_b32 v21, v15
	ds_read_b32 v22, v17
	ds_read_b32 v19, v19
	ds_read_b32 v23, v20
	ds_read_b32 v24, v24
	ds_read_b32 v20, v25
	ds_read_b32 v25, v26
	ds_read_b32 v26, v27
	ds_read_b32 v28, v28
	ds_read_b32 v27, v29
	ds_read_b32 v29, v30
	ds_read_b32 v30, v31
	ds_read_b32 v32, v32
	ds_read_b32 v31, v33
	ds_read_b32 v33, v40
	s_add_i32 vcc_hi, vcc_hi, 2
	s_add_i32 s21, s21, s11
	s_add_i32 s10, s10, s12
	s_add_i32 s18, s18, s14
	s_add_i32 s4, s4, s15
	s_add_i32 s91, s91, s16
	s_add_i32 s13, s13, s17
	s_add_i32 vcc_lo, vcc_lo, s90
	s_add_i32 s42, s42, s5
	s_waitcnt vmcnt(32) lgkmcnt(0)
	v_pk_fma_f32 v[8:9], v[180:181], v[18:19], v[8:9] op_sel_hi:[0,1,1]
	v_pk_fma_f32 v[2:3], v[180:181], v[22:23], v[2:3] op_sel_hi:[0,1,1]
	v_pk_fma_f32 v[10:11], v[180:181], v[24:25], v[10:11] op_sel_hi:[0,1,1]
	v_pk_fma_f32 v[6:7], v[180:181], v[20:21], v[6:7] op_sel_hi:[0,1,1]
	v_pk_fma_f32 v[8:9], v[182:183], v[26:27], v[8:9] op_sel_hi:[0,1,1]
	v_pk_fma_f32 v[2:3], v[182:183], v[28:29], v[2:3] op_sel_hi:[0,1,1]
	v_pk_fma_f32 v[10:11], v[182:183], v[30:31], v[10:11] op_sel_hi:[0,1,1]
	v_pk_fma_f32 v[6:7], v[182:183], v[32:33], v[6:7] op_sel_hi:[0,1,1]
	s_and_b32 s20, s42, 0x70
	s_add_i32 s30, s21, -1
	s_add_i32 s31, s10, -2
	s_add_i32 s97, s18, -3
	s_add_i32 s3, s4, -4
	s_add_i32 s63, s91, -5
	s_add_i32 s79, s13, -6
	s_and_b32 s81, vcc_lo, 0x7e
	s_add_i32 s70, s44, s42
	s_add_i32 s76, s44, s21
	s_add_i32 s19, s44, s10
	s_add_i32 s69, s44, s18
	s_add_i32 s53, s44, s4
	s_add_i32 s94, s44, s91
	s_add_i32 s88, s44, s13
	s_add_i32 s45, s65, vcc_lo
	s_lshl_b32 s0, s20, 2
	s_and_b32 s1, s30, 0x7e
	s_and_b32 s20, s31, 0x7c
	s_and_b32 s30, s97, 0x7e
	s_and_b32 s3, s3, 0x78
	s_and_b32 s31, s63, 0x7e
	s_and_b32 s63, s79, 0x7c
	s_lshl_b32 s79, s81, 2
	s_and_b32 s70, s70, 0x78
	s_and_b32 s76, s76, 0x7f
	s_and_b32 s19, s19, 0x7e
	s_and_b32 s69, s69, 0x7f
	s_and_b32 s53, s53, 0x7c
	s_and_b32 s81, s94, 0x7f
	s_and_b32 s88, s88, 0x7e
	s_and_b32 s45, s45, 0x7f
	s_add_i32 s0, s49, s0
	s_lshl_b32 s1, s1, 2
	s_lshl_b32 s20, s20, 2
	s_lshl_b32 s30, s30, 2
	s_lshl_b32 s3, s3, 2
	s_lshl_b32 s31, s31, 2
	s_lshl_b32 s63, s63, 2
	s_add_i32 s79, s49, s79
	s_lshl_b32 s70, s70, 2
	s_lshl_b32 s76, s76, 2
	s_lshl_b32 s19, s19, 2
	s_lshl_b32 s69, s69, 2
	s_lshl_b32 s53, s53, 2
	s_lshl_b32 s81, s81, 2
	s_lshl_b32 s88, s88, 2
	s_lshl_b32 s45, s45, 2
	v_mov_b32_e32 v13, s0
	s_add_i32 s0, s49, s1
	s_add_i32 s1, s49, s20
	s_add_i32 s20, s49, s30
	s_add_i32 s3, s49, s3
	s_add_i32 s30, s49, s31
	s_add_i32 s31, s49, s63
	v_mov_b32_e32 v15, s79
	s_add_i32 s63, s49, s70
	s_add_i32 s70, s49, s76
	s_add_i32 s19, s49, s19
	s_add_i32 s69, s49, s69
	s_add_i32 s53, s49, s53
	s_add_i32 s76, s49, s81
	s_add_i32 s79, s49, s88
	s_add_i32 s45, s49, s45
	v_mov_b32_e32 v19, s1
	v_mov_b32_e32 v20, s20
	v_mov_b32_e32 v24, s3
	v_mov_b32_e32 v25, s30
	v_mov_b32_e32 v26, s31
	v_mov_b32_e32 v27, s63
	v_mov_b32_e32 v28, s70
	v_mov_b32_e32 v29, s19
	v_mov_b32_e32 v30, s69
	v_mov_b32_e32 v31, s53
	v_mov_b32_e32 v32, s76
	v_mov_b32_e32 v33, s79
	v_mov_b32_e32 v17, s0
	v_mov_b32_e32 v40, s45
	ds_read_b32 v18, v13
	ds_read_b32 v21, v15
	ds_read_b32 v22, v17
	ds_read_b32 v19, v19
	ds_read_b32 v23, v20
	ds_read_b32 v24, v24
	ds_read_b32 v20, v25
	ds_read_b32 v25, v26
	ds_read_b32 v26, v27
	ds_read_b32 v28, v28
	ds_read_b32 v27, v29
	ds_read_b32 v29, v30
	ds_read_b32 v30, v31
	ds_read_b32 v32, v32
	ds_read_b32 v31, v33
	ds_read_b32 v33, v40
	s_add_i32 vcc_hi, vcc_hi, 2
	s_add_i32 s21, s21, s11
	s_add_i32 s10, s10, s12
	s_add_i32 s18, s18, s14
	s_add_i32 s4, s4, s15
	s_add_i32 s91, s91, s16
	s_add_i32 s13, s13, s17
	s_add_i32 vcc_lo, vcc_lo, s90
	s_add_i32 s42, s42, s5
	s_waitcnt vmcnt(30) lgkmcnt(0)
; __device__ __forceinline__ void p0_prologue(Frame& F) {
;     ...
; #pragma unroll 2
;             for (int m = 0; m < 128; ++m) { const float wv = wsrc[(size_t)m * 1024];
; #pragma unroll
;                 for (int j = 0; j < 8; ++j) acc8[j] += scr[(m * (c0 + j)) & 127] * wv; }
	v_pk_fma_f32 v[8:9], v[184:185], v[18:19], v[8:9] op_sel_hi:[0,1,1]
	v_pk_fma_f32 v[2:3], v[184:185], v[22:23], v[2:3] op_sel_hi:[0,1,1]
	v_pk_fma_f32 v[10:11], v[184:185], v[24:25], v[10:11] op_sel_hi:[0,1,1]
	v_pk_fma_f32 v[6:7], v[184:185], v[20:21], v[6:7] op_sel_hi:[0,1,1]
	v_pk_fma_f32 v[8:9], v[186:187], v[26:27], v[8:9] op_sel_hi:[0,1,1]
	v_pk_fma_f32 v[2:3], v[186:187], v[28:29], v[2:3] op_sel_hi:[0,1,1]
	v_pk_fma_f32 v[10:11], v[186:187], v[30:31], v[10:11] op_sel_hi:[0,1,1]
	v_pk_fma_f32 v[6:7], v[186:187], v[32:33], v[6:7] op_sel_hi:[0,1,1]
	s_and_b32 s20, s42, 0x70
	s_add_i32 s30, s21, -1
	s_add_i32 s31, s10, -2
	s_add_i32 s97, s18, -3
	s_add_i32 s3, s4, -4
	s_add_i32 s63, s91, -5
	s_add_i32 s79, s13, -6
	s_and_b32 s81, vcc_lo, 0x7e
	s_add_i32 s70, s44, s42
	s_add_i32 s76, s44, s21
	s_add_i32 s19, s44, s10
	s_add_i32 s69, s44, s18
	s_add_i32 s53, s44, s4
	s_add_i32 s94, s44, s91
	s_add_i32 s88, s44, s13
	s_add_i32 s45, s65, vcc_lo
	s_lshl_b32 s0, s20, 2
	s_and_b32 s1, s30, 0x7e
	s_and_b32 s20, s31, 0x7c
	s_and_b32 s30, s97, 0x7e
	s_and_b32 s3, s3, 0x78
	s_and_b32 s31, s63, 0x7e
	s_and_b32 s63, s79, 0x7c
	s_lshl_b32 s79, s81, 2
	s_and_b32 s70, s70, 0x78
	s_and_b32 s76, s76, 0x7f
	s_and_b32 s19, s19, 0x7e
	s_and_b32 s69, s69, 0x7f
	s_and_b32 s53, s53, 0x7c
	s_and_b32 s81, s94, 0x7f
	s_and_b32 s88, s88, 0x7e
	s_and_b32 s45, s45, 0x7f
	s_add_i32 s0, s49, s0
	s_lshl_b32 s1, s1, 2
	s_lshl_b32 s20, s20, 2
	s_lshl_b32 s30, s30, 2
	s_lshl_b32 s3, s3, 2
	s_lshl_b32 s31, s31, 2
	s_lshl_b32 s63, s63, 2
	s_add_i32 s79, s49, s79
	s_lshl_b32 s70, s70, 2
	s_lshl_b32 s76, s76, 2
	s_lshl_b32 s19, s19, 2
	s_lshl_b32 s69, s69, 2
	s_lshl_b32 s53, s53, 2
	s_lshl_b32 s81, s81, 2
	s_lshl_b32 s88, s88, 2
	s_lshl_b32 s45, s45, 2
	v_mov_b32_e32 v13, s0
	s_add_i32 s0, s49, s1
	s_add_i32 s1, s49, s20
	s_add_i32 s20, s49, s30
	s_add_i32 s3, s49, s3
	s_add_i32 s30, s49, s31
	s_add_i32 s31, s49, s63
	v_mov_b32_e32 v15, s79
	s_add_i32 s63, s49, s70
	s_add_i32 s70, s49, s76
	s_add_i32 s19, s49, s19
	s_add_i32 s69, s49, s69
	s_add_i32 s53, s49, s53
	s_add_i32 s76, s49, s81
	s_add_i32 s79, s49, s88
	s_add_i32 s45, s49, s45
	v_mov_b32_e32 v19, s1
	v_mov_b32_e32 v20, s20
	v_mov_b32_e32 v24, s3
	v_mov_b32_e32 v25, s30
	v_mov_b32_e32 v26, s31
	v_mov_b32_e32 v27, s63
	v_mov_b32_e32 v28, s70
	v_mov_b32_e32 v29, s19
	v_mov_b32_e32 v30, s69
	v_mov_b32_e32 v31, s53
	v_mov_b32_e32 v32, s76
	v_mov_b32_e32 v33, s79
	v_mov_b32_e32 v17, s0
	v_mov_b32_e32 v40, s45
	ds_read_b32 v18, v13
	ds_read_b32 v21, v15
	ds_read_b32 v22, v17
	ds_read_b32 v19, v19
	ds_read_b32 v23, v20
	ds_read_b32 v24, v24
	ds_read_b32 v20, v25
	ds_read_b32 v25, v26
	ds_read_b32 v26, v27
	ds_read_b32 v28, v28
	ds_read_b32 v27, v29
	ds_read_b32 v29, v30
	ds_read_b32 v30, v31
	ds_read_b32 v32, v32
	ds_read_b32 v31, v33
	ds_read_b32 v33, v40
	s_add_i32 vcc_hi, vcc_hi, 2
	s_add_i32 s21, s21, s11
	s_add_i32 s10, s10, s12
	s_add_i32 s18, s18, s14
	s_add_i32 s4, s4, s15
	s_add_i32 s91, s91, s16
	s_add_i32 s13, s13, s17
	s_add_i32 vcc_lo, vcc_lo, s90
	s_add_i32 s42, s42, s5
	s_waitcnt vmcnt(28) lgkmcnt(0)
	v_pk_fma_f32 v[8:9], v[188:189], v[18:19], v[8:9] op_sel_hi:[0,1,1]
	v_pk_fma_f32 v[2:3], v[188:189], v[22:23], v[2:3] op_sel_hi:[0,1,1]
	v_pk_fma_f32 v[10:11], v[188:189], v[24:25], v[10:11] op_sel_hi:[0,1,1]
	v_pk_fma_f32 v[6:7], v[188:189], v[20:21], v[6:7] op_sel_hi:[0,1,1]
	v_pk_fma_f32 v[8:9], v[190:191], v[26:27], v[8:9] op_sel_hi:[0,1,1]
	v_pk_fma_f32 v[2:3], v[190:191], v[28:29], v[2:3] op_sel_hi:[0,1,1]
	v_pk_fma_f32 v[10:11], v[190:191], v[30:31], v[10:11] op_sel_hi:[0,1,1]
	v_pk_fma_f32 v[6:7], v[190:191], v[32:33], v[6:7] op_sel_hi:[0,1,1]
	s_and_b32 s20, s42, 0x70
	s_add_i32 s30, s21, -1
	s_add_i32 s31, s10, -2
	s_add_i32 s97, s18, -3
	s_add_i32 s3, s4, -4
	s_add_i32 s63, s91, -5
	s_add_i32 s79, s13, -6
	s_and_b32 s81, vcc_lo, 0x7e
	s_add_i32 s70, s44, s42
	s_add_i32 s76, s44, s21
	s_add_i32 s19, s44, s10
	s_add_i32 s69, s44, s18
	s_add_i32 s53, s44, s4
	s_add_i32 s94, s44, s91
	s_add_i32 s88, s44, s13
	s_add_i32 s45, s65, vcc_lo
	s_lshl_b32 s0, s20, 2
	s_and_b32 s1, s30, 0x7e
	s_and_b32 s20, s31, 0x7c
	s_and_b32 s30, s97, 0x7e
	s_and_b32 s3, s3, 0x78
	s_and_b32 s31, s63, 0x7e
	s_and_b32 s63, s79, 0x7c
	s_lshl_b32 s79, s81, 2
	s_and_b32 s70, s70, 0x78
	s_and_b32 s76, s76, 0x7f
	s_and_b32 s19, s19, 0x7e
	s_and_b32 s69, s69, 0x7f
	s_and_b32 s53, s53, 0x7c
	s_and_b32 s81, s94, 0x7f
	s_and_b32 s88, s88, 0x7e
	s_and_b32 s45, s45, 0x7f
	s_add_i32 s0, s49, s0
	s_lshl_b32 s1, s1, 2
	s_lshl_b32 s20, s20, 2
	s_lshl_b32 s30, s30, 2
	s_lshl_b32 s3, s3, 2
	s_lshl_b32 s31, s31, 2
	s_lshl_b32 s63, s63, 2
	s_add_i32 s79, s49, s79
	s_lshl_b32 s70, s70, 2
	s_lshl_b32 s76, s76, 2
	s_lshl_b32 s19, s19, 2
	s_lshl_b32 s69, s69, 2
	s_lshl_b32 s53, s53, 2
	s_lshl_b32 s81, s81, 2
	s_lshl_b32 s88, s88, 2
	s_lshl_b32 s45, s45, 2
	v_mov_b32_e32 v13, s0
	s_add_i32 s0, s49, s1
	s_add_i32 s1, s49, s20
	s_add_i32 s20, s49, s30
	s_add_i32 s3, s49, s3
	s_add_i32 s30, s49, s31
	s_add_i32 s31, s49, s63
	v_mov_b32_e32 v15, s79
	s_add_i32 s63, s49, s70
	s_add_i32 s70, s49, s76
	s_add_i32 s19, s49, s19
	s_add_i32 s69, s49, s69
	s_add_i32 s53, s49, s53
	s_add_i32 s76, s49, s81
	s_add_i32 s79, s49, s88
	s_add_i32 s45, s49, s45
	v_mov_b32_e32 v19, s1
	v_mov_b32_e32 v20, s20
	v_mov_b32_e32 v24, s3
	v_mov_b32_e32 v25, s30
	v_mov_b32_e32 v26, s31
	v_mov_b32_e32 v27, s63
	v_mov_b32_e32 v28, s70
	v_mov_b32_e32 v29, s19
	v_mov_b32_e32 v30, s69
	v_mov_b32_e32 v31, s53
	v_mov_b32_e32 v32, s76
	v_mov_b32_e32 v33, s79
	v_mov_b32_e32 v17, s0
	v_mov_b32_e32 v40, s45
	ds_read_b32 v18, v13
	ds_read_b32 v21, v15
	ds_read_b32 v22, v17
	ds_read_b32 v19, v19
	ds_read_b32 v23, v20
	ds_read_b32 v24, v24
	ds_read_b32 v20, v25
	ds_read_b32 v25, v26
	ds_read_b32 v26, v27
	ds_read_b32 v28, v28
	ds_read_b32 v27, v29
	ds_read_b32 v29, v30
	ds_read_b32 v30, v31
	ds_read_b32 v32, v32
	ds_read_b32 v31, v33
	ds_read_b32 v33, v40
	s_add_i32 vcc_hi, vcc_hi, 2
	s_add_i32 s21, s21, s11
	s_add_i32 s10, s10, s12
	s_add_i32 s18, s18, s14
	s_add_i32 s4, s4, s15
	s_add_i32 s91, s91, s16
	s_add_i32 s13, s13, s17
	s_add_i32 vcc_lo, vcc_lo, s90
	s_add_i32 s42, s42, s5
	s_waitcnt vmcnt(26) lgkmcnt(0)
; __device__ __forceinline__ void p0_prologue(Frame& F) {
;     ...
; #pragma unroll 2
;             for (int m = 0; m < 128; ++m) { const float wv = wsrc[(size_t)m * 1024];
; #pragma unroll
;                 for (int j = 0; j < 8; ++j) acc8[j] += scr[(m * (c0 + j)) & 127] * wv; }
	v_pk_fma_f32 v[8:9], v[192:193], v[18:19], v[8:9] op_sel_hi:[0,1,1]
	v_pk_fma_f32 v[2:3], v[192:193], v[22:23], v[2:3] op_sel_hi:[0,1,1]
	v_pk_fma_f32 v[10:11], v[192:193], v[24:25], v[10:11] op_sel_hi:[0,1,1]
	v_pk_fma_f32 v[6:7], v[192:193], v[20:21], v[6:7] op_sel_hi:[0,1,1]
	v_pk_fma_f32 v[8:9], v[194:195], v[26:27], v[8:9] op_sel_hi:[0,1,1]
	v_pk_fma_f32 v[2:3], v[194:195], v[28:29], v[2:3] op_sel_hi:[0,1,1]
	v_pk_fma_f32 v[10:11], v[194:195], v[30:31], v[10:11] op_sel_hi:[0,1,1]
	v_pk_fma_f32 v[6:7], v[194:195], v[32:33], v[6:7] op_sel_hi:[0,1,1]
	s_and_b32 s20, s42, 0x70
	s_add_i32 s30, s21, -1
	s_add_i32 s31, s10, -2
	s_add_i32 s97, s18, -3
	s_add_i32 s3, s4, -4
	s_add_i32 s63, s91, -5
	s_add_i32 s79, s13, -6
	s_and_b32 s81, vcc_lo, 0x7e
	s_add_i32 s70, s44, s42
	s_add_i32 s76, s44, s21
	s_add_i32 s19, s44, s10
	s_add_i32 s69, s44, s18
	s_add_i32 s53, s44, s4
	s_add_i32 s94, s44, s91
	s_add_i32 s88, s44, s13
	s_add_i32 s45, s65, vcc_lo
	s_lshl_b32 s0, s20, 2
	s_and_b32 s1, s30, 0x7e
	s_and_b32 s20, s31, 0x7c
	s_and_b32 s30, s97, 0x7e
	s_and_b32 s3, s3, 0x78
	s_and_b32 s31, s63, 0x7e
	s_and_b32 s63, s79, 0x7c
	s_lshl_b32 s79, s81, 2
	s_and_b32 s70, s70, 0x78
	s_and_b32 s76, s76, 0x7f
	s_and_b32 s19, s19, 0x7e
	s_and_b32 s69, s69, 0x7f
	s_and_b32 s53, s53, 0x7c
	s_and_b32 s81, s94, 0x7f
	s_and_b32 s88, s88, 0x7e
	s_and_b32 s45, s45, 0x7f
	s_add_i32 s0, s49, s0
	s_lshl_b32 s1, s1, 2
	s_lshl_b32 s20, s20, 2
	s_lshl_b32 s30, s30, 2
	s_lshl_b32 s3, s3, 2
	s_lshl_b32 s31, s31, 2
	s_lshl_b32 s63, s63, 2
	s_add_i32 s79, s49, s79
	s_lshl_b32 s70, s70, 2
	s_lshl_b32 s76, s76, 2
	s_lshl_b32 s19, s19, 2
	s_lshl_b32 s69, s69, 2
	s_lshl_b32 s53, s53, 2
	s_lshl_b32 s81, s81, 2
	s_lshl_b32 s88, s88, 2
	s_lshl_b32 s45, s45, 2
	v_mov_b32_e32 v13, s0
	s_add_i32 s0, s49, s1
	s_add_i32 s1, s49, s20
	s_add_i32 s20, s49, s30
	s_add_i32 s3, s49, s3
	s_add_i32 s30, s49, s31
	s_add_i32 s31, s49, s63
	v_mov_b32_e32 v15, s79
	s_add_i32 s63, s49, s70
	s_add_i32 s70, s49, s76
	s_add_i32 s19, s49, s19
	s_add_i32 s69, s49, s69
	s_add_i32 s53, s49, s53
	s_add_i32 s76, s49, s81
	s_add_i32 s79, s49, s88
	s_add_i32 s45, s49, s45
	v_mov_b32_e32 v19, s1
	v_mov_b32_e32 v20, s20
	v_mov_b32_e32 v24, s3
	v_mov_b32_e32 v25, s30
	v_mov_b32_e32 v26, s31
	v_mov_b32_e32 v27, s63
	v_mov_b32_e32 v28, s70
	v_mov_b32_e32 v29, s19
	v_mov_b32_e32 v30, s69
	v_mov_b32_e32 v31, s53
	v_mov_b32_e32 v32, s76
	v_mov_b32_e32 v33, s79
	v_mov_b32_e32 v17, s0
	v_mov_b32_e32 v40, s45
	ds_read_b32 v18, v13
	ds_read_b32 v21, v15
	ds_read_b32 v22, v17
	ds_read_b32 v19, v19
	ds_read_b32 v23, v20
	ds_read_b32 v24, v24
	ds_read_b32 v20, v25
	ds_read_b32 v25, v26
	ds_read_b32 v26, v27
	ds_read_b32 v28, v28
	ds_read_b32 v27, v29
	ds_read_b32 v29, v30
	ds_read_b32 v30, v31
	ds_read_b32 v32, v32
	ds_read_b32 v31, v33
	ds_read_b32 v33, v40
	s_add_i32 vcc_hi, vcc_hi, 2
	s_add_i32 s21, s21, s11
	s_add_i32 s10, s10, s12
	s_add_i32 s18, s18, s14
	s_add_i32 s4, s4, s15
	s_add_i32 s91, s91, s16
	s_add_i32 s13, s13, s17
	s_add_i32 vcc_lo, vcc_lo, s90
	s_add_i32 s42, s42, s5
	s_waitcnt vmcnt(24) lgkmcnt(0)
	v_pk_fma_f32 v[8:9], v[196:197], v[18:19], v[8:9] op_sel_hi:[0,1,1]
	v_pk_fma_f32 v[2:3], v[196:197], v[22:23], v[2:3] op_sel_hi:[0,1,1]
	v_pk_fma_f32 v[10:11], v[196:197], v[24:25], v[10:11] op_sel_hi:[0,1,1]
	v_pk_fma_f32 v[6:7], v[196:197], v[20:21], v[6:7] op_sel_hi:[0,1,1]
	v_pk_fma_f32 v[8:9], v[198:199], v[26:27], v[8:9] op_sel_hi:[0,1,1]
	v_pk_fma_f32 v[2:3], v[198:199], v[28:29], v[2:3] op_sel_hi:[0,1,1]
	v_pk_fma_f32 v[10:11], v[198:199], v[30:31], v[10:11] op_sel_hi:[0,1,1]
	v_pk_fma_f32 v[6:7], v[198:199], v[32:33], v[6:7] op_sel_hi:[0,1,1]
	s_and_b32 s20, s42, 0x70
	s_add_i32 s30, s21, -1
	s_add_i32 s31, s10, -2
	s_add_i32 s97, s18, -3
	s_add_i32 s3, s4, -4
	s_add_i32 s63, s91, -5
	s_add_i32 s79, s13, -6
	s_and_b32 s81, vcc_lo, 0x7e
	s_add_i32 s70, s44, s42
	s_add_i32 s76, s44, s21
	s_add_i32 s19, s44, s10
	s_add_i32 s69, s44, s18
	s_add_i32 s53, s44, s4
	s_add_i32 s94, s44, s91
	s_add_i32 s88, s44, s13
	s_add_i32 s45, s65, vcc_lo
	s_lshl_b32 s0, s20, 2
	s_and_b32 s1, s30, 0x7e
	s_and_b32 s20, s31, 0x7c
	s_and_b32 s30, s97, 0x7e
	s_and_b32 s3, s3, 0x78
	s_and_b32 s31, s63, 0x7e
	s_and_b32 s63, s79, 0x7c
	s_lshl_b32 s79, s81, 2
	s_and_b32 s70, s70, 0x78
	s_and_b32 s76, s76, 0x7f
	s_and_b32 s19, s19, 0x7e
	s_and_b32 s69, s69, 0x7f
	s_and_b32 s53, s53, 0x7c
	s_and_b32 s81, s94, 0x7f
	s_and_b32 s88, s88, 0x7e
	s_and_b32 s45, s45, 0x7f
	s_add_i32 s0, s49, s0
	s_lshl_b32 s1, s1, 2
	s_lshl_b32 s20, s20, 2
	s_lshl_b32 s30, s30, 2
	s_lshl_b32 s3, s3, 2
	s_lshl_b32 s31, s31, 2
	s_lshl_b32 s63, s63, 2
	s_add_i32 s79, s49, s79
	s_lshl_b32 s70, s70, 2
	s_lshl_b32 s76, s76, 2
	s_lshl_b32 s19, s19, 2
	s_lshl_b32 s69, s69, 2
	s_lshl_b32 s53, s53, 2
	s_lshl_b32 s81, s81, 2
	s_lshl_b32 s88, s88, 2
	s_lshl_b32 s45, s45, 2
	v_mov_b32_e32 v13, s0
	s_add_i32 s0, s49, s1
	s_add_i32 s1, s49, s20
	s_add_i32 s20, s49, s30
	s_add_i32 s3, s49, s3
	s_add_i32 s30, s49, s31
	s_add_i32 s31, s49, s63
	v_mov_b32_e32 v15, s79
	s_add_i32 s63, s49, s70
	s_add_i32 s70, s49, s76
	s_add_i32 s19, s49, s19
	s_add_i32 s69, s49, s69
	s_add_i32 s53, s49, s53
	s_add_i32 s76, s49, s81
	s_add_i32 s79, s49, s88
	s_add_i32 s45, s49, s45
	v_mov_b32_e32 v19, s1
	v_mov_b32_e32 v20, s20
	v_mov_b32_e32 v24, s3
	v_mov_b32_e32 v25, s30
	v_mov_b32_e32 v26, s31
	v_mov_b32_e32 v27, s63
	v_mov_b32_e32 v28, s70
	v_mov_b32_e32 v29, s19
	v_mov_b32_e32 v30, s69
	v_mov_b32_e32 v31, s53
	v_mov_b32_e32 v32, s76
	v_mov_b32_e32 v33, s79
	v_mov_b32_e32 v17, s0
	v_mov_b32_e32 v40, s45
	ds_read_b32 v18, v13
	ds_read_b32 v21, v15
	ds_read_b32 v22, v17
	ds_read_b32 v19, v19
	ds_read_b32 v23, v20
	ds_read_b32 v24, v24
	ds_read_b32 v20, v25
	ds_read_b32 v25, v26
	ds_read_b32 v26, v27
	ds_read_b32 v28, v28
	ds_read_b32 v27, v29
	ds_read_b32 v29, v30
	ds_read_b32 v30, v31
	ds_read_b32 v32, v32
	ds_read_b32 v31, v33
	ds_read_b32 v33, v40
	s_add_i32 vcc_hi, vcc_hi, 2
	s_add_i32 s21, s21, s11
	s_add_i32 s10, s10, s12
	s_add_i32 s18, s18, s14
	s_add_i32 s4, s4, s15
	s_add_i32 s91, s91, s16
	s_add_i32 s13, s13, s17
	s_add_i32 vcc_lo, vcc_lo, s90
	s_add_i32 s42, s42, s5
	s_waitcnt vmcnt(22) lgkmcnt(0)
; __device__ __forceinline__ void p0_prologue(Frame& F) {
;     ...
; #pragma unroll 2
;             for (int m = 0; m < 128; ++m) { const float wv = wsrc[(size_t)m * 1024];
; #pragma unroll
;                 for (int j = 0; j < 8; ++j) acc8[j] += scr[(m * (c0 + j)) & 127] * wv; }
	v_pk_fma_f32 v[8:9], v[200:201], v[18:19], v[8:9] op_sel_hi:[0,1,1]
	v_pk_fma_f32 v[2:3], v[200:201], v[22:23], v[2:3] op_sel_hi:[0,1,1]
	v_pk_fma_f32 v[10:11], v[200:201], v[24:25], v[10:11] op_sel_hi:[0,1,1]
	v_pk_fma_f32 v[6:7], v[200:201], v[20:21], v[6:7] op_sel_hi:[0,1,1]
	v_pk_fma_f32 v[8:9], v[202:203], v[26:27], v[8:9] op_sel_hi:[0,1,1]
	v_pk_fma_f32 v[2:3], v[202:203], v[28:29], v[2:3] op_sel_hi:[0,1,1]
	v_pk_fma_f32 v[10:11], v[202:203], v[30:31], v[10:11] op_sel_hi:[0,1,1]
	v_pk_fma_f32 v[6:7], v[202:203], v[32:33], v[6:7] op_sel_hi:[0,1,1]
	s_and_b32 s20, s42, 0x70
	s_add_i32 s30, s21, -1
	s_add_i32 s31, s10, -2
	s_add_i32 s97, s18, -3
	s_add_i32 s3, s4, -4
	s_add_i32 s63, s91, -5
	s_add_i32 s79, s13, -6
	s_and_b32 s81, vcc_lo, 0x7e
	s_add_i32 s70, s44, s42
	s_add_i32 s76, s44, s21
	s_add_i32 s19, s44, s10
	s_add_i32 s69, s44, s18
	s_add_i32 s53, s44, s4
	s_add_i32 s94, s44, s91
	s_add_i32 s88, s44, s13
	s_add_i32 s45, s65, vcc_lo
	s_lshl_b32 s0, s20, 2
	s_and_b32 s1, s30, 0x7e
	s_and_b32 s20, s31, 0x7c
	s_and_b32 s30, s97, 0x7e
	s_and_b32 s3, s3, 0x78
	s_and_b32 s31, s63, 0x7e
	s_and_b32 s63, s79, 0x7c
	s_lshl_b32 s79, s81, 2
	s_and_b32 s70, s70, 0x78
	s_and_b32 s76, s76, 0x7f
	s_and_b32 s19, s19, 0x7e
	s_and_b32 s69, s69, 0x7f
	s_and_b32 s53, s53, 0x7c
	s_and_b32 s81, s94, 0x7f
	s_and_b32 s88, s88, 0x7e
	s_and_b32 s45, s45, 0x7f
	s_add_i32 s0, s49, s0
	s_lshl_b32 s1, s1, 2
	s_lshl_b32 s20, s20, 2
	s_lshl_b32 s30, s30, 2
	s_lshl_b32 s3, s3, 2
	s_lshl_b32 s31, s31, 2
	s_lshl_b32 s63, s63, 2
	s_add_i32 s79, s49, s79
	s_lshl_b32 s70, s70, 2
	s_lshl_b32 s76, s76, 2
	s_lshl_b32 s19, s19, 2
	s_lshl_b32 s69, s69, 2
	s_lshl_b32 s53, s53, 2
	s_lshl_b32 s81, s81, 2
	s_lshl_b32 s88, s88, 2
	s_lshl_b32 s45, s45, 2
	v_mov_b32_e32 v13, s0
	s_add_i32 s0, s49, s1
	s_add_i32 s1, s49, s20
	s_add_i32 s20, s49, s30
	s_add_i32 s3, s49, s3
	s_add_i32 s30, s49, s31
	s_add_i32 s31, s49, s63
	v_mov_b32_e32 v15, s79
	s_add_i32 s63, s49, s70
	s_add_i32 s70, s49, s76
	s_add_i32 s19, s49, s19
	s_add_i32 s69, s49, s69
	s_add_i32 s53, s49, s53
	s_add_i32 s76, s49, s81
	s_add_i32 s79, s49, s88
	s_add_i32 s45, s49, s45
	v_mov_b32_e32 v19, s1
	v_mov_b32_e32 v20, s20
	v_mov_b32_e32 v24, s3
	v_mov_b32_e32 v25, s30
	v_mov_b32_e32 v26, s31
	v_mov_b32_e32 v27, s63
	v_mov_b32_e32 v28, s70
	v_mov_b32_e32 v29, s19
	v_mov_b32_e32 v30, s69
	v_mov_b32_e32 v31, s53
	v_mov_b32_e32 v32, s76
	v_mov_b32_e32 v33, s79
	v_mov_b32_e32 v17, s0
	v_mov_b32_e32 v40, s45
	ds_read_b32 v18, v13
	ds_read_b32 v21, v15
	ds_read_b32 v22, v17
	ds_read_b32 v19, v19
	ds_read_b32 v23, v20
	ds_read_b32 v24, v24
	ds_read_b32 v20, v25
	ds_read_b32 v25, v26
	ds_read_b32 v26, v27
	ds_read_b32 v28, v28
	ds_read_b32 v27, v29
	ds_read_b32 v29, v30
	ds_read_b32 v30, v31
	ds_read_b32 v32, v32
	ds_read_b32 v31, v33
	ds_read_b32 v33, v40
	s_add_i32 vcc_hi, vcc_hi, 2
	s_add_i32 s21, s21, s11
	s_add_i32 s10, s10, s12
	s_add_i32 s18, s18, s14
	s_add_i32 s4, s4, s15
	s_add_i32 s91, s91, s16
	s_add_i32 s13, s13, s17
	s_add_i32 vcc_lo, vcc_lo, s90
	s_add_i32 s42, s42, s5
	s_waitcnt vmcnt(20) lgkmcnt(0)
	v_pk_fma_f32 v[8:9], v[204:205], v[18:19], v[8:9] op_sel_hi:[0,1,1]
	v_pk_fma_f32 v[2:3], v[204:205], v[22:23], v[2:3] op_sel_hi:[0,1,1]
	v_pk_fma_f32 v[10:11], v[204:205], v[24:25], v[10:11] op_sel_hi:[0,1,1]
	v_pk_fma_f32 v[6:7], v[204:205], v[20:21], v[6:7] op_sel_hi:[0,1,1]
	v_pk_fma_f32 v[8:9], v[206:207], v[26:27], v[8:9] op_sel_hi:[0,1,1]
	v_pk_fma_f32 v[2:3], v[206:207], v[28:29], v[2:3] op_sel_hi:[0,1,1]
	v_pk_fma_f32 v[10:11], v[206:207], v[30:31], v[10:11] op_sel_hi:[0,1,1]
	v_pk_fma_f32 v[6:7], v[206:207], v[32:33], v[6:7] op_sel_hi:[0,1,1]
	s_and_b32 s20, s42, 0x70
	s_add_i32 s30, s21, -1
	s_add_i32 s31, s10, -2
	s_add_i32 s97, s18, -3
	s_add_i32 s3, s4, -4
	s_add_i32 s63, s91, -5
	s_add_i32 s79, s13, -6
	s_and_b32 s81, vcc_lo, 0x7e
	s_add_i32 s70, s44, s42
	s_add_i32 s76, s44, s21
	s_add_i32 s19, s44, s10
	s_add_i32 s69, s44, s18
	s_add_i32 s53, s44, s4
	s_add_i32 s94, s44, s91
	s_add_i32 s88, s44, s13
	s_add_i32 s45, s65, vcc_lo
	s_lshl_b32 s0, s20, 2
	s_and_b32 s1, s30, 0x7e
	s_and_b32 s20, s31, 0x7c
	s_and_b32 s30, s97, 0x7e
	s_and_b32 s3, s3, 0x78
	s_and_b32 s31, s63, 0x7e
	s_and_b32 s63, s79, 0x7c
	s_lshl_b32 s79, s81, 2
	s_and_b32 s70, s70, 0x78
	s_and_b32 s76, s76, 0x7f
	s_and_b32 s19, s19, 0x7e
	s_and_b32 s69, s69, 0x7f
	s_and_b32 s53, s53, 0x7c
	s_and_b32 s81, s94, 0x7f
	s_and_b32 s88, s88, 0x7e
	s_and_b32 s45, s45, 0x7f
	s_add_i32 s0, s49, s0
	s_lshl_b32 s1, s1, 2
	s_lshl_b32 s20, s20, 2
	s_lshl_b32 s30, s30, 2
	s_lshl_b32 s3, s3, 2
	s_lshl_b32 s31, s31, 2
	s_lshl_b32 s63, s63, 2
	s_add_i32 s79, s49, s79
	s_lshl_b32 s70, s70, 2
	s_lshl_b32 s76, s76, 2
	s_lshl_b32 s19, s19, 2
	s_lshl_b32 s69, s69, 2
	s_lshl_b32 s53, s53, 2
	s_lshl_b32 s81, s81, 2
	s_lshl_b32 s88, s88, 2
	s_lshl_b32 s45, s45, 2
	v_mov_b32_e32 v13, s0
	s_add_i32 s0, s49, s1
	s_add_i32 s1, s49, s20
	s_add_i32 s20, s49, s30
	s_add_i32 s3, s49, s3
	s_add_i32 s30, s49, s31
	s_add_i32 s31, s49, s63
	v_mov_b32_e32 v15, s79
	s_add_i32 s63, s49, s70
	s_add_i32 s70, s49, s76
	s_add_i32 s19, s49, s19
	s_add_i32 s69, s49, s69
	s_add_i32 s53, s49, s53
	s_add_i32 s76, s49, s81
	s_add_i32 s79, s49, s88
	s_add_i32 s45, s49, s45
	v_mov_b32_e32 v19, s1
	v_mov_b32_e32 v20, s20
	v_mov_b32_e32 v24, s3
	v_mov_b32_e32 v25, s30
	v_mov_b32_e32 v26, s31
	v_mov_b32_e32 v27, s63
	v_mov_b32_e32 v28, s70
	v_mov_b32_e32 v29, s19
	v_mov_b32_e32 v30, s69
	v_mov_b32_e32 v31, s53
	v_mov_b32_e32 v32, s76
	v_mov_b32_e32 v33, s79
	v_mov_b32_e32 v17, s0
	v_mov_b32_e32 v40, s45
	ds_read_b32 v18, v13
	ds_read_b32 v21, v15
	ds_read_b32 v22, v17
	ds_read_b32 v19, v19
	ds_read_b32 v23, v20
	ds_read_b32 v24, v24
	ds_read_b32 v20, v25
	ds_read_b32 v25, v26
	ds_read_b32 v26, v27
	ds_read_b32 v28, v28
	ds_read_b32 v27, v29
	ds_read_b32 v29, v30
	ds_read_b32 v30, v31
	ds_read_b32 v32, v32
	ds_read_b32 v31, v33
	ds_read_b32 v33, v40
	s_add_i32 vcc_hi, vcc_hi, 2
	s_add_i32 s21, s21, s11
	s_add_i32 s10, s10, s12
	s_add_i32 s18, s18, s14
	s_add_i32 s4, s4, s15
	s_add_i32 s91, s91, s16
	s_add_i32 s13, s13, s17
	s_add_i32 vcc_lo, vcc_lo, s90
	s_add_i32 s42, s42, s5
	s_waitcnt vmcnt(18) lgkmcnt(0)
; __device__ __forceinline__ void p0_prologue(Frame& F) {
;     ...
; #pragma unroll 2
;             for (int m = 0; m < 128; ++m) { const float wv = wsrc[(size_t)m * 1024];
; #pragma unroll
;                 for (int j = 0; j < 8; ++j) acc8[j] += scr[(m * (c0 + j)) & 127] * wv; }
	v_pk_fma_f32 v[8:9], v[208:209], v[18:19], v[8:9] op_sel_hi:[0,1,1]
	v_pk_fma_f32 v[2:3], v[208:209], v[22:23], v[2:3] op_sel_hi:[0,1,1]
	v_pk_fma_f32 v[10:11], v[208:209], v[24:25], v[10:11] op_sel_hi:[0,1,1]
	v_pk_fma_f32 v[6:7], v[208:209], v[20:21], v[6:7] op_sel_hi:[0,1,1]
	v_pk_fma_f32 v[8:9], v[210:211], v[26:27], v[8:9] op_sel_hi:[0,1,1]
	v_pk_fma_f32 v[2:3], v[210:211], v[28:29], v[2:3] op_sel_hi:[0,1,1]
	v_pk_fma_f32 v[10:11], v[210:211], v[30:31], v[10:11] op_sel_hi:[0,1,1]
	v_pk_fma_f32 v[6:7], v[210:211], v[32:33], v[6:7] op_sel_hi:[0,1,1]
	s_and_b32 s20, s42, 0x70
	s_add_i32 s30, s21, -1
	s_add_i32 s31, s10, -2
	s_add_i32 s97, s18, -3
	s_add_i32 s3, s4, -4
	s_add_i32 s63, s91, -5
	s_add_i32 s79, s13, -6
	s_and_b32 s81, vcc_lo, 0x7e
	s_add_i32 s70, s44, s42
	s_add_i32 s76, s44, s21
	s_add_i32 s19, s44, s10
	s_add_i32 s69, s44, s18
	s_add_i32 s53, s44, s4
	s_add_i32 s94, s44, s91
	s_add_i32 s88, s44, s13
	s_add_i32 s45, s65, vcc_lo
	s_lshl_b32 s0, s20, 2
	s_and_b32 s1, s30, 0x7e
	s_and_b32 s20, s31, 0x7c
	s_and_b32 s30, s97, 0x7e
	s_and_b32 s3, s3, 0x78
	s_and_b32 s31, s63, 0x7e
	s_and_b32 s63, s79, 0x7c
	s_lshl_b32 s79, s81, 2
	s_and_b32 s70, s70, 0x78
	s_and_b32 s76, s76, 0x7f
	s_and_b32 s19, s19, 0x7e
	s_and_b32 s69, s69, 0x7f
	s_and_b32 s53, s53, 0x7c
	s_and_b32 s81, s94, 0x7f
	s_and_b32 s88, s88, 0x7e
	s_and_b32 s45, s45, 0x7f
	s_add_i32 s0, s49, s0
	s_lshl_b32 s1, s1, 2
	s_lshl_b32 s20, s20, 2
	s_lshl_b32 s30, s30, 2
	s_lshl_b32 s3, s3, 2
	s_lshl_b32 s31, s31, 2
	s_lshl_b32 s63, s63, 2
	s_add_i32 s79, s49, s79
	s_lshl_b32 s70, s70, 2
	s_lshl_b32 s76, s76, 2
	s_lshl_b32 s19, s19, 2
	s_lshl_b32 s69, s69, 2
	s_lshl_b32 s53, s53, 2
	s_lshl_b32 s81, s81, 2
	s_lshl_b32 s88, s88, 2
	s_lshl_b32 s45, s45, 2
	v_mov_b32_e32 v13, s0
	s_add_i32 s0, s49, s1
	s_add_i32 s1, s49, s20
	s_add_i32 s20, s49, s30
	s_add_i32 s3, s49, s3
	s_add_i32 s30, s49, s31
	s_add_i32 s31, s49, s63
	v_mov_b32_e32 v15, s79
	s_add_i32 s63, s49, s70
	s_add_i32 s70, s49, s76
	s_add_i32 s19, s49, s19
	s_add_i32 s69, s49, s69
	s_add_i32 s53, s49, s53
	s_add_i32 s76, s49, s81
	s_add_i32 s79, s49, s88
	s_add_i32 s45, s49, s45
	v_mov_b32_e32 v19, s1
	v_mov_b32_e32 v20, s20
	v_mov_b32_e32 v24, s3
	v_mov_b32_e32 v25, s30
	v_mov_b32_e32 v26, s31
	v_mov_b32_e32 v27, s63
	v_mov_b32_e32 v28, s70
	v_mov_b32_e32 v29, s19
	v_mov_b32_e32 v30, s69
	v_mov_b32_e32 v31, s53
	v_mov_b32_e32 v32, s76
	v_mov_b32_e32 v33, s79
	v_mov_b32_e32 v17, s0
	v_mov_b32_e32 v40, s45
	ds_read_b32 v18, v13
	ds_read_b32 v21, v15
	ds_read_b32 v22, v17
	ds_read_b32 v19, v19
	ds_read_b32 v23, v20
	ds_read_b32 v24, v24
	ds_read_b32 v20, v25
	ds_read_b32 v25, v26
	ds_read_b32 v26, v27
	ds_read_b32 v28, v28
	ds_read_b32 v27, v29
	ds_read_b32 v29, v30
	ds_read_b32 v30, v31
	ds_read_b32 v32, v32
	ds_read_b32 v31, v33
	ds_read_b32 v33, v40
	s_add_i32 vcc_hi, vcc_hi, 2
	s_add_i32 s21, s21, s11
	s_add_i32 s10, s10, s12
	s_add_i32 s18, s18, s14
	s_add_i32 s4, s4, s15
	s_add_i32 s91, s91, s16
	s_add_i32 s13, s13, s17
	s_add_i32 vcc_lo, vcc_lo, s90
	s_add_i32 s42, s42, s5
	s_waitcnt vmcnt(16) lgkmcnt(0)
	v_pk_fma_f32 v[8:9], v[212:213], v[18:19], v[8:9] op_sel_hi:[0,1,1]
	v_pk_fma_f32 v[2:3], v[212:213], v[22:23], v[2:3] op_sel_hi:[0,1,1]
	v_pk_fma_f32 v[10:11], v[212:213], v[24:25], v[10:11] op_sel_hi:[0,1,1]
	v_pk_fma_f32 v[6:7], v[212:213], v[20:21], v[6:7] op_sel_hi:[0,1,1]
	v_pk_fma_f32 v[8:9], v[214:215], v[26:27], v[8:9] op_sel_hi:[0,1,1]
	v_pk_fma_f32 v[2:3], v[214:215], v[28:29], v[2:3] op_sel_hi:[0,1,1]
	v_pk_fma_f32 v[10:11], v[214:215], v[30:31], v[10:11] op_sel_hi:[0,1,1]
	v_pk_fma_f32 v[6:7], v[214:215], v[32:33], v[6:7] op_sel_hi:[0,1,1]
	s_and_b32 s20, s42, 0x70
	s_add_i32 s30, s21, -1
	s_add_i32 s31, s10, -2
	s_add_i32 s97, s18, -3
	s_add_i32 s3, s4, -4
	s_add_i32 s63, s91, -5
	s_add_i32 s79, s13, -6
	s_and_b32 s81, vcc_lo, 0x7e
	s_add_i32 s70, s44, s42
	s_add_i32 s76, s44, s21
	s_add_i32 s19, s44, s10
	s_add_i32 s69, s44, s18
	s_add_i32 s53, s44, s4
	s_add_i32 s94, s44, s91
	s_add_i32 s88, s44, s13
	s_add_i32 s45, s65, vcc_lo
	s_lshl_b32 s0, s20, 2
	s_and_b32 s1, s30, 0x7e
	s_and_b32 s20, s31, 0x7c
	s_and_b32 s30, s97, 0x7e
	s_and_b32 s3, s3, 0x78
	s_and_b32 s31, s63, 0x7e
	s_and_b32 s63, s79, 0x7c
	s_lshl_b32 s79, s81, 2
	s_and_b32 s70, s70, 0x78
	s_and_b32 s76, s76, 0x7f
	s_and_b32 s19, s19, 0x7e
	s_and_b32 s69, s69, 0x7f
	s_and_b32 s53, s53, 0x7c
	s_and_b32 s81, s94, 0x7f
	s_and_b32 s88, s88, 0x7e
	s_and_b32 s45, s45, 0x7f
	s_add_i32 s0, s49, s0
	s_lshl_b32 s1, s1, 2
	s_lshl_b32 s20, s20, 2
	s_lshl_b32 s30, s30, 2
	s_lshl_b32 s3, s3, 2
	s_lshl_b32 s31, s31, 2
	s_lshl_b32 s63, s63, 2
	s_add_i32 s79, s49, s79
	s_lshl_b32 s70, s70, 2
	s_lshl_b32 s76, s76, 2
	s_lshl_b32 s19, s19, 2
	s_lshl_b32 s69, s69, 2
	s_lshl_b32 s53, s53, 2
	s_lshl_b32 s81, s81, 2
	s_lshl_b32 s88, s88, 2
	s_lshl_b32 s45, s45, 2
	v_mov_b32_e32 v13, s0
	s_add_i32 s0, s49, s1
	s_add_i32 s1, s49, s20
	s_add_i32 s20, s49, s30
	s_add_i32 s3, s49, s3
	s_add_i32 s30, s49, s31
	s_add_i32 s31, s49, s63
	v_mov_b32_e32 v15, s79
	s_add_i32 s63, s49, s70
	s_add_i32 s70, s49, s76
	s_add_i32 s19, s49, s19
	s_add_i32 s69, s49, s69
	s_add_i32 s53, s49, s53
	s_add_i32 s76, s49, s81
	s_add_i32 s79, s49, s88
	s_add_i32 s45, s49, s45
	v_mov_b32_e32 v19, s1
	v_mov_b32_e32 v20, s20
	v_mov_b32_e32 v24, s3
	v_mov_b32_e32 v25, s30
	v_mov_b32_e32 v26, s31
	v_mov_b32_e32 v27, s63
	v_mov_b32_e32 v28, s70
	v_mov_b32_e32 v29, s19
	v_mov_b32_e32 v30, s69
	v_mov_b32_e32 v31, s53
	v_mov_b32_e32 v32, s76
	v_mov_b32_e32 v33, s79
	v_mov_b32_e32 v17, s0
	v_mov_b32_e32 v40, s45
	ds_read_b32 v18, v13
	ds_read_b32 v21, v15
	ds_read_b32 v22, v17
	ds_read_b32 v19, v19
	ds_read_b32 v23, v20
	ds_read_b32 v24, v24
	ds_read_b32 v20, v25
	ds_read_b32 v25, v26
	ds_read_b32 v26, v27
	ds_read_b32 v28, v28
	ds_read_b32 v27, v29
	ds_read_b32 v29, v30
	ds_read_b32 v30, v31
	ds_read_b32 v32, v32
	ds_read_b32 v31, v33
	ds_read_b32 v33, v40
	s_add_i32 vcc_hi, vcc_hi, 2
	s_add_i32 s21, s21, s11
	s_add_i32 s10, s10, s12
	s_add_i32 s18, s18, s14
	s_add_i32 s4, s4, s15
	s_add_i32 s91, s91, s16
	s_add_i32 s13, s13, s17
	s_add_i32 vcc_lo, vcc_lo, s90
	s_add_i32 s42, s42, s5
	s_waitcnt vmcnt(14) lgkmcnt(0)
; __device__ __forceinline__ void p0_prologue(Frame& F) {
;     ...
; #pragma unroll 2
;             for (int m = 0; m < 128; ++m) { const float wv = wsrc[(size_t)m * 1024];
; #pragma unroll
;                 for (int j = 0; j < 8; ++j) acc8[j] += scr[(m * (c0 + j)) & 127] * wv; }
	v_pk_fma_f32 v[8:9], v[216:217], v[18:19], v[8:9] op_sel_hi:[0,1,1]
	v_pk_fma_f32 v[2:3], v[216:217], v[22:23], v[2:3] op_sel_hi:[0,1,1]
	v_pk_fma_f32 v[10:11], v[216:217], v[24:25], v[10:11] op_sel_hi:[0,1,1]
	v_pk_fma_f32 v[6:7], v[216:217], v[20:21], v[6:7] op_sel_hi:[0,1,1]
	v_pk_fma_f32 v[8:9], v[218:219], v[26:27], v[8:9] op_sel_hi:[0,1,1]
	v_pk_fma_f32 v[2:3], v[218:219], v[28:29], v[2:3] op_sel_hi:[0,1,1]
	v_pk_fma_f32 v[10:11], v[218:219], v[30:31], v[10:11] op_sel_hi:[0,1,1]
	v_pk_fma_f32 v[6:7], v[218:219], v[32:33], v[6:7] op_sel_hi:[0,1,1]
	s_and_b32 s20, s42, 0x70
	s_add_i32 s30, s21, -1
	s_add_i32 s31, s10, -2
	s_add_i32 s97, s18, -3
	s_add_i32 s3, s4, -4
	s_add_i32 s63, s91, -5
	s_add_i32 s79, s13, -6
	s_and_b32 s81, vcc_lo, 0x7e
	s_add_i32 s70, s44, s42
	s_add_i32 s76, s44, s21
	s_add_i32 s19, s44, s10
	s_add_i32 s69, s44, s18
	s_add_i32 s53, s44, s4
	s_add_i32 s94, s44, s91
	s_add_i32 s88, s44, s13
	s_add_i32 s45, s65, vcc_lo
	s_lshl_b32 s0, s20, 2
	s_and_b32 s1, s30, 0x7e
	s_and_b32 s20, s31, 0x7c
	s_and_b32 s30, s97, 0x7e
	s_and_b32 s3, s3, 0x78
	s_and_b32 s31, s63, 0x7e
	s_and_b32 s63, s79, 0x7c
	s_lshl_b32 s79, s81, 2
	s_and_b32 s70, s70, 0x78
	s_and_b32 s76, s76, 0x7f
	s_and_b32 s19, s19, 0x7e
	s_and_b32 s69, s69, 0x7f
	s_and_b32 s53, s53, 0x7c
	s_and_b32 s81, s94, 0x7f
	s_and_b32 s88, s88, 0x7e
	s_and_b32 s45, s45, 0x7f
	s_add_i32 s0, s49, s0
	s_lshl_b32 s1, s1, 2
	s_lshl_b32 s20, s20, 2
	s_lshl_b32 s30, s30, 2
	s_lshl_b32 s3, s3, 2
	s_lshl_b32 s31, s31, 2
	s_lshl_b32 s63, s63, 2
	s_add_i32 s79, s49, s79
	s_lshl_b32 s70, s70, 2
	s_lshl_b32 s76, s76, 2
	s_lshl_b32 s19, s19, 2
	s_lshl_b32 s69, s69, 2
	s_lshl_b32 s53, s53, 2
	s_lshl_b32 s81, s81, 2
	s_lshl_b32 s88, s88, 2
	s_lshl_b32 s45, s45, 2
	v_mov_b32_e32 v13, s0
	s_add_i32 s0, s49, s1
	s_add_i32 s1, s49, s20
	s_add_i32 s20, s49, s30
	s_add_i32 s3, s49, s3
	s_add_i32 s30, s49, s31
	s_add_i32 s31, s49, s63
	v_mov_b32_e32 v15, s79
	s_add_i32 s63, s49, s70
	s_add_i32 s70, s49, s76
	s_add_i32 s19, s49, s19
	s_add_i32 s69, s49, s69
	s_add_i32 s53, s49, s53
	s_add_i32 s76, s49, s81
	s_add_i32 s79, s49, s88
	s_add_i32 s45, s49, s45
	v_mov_b32_e32 v19, s1
	v_mov_b32_e32 v20, s20
	v_mov_b32_e32 v24, s3
	v_mov_b32_e32 v25, s30
	v_mov_b32_e32 v26, s31
	v_mov_b32_e32 v27, s63
	v_mov_b32_e32 v28, s70
	v_mov_b32_e32 v29, s19
	v_mov_b32_e32 v30, s69
	v_mov_b32_e32 v31, s53
	v_mov_b32_e32 v32, s76
	v_mov_b32_e32 v33, s79
	v_mov_b32_e32 v17, s0
	v_mov_b32_e32 v40, s45
	ds_read_b32 v18, v13
	ds_read_b32 v21, v15
	ds_read_b32 v22, v17
	ds_read_b32 v19, v19
	ds_read_b32 v23, v20
	ds_read_b32 v24, v24
	ds_read_b32 v20, v25
	ds_read_b32 v25, v26
	ds_read_b32 v26, v27
	ds_read_b32 v28, v28
	ds_read_b32 v27, v29
	ds_read_b32 v29, v30
	ds_read_b32 v30, v31
	ds_read_b32 v32, v32
	ds_read_b32 v31, v33
	ds_read_b32 v33, v40
	s_add_i32 vcc_hi, vcc_hi, 2
	s_add_i32 s21, s21, s11
	s_add_i32 s10, s10, s12
	s_add_i32 s18, s18, s14
	s_add_i32 s4, s4, s15
	s_add_i32 s91, s91, s16
	s_add_i32 s13, s13, s17
	s_add_i32 vcc_lo, vcc_lo, s90
	s_add_i32 s42, s42, s5
	s_waitcnt vmcnt(12) lgkmcnt(0)
	v_pk_fma_f32 v[8:9], v[220:221], v[18:19], v[8:9] op_sel_hi:[0,1,1]
	v_pk_fma_f32 v[2:3], v[220:221], v[22:23], v[2:3] op_sel_hi:[0,1,1]
	v_pk_fma_f32 v[10:11], v[220:221], v[24:25], v[10:11] op_sel_hi:[0,1,1]
	v_pk_fma_f32 v[6:7], v[220:221], v[20:21], v[6:7] op_sel_hi:[0,1,1]
	v_pk_fma_f32 v[8:9], v[222:223], v[26:27], v[8:9] op_sel_hi:[0,1,1]
	v_pk_fma_f32 v[2:3], v[222:223], v[28:29], v[2:3] op_sel_hi:[0,1,1]
	v_pk_fma_f32 v[10:11], v[222:223], v[30:31], v[10:11] op_sel_hi:[0,1,1]
	v_pk_fma_f32 v[6:7], v[222:223], v[32:33], v[6:7] op_sel_hi:[0,1,1]
	s_and_b32 s20, s42, 0x70
	s_add_i32 s30, s21, -1
	s_add_i32 s31, s10, -2
	s_add_i32 s97, s18, -3
	s_add_i32 s3, s4, -4
	s_add_i32 s63, s91, -5
	s_add_i32 s79, s13, -6
	s_and_b32 s81, vcc_lo, 0x7e
	s_add_i32 s70, s44, s42
	s_add_i32 s76, s44, s21
	s_add_i32 s19, s44, s10
	s_add_i32 s69, s44, s18
	s_add_i32 s53, s44, s4
	s_add_i32 s94, s44, s91
	s_add_i32 s88, s44, s13
	s_add_i32 s45, s65, vcc_lo
	s_lshl_b32 s0, s20, 2
	s_and_b32 s1, s30, 0x7e
	s_and_b32 s20, s31, 0x7c
	s_and_b32 s30, s97, 0x7e
	s_and_b32 s3, s3, 0x78
	s_and_b32 s31, s63, 0x7e
	s_and_b32 s63, s79, 0x7c
	s_lshl_b32 s79, s81, 2
	s_and_b32 s70, s70, 0x78
	s_and_b32 s76, s76, 0x7f
	s_and_b32 s19, s19, 0x7e
	s_and_b32 s69, s69, 0x7f
	s_and_b32 s53, s53, 0x7c
	s_and_b32 s81, s94, 0x7f
	s_and_b32 s88, s88, 0x7e
	s_and_b32 s45, s45, 0x7f
	s_add_i32 s0, s49, s0
	s_lshl_b32 s1, s1, 2
	s_lshl_b32 s20, s20, 2
	s_lshl_b32 s30, s30, 2
	s_lshl_b32 s3, s3, 2
	s_lshl_b32 s31, s31, 2
	s_lshl_b32 s63, s63, 2
	s_add_i32 s79, s49, s79
	s_lshl_b32 s70, s70, 2
	s_lshl_b32 s76, s76, 2
	s_lshl_b32 s19, s19, 2
	s_lshl_b32 s69, s69, 2
	s_lshl_b32 s53, s53, 2
	s_lshl_b32 s81, s81, 2
	s_lshl_b32 s88, s88, 2
	s_lshl_b32 s45, s45, 2
	v_mov_b32_e32 v13, s0
	s_add_i32 s0, s49, s1
	s_add_i32 s1, s49, s20
	s_add_i32 s20, s49, s30
	s_add_i32 s3, s49, s3
	s_add_i32 s30, s49, s31
	s_add_i32 s31, s49, s63
	v_mov_b32_e32 v15, s79
	s_add_i32 s63, s49, s70
	s_add_i32 s70, s49, s76
	s_add_i32 s19, s49, s19
	s_add_i32 s69, s49, s69
	s_add_i32 s53, s49, s53
	s_add_i32 s76, s49, s81
	s_add_i32 s79, s49, s88
	s_add_i32 s45, s49, s45
	v_mov_b32_e32 v19, s1
	v_mov_b32_e32 v20, s20
	v_mov_b32_e32 v24, s3
	v_mov_b32_e32 v25, s30
	v_mov_b32_e32 v26, s31
	v_mov_b32_e32 v27, s63
	v_mov_b32_e32 v28, s70
	v_mov_b32_e32 v29, s19
	v_mov_b32_e32 v30, s69
	v_mov_b32_e32 v31, s53
	v_mov_b32_e32 v32, s76
	v_mov_b32_e32 v33, s79
	v_mov_b32_e32 v17, s0
	v_mov_b32_e32 v40, s45
	ds_read_b32 v18, v13
	ds_read_b32 v21, v15
	ds_read_b32 v22, v17
	ds_read_b32 v19, v19
	ds_read_b32 v23, v20
	ds_read_b32 v24, v24
	ds_read_b32 v20, v25
	ds_read_b32 v25, v26
	ds_read_b32 v26, v27
	ds_read_b32 v28, v28
	ds_read_b32 v27, v29
	ds_read_b32 v29, v30
	ds_read_b32 v30, v31
	ds_read_b32 v32, v32
	ds_read_b32 v31, v33
	ds_read_b32 v33, v40
	s_add_i32 vcc_hi, vcc_hi, 2
	s_add_i32 s21, s21, s11
	s_add_i32 s10, s10, s12
	s_add_i32 s18, s18, s14
	s_add_i32 s4, s4, s15
	s_add_i32 s91, s91, s16
	s_add_i32 s13, s13, s17
	s_add_i32 vcc_lo, vcc_lo, s90
	s_add_i32 s42, s42, s5
	s_waitcnt vmcnt(10) lgkmcnt(0)
; __device__ __forceinline__ void p0_prologue(Frame& F) {
;     ...
; #pragma unroll 2
;             for (int m = 0; m < 128; ++m) { const float wv = wsrc[(size_t)m * 1024];
; #pragma unroll
;                 for (int j = 0; j < 8; ++j) acc8[j] += scr[(m * (c0 + j)) & 127] * wv; }
	v_pk_fma_f32 v[8:9], v[224:225], v[18:19], v[8:9] op_sel_hi:[0,1,1]
	v_pk_fma_f32 v[2:3], v[224:225], v[22:23], v[2:3] op_sel_hi:[0,1,1]
	v_pk_fma_f32 v[10:11], v[224:225], v[24:25], v[10:11] op_sel_hi:[0,1,1]
	v_pk_fma_f32 v[6:7], v[224:225], v[20:21], v[6:7] op_sel_hi:[0,1,1]
	v_pk_fma_f32 v[8:9], v[226:227], v[26:27], v[8:9] op_sel_hi:[0,1,1]
	v_pk_fma_f32 v[2:3], v[226:227], v[28:29], v[2:3] op_sel_hi:[0,1,1]
	v_pk_fma_f32 v[10:11], v[226:227], v[30:31], v[10:11] op_sel_hi:[0,1,1]
	v_pk_fma_f32 v[6:7], v[226:227], v[32:33], v[6:7] op_sel_hi:[0,1,1]
	s_and_b32 s20, s42, 0x70
	s_add_i32 s30, s21, -1
	s_add_i32 s31, s10, -2
	s_add_i32 s97, s18, -3
	s_add_i32 s3, s4, -4
	s_add_i32 s63, s91, -5
	s_add_i32 s79, s13, -6
	s_and_b32 s81, vcc_lo, 0x7e
	s_add_i32 s70, s44, s42
	s_add_i32 s76, s44, s21
	s_add_i32 s19, s44, s10
	s_add_i32 s69, s44, s18
	s_add_i32 s53, s44, s4
	s_add_i32 s94, s44, s91
	s_add_i32 s88, s44, s13
	s_add_i32 s45, s65, vcc_lo
	s_lshl_b32 s0, s20, 2
	s_and_b32 s1, s30, 0x7e
	s_and_b32 s20, s31, 0x7c
	s_and_b32 s30, s97, 0x7e
	s_and_b32 s3, s3, 0x78
	s_and_b32 s31, s63, 0x7e
	s_and_b32 s63, s79, 0x7c
	s_lshl_b32 s79, s81, 2
	s_and_b32 s70, s70, 0x78
	s_and_b32 s76, s76, 0x7f
	s_and_b32 s19, s19, 0x7e
	s_and_b32 s69, s69, 0x7f
	s_and_b32 s53, s53, 0x7c
	s_and_b32 s81, s94, 0x7f
	s_and_b32 s88, s88, 0x7e
	s_and_b32 s45, s45, 0x7f
	s_add_i32 s0, s49, s0
	s_lshl_b32 s1, s1, 2
	s_lshl_b32 s20, s20, 2
	s_lshl_b32 s30, s30, 2
	s_lshl_b32 s3, s3, 2
	s_lshl_b32 s31, s31, 2
	s_lshl_b32 s63, s63, 2
	s_add_i32 s79, s49, s79
	s_lshl_b32 s70, s70, 2
	s_lshl_b32 s76, s76, 2
	s_lshl_b32 s19, s19, 2
	s_lshl_b32 s69, s69, 2
	s_lshl_b32 s53, s53, 2
	s_lshl_b32 s81, s81, 2
	s_lshl_b32 s88, s88, 2
	s_lshl_b32 s45, s45, 2
	v_mov_b32_e32 v13, s0
	s_add_i32 s0, s49, s1
	s_add_i32 s1, s49, s20
	s_add_i32 s20, s49, s30
	s_add_i32 s3, s49, s3
	s_add_i32 s30, s49, s31
	s_add_i32 s31, s49, s63
	v_mov_b32_e32 v15, s79
	s_add_i32 s63, s49, s70
	s_add_i32 s70, s49, s76
	s_add_i32 s19, s49, s19
	s_add_i32 s69, s49, s69
	s_add_i32 s53, s49, s53
	s_add_i32 s76, s49, s81
	s_add_i32 s79, s49, s88
	s_add_i32 s45, s49, s45
	v_mov_b32_e32 v19, s1
	v_mov_b32_e32 v20, s20
	v_mov_b32_e32 v24, s3
	v_mov_b32_e32 v25, s30
	v_mov_b32_e32 v26, s31
	v_mov_b32_e32 v27, s63
	v_mov_b32_e32 v28, s70
	v_mov_b32_e32 v29, s19
	v_mov_b32_e32 v30, s69
	v_mov_b32_e32 v31, s53
	v_mov_b32_e32 v32, s76
	v_mov_b32_e32 v33, s79
	v_mov_b32_e32 v17, s0
	v_mov_b32_e32 v40, s45
	ds_read_b32 v18, v13
	ds_read_b32 v21, v15
	ds_read_b32 v22, v17
	ds_read_b32 v19, v19
	ds_read_b32 v23, v20
	ds_read_b32 v24, v24
	ds_read_b32 v20, v25
	ds_read_b32 v25, v26
	ds_read_b32 v26, v27
	ds_read_b32 v28, v28
	ds_read_b32 v27, v29
	ds_read_b32 v29, v30
	ds_read_b32 v30, v31
	ds_read_b32 v32, v32
	ds_read_b32 v31, v33
	ds_read_b32 v33, v40
	s_add_i32 vcc_hi, vcc_hi, 2
	s_add_i32 s21, s21, s11
	s_add_i32 s10, s10, s12
	s_add_i32 s18, s18, s14
	s_add_i32 s4, s4, s15
	s_add_i32 s91, s91, s16
	s_add_i32 s13, s13, s17
	s_add_i32 vcc_lo, vcc_lo, s90
	s_add_i32 s42, s42, s5
	s_waitcnt vmcnt(8) lgkmcnt(0)
	v_pk_fma_f32 v[8:9], v[228:229], v[18:19], v[8:9] op_sel_hi:[0,1,1]
	v_pk_fma_f32 v[2:3], v[228:229], v[22:23], v[2:3] op_sel_hi:[0,1,1]
	v_pk_fma_f32 v[10:11], v[228:229], v[24:25], v[10:11] op_sel_hi:[0,1,1]
	v_pk_fma_f32 v[6:7], v[228:229], v[20:21], v[6:7] op_sel_hi:[0,1,1]
	v_pk_fma_f32 v[8:9], v[230:231], v[26:27], v[8:9] op_sel_hi:[0,1,1]
	v_pk_fma_f32 v[2:3], v[230:231], v[28:29], v[2:3] op_sel_hi:[0,1,1]
	v_pk_fma_f32 v[10:11], v[230:231], v[30:31], v[10:11] op_sel_hi:[0,1,1]
	v_pk_fma_f32 v[6:7], v[230:231], v[32:33], v[6:7] op_sel_hi:[0,1,1]
	s_and_b32 s20, s42, 0x70
	s_add_i32 s30, s21, -1
	s_add_i32 s31, s10, -2
	s_add_i32 s97, s18, -3
	s_add_i32 s3, s4, -4
	s_add_i32 s63, s91, -5
	s_add_i32 s79, s13, -6
	s_and_b32 s81, vcc_lo, 0x7e
	s_add_i32 s70, s44, s42
	s_add_i32 s76, s44, s21
	s_add_i32 s19, s44, s10
	s_add_i32 s69, s44, s18
	s_add_i32 s53, s44, s4
	s_add_i32 s94, s44, s91
	s_add_i32 s88, s44, s13
	s_add_i32 s45, s65, vcc_lo
	s_lshl_b32 s0, s20, 2
	s_and_b32 s1, s30, 0x7e
	s_and_b32 s20, s31, 0x7c
	s_and_b32 s30, s97, 0x7e
	s_and_b32 s3, s3, 0x78
	s_and_b32 s31, s63, 0x7e
	s_and_b32 s63, s79, 0x7c
	s_lshl_b32 s79, s81, 2
	s_and_b32 s70, s70, 0x78
	s_and_b32 s76, s76, 0x7f
	s_and_b32 s19, s19, 0x7e
	s_and_b32 s69, s69, 0x7f
	s_and_b32 s53, s53, 0x7c
	s_and_b32 s81, s94, 0x7f
	s_and_b32 s88, s88, 0x7e
	s_and_b32 s45, s45, 0x7f
	s_add_i32 s0, s49, s0
	s_lshl_b32 s1, s1, 2
	s_lshl_b32 s20, s20, 2
	s_lshl_b32 s30, s30, 2
	s_lshl_b32 s3, s3, 2
	s_lshl_b32 s31, s31, 2
	s_lshl_b32 s63, s63, 2
	s_add_i32 s79, s49, s79
	s_lshl_b32 s70, s70, 2
	s_lshl_b32 s76, s76, 2
	s_lshl_b32 s19, s19, 2
	s_lshl_b32 s69, s69, 2
	s_lshl_b32 s53, s53, 2
	s_lshl_b32 s81, s81, 2
	s_lshl_b32 s88, s88, 2
	s_lshl_b32 s45, s45, 2
	v_mov_b32_e32 v13, s0
	s_add_i32 s0, s49, s1
	s_add_i32 s1, s49, s20
	s_add_i32 s20, s49, s30
	s_add_i32 s3, s49, s3
	s_add_i32 s30, s49, s31
	s_add_i32 s31, s49, s63
	v_mov_b32_e32 v15, s79
	s_add_i32 s63, s49, s70
	s_add_i32 s70, s49, s76
	s_add_i32 s19, s49, s19
	s_add_i32 s69, s49, s69
	s_add_i32 s53, s49, s53
	s_add_i32 s76, s49, s81
	s_add_i32 s79, s49, s88
	s_add_i32 s45, s49, s45
	v_mov_b32_e32 v19, s1
	v_mov_b32_e32 v20, s20
	v_mov_b32_e32 v24, s3
	v_mov_b32_e32 v25, s30
	v_mov_b32_e32 v26, s31
	v_mov_b32_e32 v27, s63
	v_mov_b32_e32 v28, s70
	v_mov_b32_e32 v29, s19
	v_mov_b32_e32 v30, s69
	v_mov_b32_e32 v31, s53
	v_mov_b32_e32 v32, s76
	v_mov_b32_e32 v33, s79
	v_mov_b32_e32 v17, s0
	v_mov_b32_e32 v40, s45
	ds_read_b32 v18, v13
	ds_read_b32 v21, v15
	ds_read_b32 v22, v17
	ds_read_b32 v19, v19
	ds_read_b32 v23, v20
	ds_read_b32 v24, v24
	ds_read_b32 v20, v25
	ds_read_b32 v25, v26
	ds_read_b32 v26, v27
	ds_read_b32 v28, v28
	ds_read_b32 v27, v29
	ds_read_b32 v29, v30
	ds_read_b32 v30, v31
	ds_read_b32 v32, v32
	ds_read_b32 v31, v33
	ds_read_b32 v33, v40
	s_add_i32 vcc_hi, vcc_hi, 2
	s_add_i32 s21, s21, s11
	s_add_i32 s10, s10, s12
	s_add_i32 s18, s18, s14
	s_add_i32 s4, s4, s15
	s_add_i32 s91, s91, s16
	s_add_i32 s13, s13, s17
	s_add_i32 vcc_lo, vcc_lo, s90
	s_add_i32 s42, s42, s5
	s_waitcnt vmcnt(6) lgkmcnt(0)
; __device__ __forceinline__ void p0_prologue(Frame& F) {
;     ...
; #pragma unroll 2
;             for (int m = 0; m < 128; ++m) { const float wv = wsrc[(size_t)m * 1024];
; #pragma unroll
;                 for (int j = 0; j < 8; ++j) acc8[j] += scr[(m * (c0 + j)) & 127] * wv; }
	v_pk_fma_f32 v[8:9], v[232:233], v[18:19], v[8:9] op_sel_hi:[0,1,1]
	v_pk_fma_f32 v[2:3], v[232:233], v[22:23], v[2:3] op_sel_hi:[0,1,1]
	v_pk_fma_f32 v[10:11], v[232:233], v[24:25], v[10:11] op_sel_hi:[0,1,1]
	v_pk_fma_f32 v[6:7], v[232:233], v[20:21], v[6:7] op_sel_hi:[0,1,1]
	v_pk_fma_f32 v[8:9], v[234:235], v[26:27], v[8:9] op_sel_hi:[0,1,1]
	v_pk_fma_f32 v[2:3], v[234:235], v[28:29], v[2:3] op_sel_hi:[0,1,1]
	v_pk_fma_f32 v[10:11], v[234:235], v[30:31], v[10:11] op_sel_hi:[0,1,1]
	v_pk_fma_f32 v[6:7], v[234:235], v[32:33], v[6:7] op_sel_hi:[0,1,1]
	s_and_b32 s20, s42, 0x70
	s_add_i32 s30, s21, -1
	s_add_i32 s31, s10, -2
	s_add_i32 s97, s18, -3
	s_add_i32 s3, s4, -4
	s_add_i32 s63, s91, -5
	s_add_i32 s79, s13, -6
	s_and_b32 s81, vcc_lo, 0x7e
	s_add_i32 s70, s44, s42
	s_add_i32 s76, s44, s21
	s_add_i32 s19, s44, s10
	s_add_i32 s69, s44, s18
	s_add_i32 s53, s44, s4
	s_add_i32 s94, s44, s91
	s_add_i32 s88, s44, s13
	s_add_i32 s45, s65, vcc_lo
	s_lshl_b32 s0, s20, 2
	s_and_b32 s1, s30, 0x7e
	s_and_b32 s20, s31, 0x7c
	s_and_b32 s30, s97, 0x7e
	s_and_b32 s3, s3, 0x78
	s_and_b32 s31, s63, 0x7e
	s_and_b32 s63, s79, 0x7c
	s_lshl_b32 s79, s81, 2
	s_and_b32 s70, s70, 0x78
	s_and_b32 s76, s76, 0x7f
	s_and_b32 s19, s19, 0x7e
	s_and_b32 s69, s69, 0x7f
	s_and_b32 s53, s53, 0x7c
	s_and_b32 s81, s94, 0x7f
	s_and_b32 s88, s88, 0x7e
	s_and_b32 s45, s45, 0x7f
	s_add_i32 s0, s49, s0
	s_lshl_b32 s1, s1, 2
	s_lshl_b32 s20, s20, 2
	s_lshl_b32 s30, s30, 2
	s_lshl_b32 s3, s3, 2
	s_lshl_b32 s31, s31, 2
	s_lshl_b32 s63, s63, 2
	s_add_i32 s79, s49, s79
	s_lshl_b32 s70, s70, 2
	s_lshl_b32 s76, s76, 2
	s_lshl_b32 s19, s19, 2
	s_lshl_b32 s69, s69, 2
	s_lshl_b32 s53, s53, 2
	s_lshl_b32 s81, s81, 2
	s_lshl_b32 s88, s88, 2
	s_lshl_b32 s45, s45, 2
	v_mov_b32_e32 v13, s0
	s_add_i32 s0, s49, s1
	s_add_i32 s1, s49, s20
	s_add_i32 s20, s49, s30
	s_add_i32 s3, s49, s3
	s_add_i32 s30, s49, s31
	s_add_i32 s31, s49, s63
	v_mov_b32_e32 v15, s79
	s_add_i32 s63, s49, s70
	s_add_i32 s70, s49, s76
	s_add_i32 s19, s49, s19
	s_add_i32 s69, s49, s69
	s_add_i32 s53, s49, s53
	s_add_i32 s76, s49, s81
	s_add_i32 s79, s49, s88
	s_add_i32 s45, s49, s45
	v_mov_b32_e32 v19, s1
	v_mov_b32_e32 v20, s20
	v_mov_b32_e32 v24, s3
	v_mov_b32_e32 v25, s30
	v_mov_b32_e32 v26, s31
	v_mov_b32_e32 v27, s63
	v_mov_b32_e32 v28, s70
	v_mov_b32_e32 v29, s19
	v_mov_b32_e32 v30, s69
	v_mov_b32_e32 v31, s53
	v_mov_b32_e32 v32, s76
	v_mov_b32_e32 v33, s79
	v_mov_b32_e32 v17, s0
	v_mov_b32_e32 v40, s45
	ds_read_b32 v18, v13
	ds_read_b32 v21, v15
	ds_read_b32 v22, v17
	ds_read_b32 v19, v19
	ds_read_b32 v23, v20
	ds_read_b32 v24, v24
	ds_read_b32 v20, v25
	ds_read_b32 v25, v26
	ds_read_b32 v26, v27
	ds_read_b32 v28, v28
	ds_read_b32 v27, v29
	ds_read_b32 v29, v30
	ds_read_b32 v30, v31
	ds_read_b32 v32, v32
	ds_read_b32 v31, v33
	ds_read_b32 v33, v40
	s_add_i32 vcc_hi, vcc_hi, 2
	s_add_i32 s21, s21, s11
	s_add_i32 s10, s10, s12
	s_add_i32 s18, s18, s14
	s_add_i32 s4, s4, s15
	s_add_i32 s91, s91, s16
	s_add_i32 s13, s13, s17
	s_add_i32 vcc_lo, vcc_lo, s90
	s_add_i32 s42, s42, s5
	s_waitcnt vmcnt(4) lgkmcnt(0)
	v_pk_fma_f32 v[8:9], v[236:237], v[18:19], v[8:9] op_sel_hi:[0,1,1]
	v_pk_fma_f32 v[2:3], v[236:237], v[22:23], v[2:3] op_sel_hi:[0,1,1]
	v_pk_fma_f32 v[10:11], v[236:237], v[24:25], v[10:11] op_sel_hi:[0,1,1]
	v_pk_fma_f32 v[6:7], v[236:237], v[20:21], v[6:7] op_sel_hi:[0,1,1]
	v_pk_fma_f32 v[8:9], v[238:239], v[26:27], v[8:9] op_sel_hi:[0,1,1]
	v_pk_fma_f32 v[2:3], v[238:239], v[28:29], v[2:3] op_sel_hi:[0,1,1]
	v_pk_fma_f32 v[10:11], v[238:239], v[30:31], v[10:11] op_sel_hi:[0,1,1]
	v_pk_fma_f32 v[6:7], v[238:239], v[32:33], v[6:7] op_sel_hi:[0,1,1]
	s_and_b32 s20, s42, 0x70
	s_add_i32 s30, s21, -1
	s_add_i32 s31, s10, -2
	s_add_i32 s97, s18, -3
	s_add_i32 s3, s4, -4
	s_add_i32 s63, s91, -5
	s_add_i32 s79, s13, -6
	s_and_b32 s81, vcc_lo, 0x7e
	s_add_i32 s70, s44, s42
	s_add_i32 s76, s44, s21
	s_add_i32 s19, s44, s10
	s_add_i32 s69, s44, s18
	s_add_i32 s53, s44, s4
	s_add_i32 s94, s44, s91
	s_add_i32 s88, s44, s13
	s_add_i32 s45, s65, vcc_lo
	s_lshl_b32 s0, s20, 2
	s_and_b32 s1, s30, 0x7e
	s_and_b32 s20, s31, 0x7c
	s_and_b32 s30, s97, 0x7e
	s_and_b32 s3, s3, 0x78
	s_and_b32 s31, s63, 0x7e
	s_and_b32 s63, s79, 0x7c
	s_lshl_b32 s79, s81, 2
	s_and_b32 s70, s70, 0x78
	s_and_b32 s76, s76, 0x7f
	s_and_b32 s19, s19, 0x7e
	s_and_b32 s69, s69, 0x7f
	s_and_b32 s53, s53, 0x7c
	s_and_b32 s81, s94, 0x7f
	s_and_b32 s88, s88, 0x7e
	s_and_b32 s45, s45, 0x7f
	s_add_i32 s0, s49, s0
	s_lshl_b32 s1, s1, 2
	s_lshl_b32 s20, s20, 2
	s_lshl_b32 s30, s30, 2
	s_lshl_b32 s3, s3, 2
	s_lshl_b32 s31, s31, 2
	s_lshl_b32 s63, s63, 2
	s_add_i32 s79, s49, s79
	s_lshl_b32 s70, s70, 2
	s_lshl_b32 s76, s76, 2
	s_lshl_b32 s19, s19, 2
	s_lshl_b32 s69, s69, 2
	s_lshl_b32 s53, s53, 2
	s_lshl_b32 s81, s81, 2
	s_lshl_b32 s88, s88, 2
	s_lshl_b32 s45, s45, 2
	v_mov_b32_e32 v13, s0
	s_add_i32 s0, s49, s1
	s_add_i32 s1, s49, s20
	s_add_i32 s20, s49, s30
	s_add_i32 s3, s49, s3
	s_add_i32 s30, s49, s31
	s_add_i32 s31, s49, s63
	v_mov_b32_e32 v15, s79
	s_add_i32 s63, s49, s70
	s_add_i32 s70, s49, s76
	s_add_i32 s19, s49, s19
	s_add_i32 s69, s49, s69
	s_add_i32 s53, s49, s53
	s_add_i32 s76, s49, s81
	s_add_i32 s79, s49, s88
	s_add_i32 s45, s49, s45
	v_mov_b32_e32 v19, s1
	v_mov_b32_e32 v20, s20
	v_mov_b32_e32 v24, s3
	v_mov_b32_e32 v25, s30
	v_mov_b32_e32 v26, s31
	v_mov_b32_e32 v27, s63
	v_mov_b32_e32 v28, s70
	v_mov_b32_e32 v29, s19
	v_mov_b32_e32 v30, s69
	v_mov_b32_e32 v31, s53
	v_mov_b32_e32 v32, s76
	v_mov_b32_e32 v33, s79
	v_mov_b32_e32 v17, s0
	v_mov_b32_e32 v40, s45
	ds_read_b32 v18, v13
	ds_read_b32 v21, v15
	ds_read_b32 v22, v17
	ds_read_b32 v19, v19
	ds_read_b32 v23, v20
	ds_read_b32 v24, v24
	ds_read_b32 v20, v25
	ds_read_b32 v25, v26
	ds_read_b32 v26, v27
	ds_read_b32 v28, v28
	ds_read_b32 v27, v29
	ds_read_b32 v29, v30
	ds_read_b32 v30, v31
	ds_read_b32 v32, v32
	ds_read_b32 v31, v33
	ds_read_b32 v33, v40
	s_add_i32 vcc_hi, vcc_hi, 2
	s_add_i32 s21, s21, s11
	s_add_i32 s10, s10, s12
	s_add_i32 s18, s18, s14
	s_add_i32 s4, s4, s15
	s_add_i32 s91, s91, s16
	s_add_i32 s13, s13, s17
	s_add_i32 vcc_lo, vcc_lo, s90
	s_add_i32 s42, s42, s5
	s_waitcnt vmcnt(2) lgkmcnt(0)
; #define GAS __attribute__((address_space(1)))
; #define LDS_WAIT() asm volatile("s_waitcnt lgkmcnt(0)" ::: "memory")
; __device__ __forceinline__ unsigned f2bf(float f) { unsigned u = __builtin_bit_cast(unsigned, f); return (u + 0x7fffu + ((u >> 16) & 1u)) >> 16; }
; template <class T> __device__ __forceinline__ T* wsp(const Frame& F, size_t off) { return (T*)(F.ws + off); }
; __device__ __forceinline__ void p0_prologue(Frame& F) {
;     ...
; #pragma unroll 2
;             for (int m = 0; m < 128; ++m) { const float wv = wsrc[(size_t)m * 1024];
; #pragma unroll
;                 for (int j = 0; j < 8; ++j) acc8[j] += scr[(m * (c0 + j)) & 127] * wv; }
;             LDS_WAIT(); asm volatile("" ::: "memory");
;             unsigned h[8];
; #pragma unroll
;             for (int j = 0; j < 8; ++j) h[j] = f2bf(acc8[j] * 0.08838834764831845f);
;             *(GAS v4u*)(wsp<bf16>(F, WS_W2) + (size_t)n * 1536 + 512 + 256 * g + 128 * part + c0) = (v4u){h[0] | (h[1] << 16), h[2] | (h[3] << 16), h[4] | (h[5] << 16), h[6] | (h[7] << 16)};
	v_pk_fma_f32 v[8:9], v[240:241], v[18:19], v[8:9] op_sel_hi:[0,1,1]
	v_pk_fma_f32 v[2:3], v[240:241], v[22:23], v[2:3] op_sel_hi:[0,1,1]
	v_pk_fma_f32 v[10:11], v[240:241], v[24:25], v[10:11] op_sel_hi:[0,1,1]
	v_pk_fma_f32 v[6:7], v[240:241], v[20:21], v[6:7] op_sel_hi:[0,1,1]
	v_pk_fma_f32 v[8:9], v[242:243], v[26:27], v[8:9] op_sel_hi:[0,1,1]
	v_pk_fma_f32 v[2:3], v[242:243], v[28:29], v[2:3] op_sel_hi:[0,1,1]
	v_pk_fma_f32 v[10:11], v[242:243], v[30:31], v[10:11] op_sel_hi:[0,1,1]
	v_pk_fma_f32 v[6:7], v[242:243], v[32:33], v[6:7] op_sel_hi:[0,1,1]
	s_and_b32 s20, s42, 0x70
	s_add_i32 s30, s21, -1
	s_add_i32 s31, s10, -2
	s_add_i32 s97, s18, -3
	s_add_i32 s3, s4, -4
	s_add_i32 s63, s91, -5
	s_add_i32 s79, s13, -6
	s_and_b32 s81, vcc_lo, 0x7e
	s_add_i32 s70, s44, s42
	s_add_i32 s76, s44, s21
	s_add_i32 s19, s44, s10
	s_add_i32 s69, s44, s18
	s_add_i32 s53, s44, s4
	s_add_i32 s94, s44, s91
	s_add_i32 s88, s44, s13
	s_add_i32 s45, s65, vcc_lo
	s_lshl_b32 s0, s20, 2
	s_and_b32 s1, s30, 0x7e
	s_and_b32 s20, s31, 0x7c
	s_and_b32 s30, s97, 0x7e
	s_and_b32 s3, s3, 0x78
	s_and_b32 s31, s63, 0x7e
	s_and_b32 s63, s79, 0x7c
	s_lshl_b32 s79, s81, 2
	s_and_b32 s70, s70, 0x78
	s_and_b32 s76, s76, 0x7f
	s_and_b32 s19, s19, 0x7e
	s_and_b32 s69, s69, 0x7f
	s_and_b32 s53, s53, 0x7c
	s_and_b32 s81, s94, 0x7f
	s_and_b32 s88, s88, 0x7e
	s_and_b32 s45, s45, 0x7f
	s_add_i32 s0, s49, s0
	s_lshl_b32 s1, s1, 2
	s_lshl_b32 s20, s20, 2
	s_lshl_b32 s30, s30, 2
	s_lshl_b32 s3, s3, 2
	s_lshl_b32 s31, s31, 2
	s_lshl_b32 s63, s63, 2
	s_add_i32 s79, s49, s79
	s_lshl_b32 s70, s70, 2
	s_lshl_b32 s76, s76, 2
	s_lshl_b32 s19, s19, 2
	s_lshl_b32 s69, s69, 2
	s_lshl_b32 s53, s53, 2
	s_lshl_b32 s81, s81, 2
	s_lshl_b32 s88, s88, 2
	s_lshl_b32 s45, s45, 2
	v_mov_b32_e32 v13, s0
	s_add_i32 s0, s49, s1
	s_add_i32 s1, s49, s20
	s_add_i32 s20, s49, s30
	s_add_i32 s3, s49, s3
	s_add_i32 s30, s49, s31
	s_add_i32 s31, s49, s63
	v_mov_b32_e32 v15, s79
	s_add_i32 s63, s49, s70
	s_add_i32 s70, s49, s76
	s_add_i32 s19, s49, s19
	s_add_i32 s69, s49, s69
	s_add_i32 s53, s49, s53
	s_add_i32 s76, s49, s81
	s_add_i32 s79, s49, s88
	s_add_i32 s45, s49, s45
	v_mov_b32_e32 v19, s1
	v_mov_b32_e32 v20, s20
	v_mov_b32_e32 v24, s3
	v_mov_b32_e32 v25, s30
	v_mov_b32_e32 v26, s31
	v_mov_b32_e32 v27, s63
	v_mov_b32_e32 v28, s70
	v_mov_b32_e32 v29, s19
	v_mov_b32_e32 v30, s69
	v_mov_b32_e32 v31, s53
	v_mov_b32_e32 v32, s76
	v_mov_b32_e32 v33, s79
	v_mov_b32_e32 v17, s0
	v_mov_b32_e32 v40, s45
	ds_read_b32 v18, v13
	ds_read_b32 v21, v15
	ds_read_b32 v22, v17
	ds_read_b32 v19, v19
	ds_read_b32 v23, v20
	ds_read_b32 v24, v24
	ds_read_b32 v20, v25
	ds_read_b32 v25, v26
	ds_read_b32 v26, v27
	ds_read_b32 v28, v28
	ds_read_b32 v27, v29
	ds_read_b32 v29, v30
	ds_read_b32 v30, v31
	ds_read_b32 v32, v32
	ds_read_b32 v31, v33
	ds_read_b32 v33, v40
	s_add_i32 vcc_hi, vcc_hi, 2
	s_add_i32 s21, s21, s11
	s_add_i32 s10, s10, s12
	s_add_i32 s18, s18, s14
	s_add_i32 s4, s4, s15
	s_add_i32 s91, s91, s16
	s_add_i32 s13, s13, s17
	s_add_i32 vcc_lo, vcc_lo, s90
	s_add_i32 s42, s42, s5
	s_waitcnt vmcnt(0) lgkmcnt(0)
	v_pk_fma_f32 v[8:9], v[244:245], v[18:19], v[8:9] op_sel_hi:[0,1,1]
	v_pk_fma_f32 v[2:3], v[244:245], v[22:23], v[2:3] op_sel_hi:[0,1,1]
	v_pk_fma_f32 v[10:11], v[244:245], v[24:25], v[10:11] op_sel_hi:[0,1,1]
	v_pk_fma_f32 v[6:7], v[244:245], v[20:21], v[6:7] op_sel_hi:[0,1,1]
	v_pk_fma_f32 v[8:9], v[246:247], v[26:27], v[8:9] op_sel_hi:[0,1,1]
	v_pk_fma_f32 v[2:3], v[246:247], v[28:29], v[2:3] op_sel_hi:[0,1,1]
	v_pk_fma_f32 v[10:11], v[246:247], v[30:31], v[10:11] op_sel_hi:[0,1,1]
	v_pk_fma_f32 v[6:7], v[246:247], v[32:33], v[6:7] op_sel_hi:[0,1,1]
	s_mov_b32 s4, 0x3db504f3
	v_pk_mul_f32 v[2:3], v[2:3], s[4:5] op_sel_hi:[1,0]
	v_pk_mul_f32 v[6:7], v[6:7], s[4:5] op_sel_hi:[1,0]
	v_pk_mul_f32 v[4:5], v[8:9], s[4:5] op_sel_hi:[1,0]
	v_pk_mul_f32 v[8:9], v[10:11], s[4:5] op_sel_hi:[1,0]
	v_bfe_u32 v10, v7, 16, 1
	v_bfe_u32 v11, v6, 16, 1
	v_bfe_u32 v13, v3, 16, 1
	v_bfe_u32 v14, v2, 16, 1
	v_add3_u32 v2, v2, v14, s89
	v_add3_u32 v3, v3, v13, s89
	v_add3_u32 v6, v6, v11, s89
	v_add3_u32 v7, v7, v10, s89
	v_bfe_u32 v10, v4, 16, 1
	v_bfe_u32 v11, v5, 16, 1
	v_bfe_u32 v13, v8, 16, 1
	v_bfe_u32 v14, v9, 16, 1
	v_add3_u32 v9, v9, v14, s89
	v_add3_u32 v8, v8, v13, s89
	v_add3_u32 v5, v5, v11, s89
	v_add3_u32 v4, v4, v10, s89
	v_lshrrev_b32_e32 v10, 16, v4
	v_lshrrev_b32_e32 v11, 16, v5
	v_lshrrev_b32_e32 v4, 16, v8
	v_lshrrev_b32_e32 v5, 16, v9
	v_and_or_b32 v5, v7, s92, v5
	v_and_or_b32 v4, v6, s92, v4
	v_mov_b64_e32 v[6:7], s[38:39]
	s_movk_i32 s1, 0xc00
	v_readlane_b32 s0, v255, 21
	v_mad_u64_u32 v[6:7], s[4:5], v12, s1, v[6:7]
	s_and_b32 s42, s29, 0xfffffe00
	s_and_b32 s0, s0, 0x78
	v_lshl_add_u64 v[6:7], v[6:7], 0, s[42:43]
	s_lshl_b32 s42, s7, 8
	s_waitcnt lgkmcnt(0)
	v_lshl_add_u64 v[6:7], v[6:7], 0, s[42:43]
	s_lshl_b32 s42, s0, 1
	v_lshl_add_u64 v[6:7], v[6:7], 0, s[42:43]
	v_add_co_u32_e32 v6, vcc, 0x600000, v6
	v_readlane_b32 s30, v255, 19
	v_and_or_b32 v3, v3, s92, v11
	v_and_or_b32 v2, v2, s92, v10
	v_addc_co_u32_e32 v7, vcc, 0, v7, vcc
	v_readlane_b32 s31, v255, 20
	s_brev_b32 s44, 1
	v_readlane_b32 s45, v255, 18
	v_readlane_b32 s53, v255, 17
	v_readlane_b32 s63, v255, 16
	v_readlane_b32 s69, v255, 15
	v_readlane_b32 s70, v255, 14
	v_readlane_b32 s76, v255, 13
	s_mov_b32 s79, 0xfe5163ab
	s_mov_b32 s81, 0x3c439041
	s_mov_b32 s88, 0xdb629599
	s_mov_b32 s94, 0xf534ddc0
	s_mov_b32 s97, 0xfc2757d1
	global_store_dwordx4 v[6:7], v[2:5], off offset:1024
